# v18
# speedup vs baseline: 1.0890x; 1.0460x over previous
_Z15embed_ln_kernelPKiPKfS2_S2_S2_PfPDF16_7ConvJob:
	s_cmpk_lt_u32 s2, 0x200
	s_mov_b64 s[4:5], -1
	s_cbranch_scc0 .LBB2_2
	s_load_dwordx8 s[4:11], s[0:1], 0x0
	s_lshl_b32 s12, s2, 2
	v_lshrrev_b32_e32 v1, 6, v0
	v_mov_b32_e32 v3, 0
	v_or_b32_e32 v2, s12, v1
	s_waitcnt lgkmcnt(0)
	v_lshl_add_u64 v[4:5], v[2:3], 2, s[4:5]
	global_load_dword v8, v[4:5], off nt
	v_mov_b32_e32 v5, 0x3ff
	v_bitop3_b32 v1, s12, v5, v1 bitop3:0xc8
	v_lshlrev_b32_e32 v4, 2, v0
	v_mul_u32_u24_e32 v1, 0x300, v1
	v_and_b32_e32 v58, 0xfc, v4
	v_mov_b32_e32 v5, v3
	v_lshlrev_b32_e32 v4, 2, v1
	s_movk_i32 s3, 0xc00
	v_mov_b32_e32 v41, v3
	v_lshlrev_b32_e32 v40, 2, v58
	v_mov_b64_e32 v[6:7], s[6:7]
	v_lshl_add_u64 v[4:5], s[8:9], 0, v[4:5]
	v_lshl_add_u64 v[28:29], v[4:5], 0, v[40:41]
	v_mbcnt_lo_u32_b32 v1, -1, 0
	v_mbcnt_hi_u32_b32 v1, -1, v1
	s_movk_i32 s12, 0x600
	s_waitcnt vmcnt(0)
	v_mad_i64_i32 v[4:5], s[4:5], v8, s3, v[6:7]
	v_lshl_add_u64 v[30:31], v[4:5], 0, v[40:41]
	global_load_dwordx4 v[4:7], v[30:31], off
	global_load_dwordx4 v[8:11], v[28:29], off
	global_load_dwordx4 v[12:15], v[28:29], off offset:1024
	global_load_dwordx4 v[16:19], v[30:31], off offset:1024
	global_load_dwordx4 v[20:23], v[28:29], off offset:2048
	global_load_dwordx4 v[24:27], v[30:31], off offset:2048
	v_and_b32_e32 v28, 64, v1
	v_xor_b32_e32 v29, 32, v1
	v_add_u32_e32 v28, 64, v28
	v_cmp_lt_i32_e32 vcc, v29, v28
	s_load_dwordx4 s[4:7], s[0:1], 0x20
	s_load_dwordx2 s[8:9], s[0:1], 0x30
	v_cndmask_b32_e32 v29, v1, v29, vcc
	v_lshlrev_b32_e32 v29, 2, v29
	s_waitcnt lgkmcnt(0)
	v_mov_b64_e32 v[36:37], s[6:7]
	v_mov_b64_e32 v[38:39], s[8:9]
	s_waitcnt vmcnt(4)
	v_pk_add_f32 v[4:5], v[4:5], v[8:9]
	v_pk_add_f32 v[6:7], v[6:7], v[10:11]
	s_waitcnt vmcnt(2)
	v_pk_add_f32 v[8:9], v[16:17], v[12:13]
	v_pk_add_f32 v[10:11], v[18:19], v[14:15]
	s_waitcnt vmcnt(0)
	v_pk_add_f32 v[12:13], v[24:25], v[20:21]
	v_pk_add_f32 v[14:15], v[26:27], v[22:23]
	v_add_f32_e32 v24, v4, v5
	v_mov_b32_e32 v16, v8
	v_mov_b32_e32 v17, v12
	v_mov_b32_e32 v18, v9
	v_mov_b32_e32 v19, v13
	v_mov_b32_e32 v20, v10
	v_mov_b32_e32 v21, v14
	v_add_f32_e32 v24, v24, v6
	v_pk_add_f32 v[16:17], v[16:17], v[18:19]
	v_mov_b32_e32 v22, v11
	v_mov_b32_e32 v23, v15
	v_add_f32_e32 v18, v24, v7
	v_pk_add_f32 v[16:17], v[16:17], v[20:21]
	v_add_f32_e32 v18, 0, v18
	v_pk_add_f32 v[16:17], v[16:17], v[22:23]
	s_nop 0
	v_add_f32_e32 v16, v18, v16
	v_add_f32_e32 v16, v16, v17
	ds_bpermute_b32 v17, v29, v16
	v_xor_b32_e32 v18, 16, v1
	v_cmp_lt_i32_e32 vcc, v18, v28
	s_waitcnt lgkmcnt(0)
	v_add_f32_e32 v16, v16, v17
	v_cndmask_b32_e32 v18, v1, v18, vcc
	v_lshlrev_b32_e32 v30, 2, v18
	ds_bpermute_b32 v17, v30, v16
	v_xor_b32_e32 v18, 8, v1
	v_cmp_lt_i32_e32 vcc, v18, v28
	s_waitcnt lgkmcnt(0)
	v_add_f32_e32 v16, v16, v17
	v_cndmask_b32_e32 v18, v1, v18, vcc
	v_lshlrev_b32_e32 v31, 2, v18
	ds_bpermute_b32 v17, v31, v16
	v_xor_b32_e32 v18, 4, v1
	v_cmp_lt_i32_e32 vcc, v18, v28
	s_waitcnt lgkmcnt(0)
	v_add_f32_e32 v16, v16, v17
	v_cndmask_b32_e32 v18, v1, v18, vcc
	v_lshlrev_b32_e32 v54, 2, v18
	ds_bpermute_b32 v17, v54, v16
	v_xor_b32_e32 v18, 2, v1
	v_cmp_lt_i32_e32 vcc, v18, v28
	s_waitcnt lgkmcnt(0)
	v_add_f32_e32 v16, v16, v17
	v_cndmask_b32_e32 v18, v1, v18, vcc
	v_lshlrev_b32_e32 v59, 2, v18
	ds_bpermute_b32 v17, v59, v16
	v_xor_b32_e32 v18, 1, v1
	v_cmp_lt_i32_e32 vcc, v18, v28
	s_waitcnt lgkmcnt(0)
	v_add_f32_e32 v16, v16, v17
	v_cndmask_b32_e32 v1, v1, v18, vcc
	v_lshlrev_b32_e32 v1, 2, v1
	ds_bpermute_b32 v17, v1, v16
	s_waitcnt lgkmcnt(0)
	v_add_f32_e32 v16, v16, v17
	v_mul_f32_e32 v16, 0x3aaaaaab, v16
	v_pk_add_f32 v[42:43], v[4:5], v[16:17] op_sel_hi:[1,0] neg_lo:[0,1] neg_hi:[0,1]
	v_pk_add_f32 v[50:51], v[12:13], v[16:17] op_sel_hi:[1,0] neg_lo:[0,1] neg_hi:[0,1]
	v_pk_add_f32 v[46:47], v[8:9], v[16:17] op_sel_hi:[1,0] neg_lo:[0,1] neg_hi:[0,1]
	v_mov_b32_e32 v22, v51
	v_mov_b32_e32 v23, v43
	v_pk_add_f32 v[44:45], v[6:7], v[16:17] op_sel_hi:[1,0] neg_lo:[0,1] neg_hi:[0,1]
	v_pk_add_f32 v[48:49], v[10:11], v[16:17] op_sel_hi:[1,0] neg_lo:[0,1] neg_hi:[0,1]
	v_pk_add_f32 v[52:53], v[14:15], v[16:17] op_sel_hi:[1,0] neg_lo:[0,1] neg_hi:[0,1]
	v_pk_mul_f32 v[16:17], v[46:47], v[46:47]
	v_mov_b32_e32 v20, v50
	v_mov_b32_e32 v21, v42
	v_pk_mul_f32 v[22:23], v[22:23], v[22:23]
	v_pk_mul_f32 v[18:19], v[48:49], v[48:49]
	v_mov_b32_e32 v24, v52
	v_mov_b32_e32 v25, v44
	v_add_f32_e32 v28, v16, v17
	v_pk_fma_f32 v[16:17], v[20:21], v[20:21], v[22:23]
	v_mov_b32_e32 v26, v53
	v_mov_b32_e32 v27, v45
	v_add_f32_e32 v18, v18, v28
	v_pk_fma_f32 v[16:17], v[24:25], v[24:25], v[16:17]
	v_add_f32_e32 v18, v19, v18
	v_pk_fma_f32 v[16:17], v[26:27], v[26:27], v[16:17]
	s_nop 0
	v_add_f32_e32 v17, v17, v18
	v_add_f32_e32 v16, v16, v17
	ds_bpermute_b32 v17, v29, v16
	s_waitcnt lgkmcnt(0)
	v_add_f32_e32 v20, v16, v17
	ds_bpermute_b32 v21, v30, v20
	global_load_dwordx4 v[16:19], v40, s[10:11]
	s_waitcnt lgkmcnt(0)
	v_add_f32_e32 v55, v20, v21
	ds_bpermute_b32 v56, v31, v55
	global_load_dwordx4 v[20:23], v40, s[4:5]
	global_load_dwordx4 v[24:27], v40, s[4:5] offset:1024
	global_load_dwordx4 v[28:31], v40, s[10:11] offset:1024
	global_load_dwordx4 v[32:35], v40, s[10:11] offset:2048
	s_waitcnt lgkmcnt(0)
	v_add_f32_e32 v60, v55, v56
	ds_bpermute_b32 v61, v54, v60
	v_mad_u64_u32 v[54:55], s[6:7], v2, s3, v[36:37]
	v_mad_u64_u32 v[56:57], s[6:7], v2, s12, v[38:39]
	global_load_dwordx4 v[36:39], v40, s[4:5] offset:2048
	v_lshlrev_b32_e32 v2, 1, v58
	s_waitcnt lgkmcnt(0)
	v_add_f32_e32 v58, v60, v61
	ds_bpermute_b32 v59, v59, v58
	s_mov_b32 s3, 0x800000
	v_lshl_add_u64 v[40:41], v[54:55], 0, v[40:41]
	global_store_dwordx4 v[40:41], v[4:7], off sc1
	global_store_dwordx4 v[40:41], v[8:11], off offset:1024 sc1
	global_store_dwordx4 v[40:41], v[12:15], off offset:2048 sc1
	v_lshl_add_u64 v[2:3], v[56:57], 0, v[2:3]
	s_waitcnt lgkmcnt(0)
	v_add_f32_e32 v58, v58, v59
	ds_bpermute_b32 v1, v1, v58
	v_mov_b32_e32 v59, 0x3727c5ac
	s_mov_b64 s[4:5], 0
	s_waitcnt lgkmcnt(0)
	v_add_f32_e32 v1, v58, v1
	v_fmac_f32_e32 v59, 0x3aaaaaab, v1
	v_mul_f32_e32 v1, 0x4b800000, v59
	v_cmp_gt_f32_e32 vcc, s3, v59
	s_nop 1
	v_cndmask_b32_e32 v1, v59, v1, vcc
	v_rsq_f32_e32 v1, v1
	s_nop 0
	v_mul_f32_e32 v4, 0x45800000, v1
	v_cndmask_b32_e32 v4, v1, v4, vcc
	v_pk_mul_f32 v[6:7], v[42:43], v[4:5] op_sel_hi:[1,0]
	v_pk_mul_f32 v[8:9], v[44:45], v[4:5] op_sel_hi:[1,0]
	v_pk_mul_f32 v[10:11], v[46:47], v[4:5] op_sel_hi:[1,0]
	v_pk_mul_f32 v[12:13], v[48:49], v[4:5] op_sel_hi:[1,0]
	v_pk_mul_f32 v[14:15], v[50:51], v[4:5] op_sel_hi:[1,0]
	v_pk_mul_f32 v[4:5], v[52:53], v[4:5] op_sel_hi:[1,0]
	s_waitcnt vmcnt(7)
	v_pk_fma_f32 v[6:7], v[16:17], v[6:7], v[20:21]
	v_pk_fma_f32 v[8:9], v[18:19], v[8:9], v[22:23]
	s_waitcnt vmcnt(5)
	v_pk_fma_f32 v[10:11], v[28:29], v[10:11], v[24:25]
	v_pk_fma_f32 v[12:13], v[30:31], v[12:13], v[26:27]
	v_cvt_pk_f16_f32 v6, v6, v7
	v_cvt_pk_f16_f32 v7, v8, v9
	v_cvt_pk_f16_f32 v8, v10, v11
	v_cvt_pk_f16_f32 v9, v12, v13
	s_waitcnt vmcnt(3)
	v_pk_fma_f32 v[14:15], v[14:15], v[32:33], v[36:37]
	v_pk_fma_f32 v[4:5], v[4:5], v[34:35], v[38:39]
	v_cvt_pk_f16_f32 v10, v14, v15
	v_cvt_pk_f16_f32 v11, v4, v5
	global_store_dwordx2 v[2:3], v[6:7], off sc1
	global_store_dwordx2 v[2:3], v[8:9], off offset:512 sc1
	global_store_dwordx2 v[2:3], v[10:11], off offset:1024 sc1

.LBB2_6:
	s_load_dwordx16 s[8:23], s[0:1], 0x100
	v_mad_u32_u24 v35, v37, s46, v2
	v_lshl_add_u32 v34, v4, 1, v1
	v_lshl_add_u32 v33, v5, 1, v1
	v_lshl_add_u32 v32, v6, 1, v1
	s_andn2_b64 vcc, exec, s[44:45]
	v_lshl_add_u32 v31, v3, 1, v1
	s_cbranch_vccnz .LBB2_30
	s_load_dwordx4 s[44:47], s[0:1], 0x48
	s_load_dwordx4 s[48:51], s[60:61], 0x0
	s_add_i32 s60, s7, s33
	s_abs_i32 s7, s60
	s_waitcnt lgkmcnt(0)
	s_abs_i32 s6, s47
	v_cvt_f32_u32_e32 v1, s6
	s_sub_i32 s62, 0, s6
	s_xor_b32 s61, s60, s47
	s_ashr_i32 s61, s61, 31
	v_rcp_iflag_f32_e32 v1, v1
	s_nop 0
	v_mul_f32_e32 v1, 0x4f7ffffe, v1
	v_cvt_u32_f32_e32 v1, v1
	s_nop 0
	v_readfirstlane_b32 s63, v1
	s_mul_i32 s62, s62, s63
	s_mul_hi_u32 s62, s63, s62
	s_add_i32 s63, s63, s62
	s_mul_hi_u32 s62, s7, s63
	s_mul_i32 s63, s62, s6
	s_sub_i32 s7, s7, s63
	s_add_i32 s64, s62, 1
	s_sub_i32 s63, s7, s6
	s_cmp_ge_u32 s7, s6
	s_cselect_b32 s62, s64, s62
	s_cselect_b32 s7, s63, s7
	s_add_i32 s63, s62, 1
	s_cmp_ge_u32 s7, s6
	s_cselect_b32 s6, s63, s62
	s_abs_i32 s62, s46
	v_cvt_f32_u32_e32 v1, s62
	s_xor_b32 s6, s6, s61
	s_sub_i32 s63, 0, s62
	s_sub_i32 s7, s6, s61
	v_rcp_iflag_f32_e32 v1, v1
	s_mul_i32 s6, s7, s47
	s_sub_i32 s6, s60, s6
	s_abs_i32 s61, s6
	v_mul_f32_e32 v1, 0x4f7ffffe, v1
	v_cvt_u32_f32_e32 v1, v1
	s_xor_b32 s60, s6, s46
	s_ashr_i32 s60, s60, 31
	s_mul_hi_i32 s47, s7, s44
	v_readfirstlane_b32 s64, v1
	s_mul_i32 s63, s63, s64
	s_mul_hi_u32 s63, s64, s63
	s_add_i32 s64, s64, s63
	s_mul_hi_u32 s63, s61, s64
	s_mul_i32 s64, s63, s62
	s_sub_i32 s61, s61, s64
	s_add_i32 s65, s63, 1
	s_sub_i32 s64, s61, s62
	s_cmp_ge_u32 s61, s62
	s_cselect_b32 s63, s65, s63
	s_cselect_b32 s61, s64, s61
	s_add_i32 s64, s63, 1
	s_cmp_ge_u32 s61, s62
	s_cselect_b32 s61, s64, s63
	s_xor_b32 s61, s61, s60
	s_sub_i32 s61, s61, s60
	s_mul_i32 s60, s61, s46
	s_sub_i32 s6, s6, s60
	s_mul_i32 s7, s7, s44
	s_ashr_i32 s66, s45, 31
	s_lshl_b32 s60, s6, 6
	s_lshl_b32 s6, s61, 7
	s_and_saveexec_b64 s[62:63], s[4:5]
	s_cbranch_execz .LBB2_11
	v_or_b32_e32 v2, s60, v37
	v_cmp_gt_i32_e32 vcc, s45, v2
	v_mov_b32_e32 v1, 0
	v_mov_b32_e32 v3, 0
	v_mov_b32_e32 v4, 0
	v_mov_b32_e32 v5, 0
	v_mov_b32_e32 v6, 0
	v_mov_b32_e32 v7, 0
	v_mov_b32_e32 v8, 0
	v_mov_b32_e32 v9, 0
	v_mov_b32_e32 v10, 0
	v_mov_b32_e32 v11, 0
	v_mov_b32_e32 v12, 0
	v_mov_b32_e32 v13, 0
	v_mov_b32_e32 v14, 0
	v_mov_b32_e32 v15, 0
	v_mov_b32_e32 v16, 0
	v_mov_b32_e32 v17, 0
	v_mov_b32_e32 v18, 0
	v_mov_b32_e32 v19, 0
	v_mov_b32_e32 v20, 0
	v_mov_b32_e32 v21, 0
	v_mov_b32_e32 v23, 0
	v_mov_b32_e32 v24, 0
	v_mov_b32_e32 v25, 0
	v_mov_b32_e32 v26, 0
	v_mov_b32_e32 v27, 0
	v_mov_b32_e32 v39, 0
	v_mov_b32_e32 v40, 0
	v_mov_b32_e32 v41, 0
	v_mov_b32_e32 v42, 0
	v_mov_b32_e32 v43, 0
	v_mov_b32_e32 v44, 0
	v_mov_b32_e32 v45, 0
	s_and_saveexec_b64 s[64:65], vcc
	s_cbranch_execz .LBB2_10
	s_mul_i32 s66, s7, s66
	s_mul_hi_u32 s67, s7, s45
	s_add_i32 s66, s67, s66
	s_mul_i32 s67, s47, s45
	s_add_i32 s67, s66, s67
	s_mul_i32 s66, s7, s45
	s_lshl_b64 s[66:67], s[66:67], 2
	s_add_u32 s48, s48, s66
	v_or_b32_e32 v39, s6, v36
	s_addc_u32 s49, s49, s67
	v_ashrrev_i32_e32 v3, 31, v2
	v_or_b32_e32 v1, 1, v39
	v_lshl_add_u64 v[40:41], v[2:3], 2, s[48:49]
	v_mad_i64_i32 v[4:5], s[48:49], v1, s45, 0
	v_or_b32_e32 v1, 2, v39
	v_mad_i64_i32 v[6:7], s[48:49], v1, s45, 0
	v_or_b32_e32 v1, 3, v39
	v_mad_i64_i32 v[8:9], s[48:49], v1, s45, 0
	v_or_b32_e32 v1, 4, v39
	v_mad_i64_i32 v[10:11], s[48:49], v1, s45, 0
	v_or_b32_e32 v1, 5, v39
	v_mad_i64_i32 v[12:13], s[48:49], v1, s45, 0
	v_or_b32_e32 v1, 6, v39
	v_mad_i64_i32 v[2:3], s[48:49], v39, s45, 0
	v_mad_i64_i32 v[14:15], s[48:49], v1, s45, 0
	v_or_b32_e32 v1, 7, v39
	v_lshl_add_u64 v[2:3], v[2:3], 2, v[40:41]
	v_lshl_add_u64 v[4:5], v[4:5], 2, v[40:41]
	v_lshl_add_u64 v[6:7], v[6:7], 2, v[40:41]
	v_lshl_add_u64 v[8:9], v[8:9], 2, v[40:41]
	v_mad_i64_i32 v[16:17], s[48:49], v1, s45, 0
	v_lshl_add_u64 v[10:11], v[10:11], 2, v[40:41]
	v_lshl_add_u64 v[12:13], v[12:13], 2, v[40:41]
	v_lshl_add_u64 v[14:15], v[14:15], 2, v[40:41]
	v_lshl_add_u64 v[16:17], v[16:17], 2, v[40:41]
	global_load_dword v1, v[2:3], off nt
	s_nop 0
	global_load_dword v3, v[4:5], off nt
	s_nop 0
	global_load_dword v4, v[6:7], off nt
	global_load_dword v5, v[8:9], off nt
	s_nop 0
	global_load_dword v6, v[10:11], off nt
	global_load_dword v7, v[12:13], off nt
	global_load_dword v8, v[14:15], off nt
	global_load_dword v9, v[16:17], off nt
	v_or_b32_e32 v2, 8, v39
	v_mad_i64_i32 v[10:11], s[48:49], v2, s45, 0
	v_or_b32_e32 v2, 9, v39
	v_mad_i64_i32 v[12:13], s[48:49], v2, s45, 0
	v_or_b32_e32 v2, 10, v39
	v_mad_i64_i32 v[14:15], s[48:49], v2, s45, 0
	v_or_b32_e32 v2, 11, v39
	v_mad_i64_i32 v[16:17], s[48:49], v2, s45, 0
	v_or_b32_e32 v2, 12, v39
	v_mad_i64_i32 v[18:19], s[48:49], v2, s45, 0
	v_or_b32_e32 v2, 13, v39
	v_mad_i64_i32 v[20:21], s[48:49], v2, s45, 0
	v_or_b32_e32 v2, 14, v39
	v_mad_i64_i32 v[24:25], s[48:49], v2, s45, 0
	v_or_b32_e32 v2, 15, v39
	v_lshl_add_u64 v[10:11], v[10:11], 2, v[40:41]
	v_lshl_add_u64 v[12:13], v[12:13], 2, v[40:41]
	v_lshl_add_u64 v[14:15], v[14:15], 2, v[40:41]
	v_lshl_add_u64 v[16:17], v[16:17], 2, v[40:41]
	v_lshl_add_u64 v[18:19], v[18:19], 2, v[40:41]
	v_mad_i64_i32 v[26:27], s[48:49], v2, s45, 0
	v_or_b32_e32 v2, 16, v39
	v_lshl_add_u64 v[20:21], v[20:21], 2, v[40:41]
	v_lshl_add_u64 v[24:25], v[24:25], 2, v[40:41]
	v_lshl_add_u64 v[26:27], v[26:27], 2, v[40:41]
	global_load_dword v10, v[10:11], off nt
	s_nop 0
	global_load_dword v11, v[12:13], off nt
	s_nop 0
	global_load_dword v12, v[14:15], off nt
	global_load_dword v13, v[16:17], off nt
	s_nop 0
	global_load_dword v14, v[18:19], off nt
	global_load_dword v15, v[20:21], off nt
	global_load_dword v16, v[24:25], off nt
	global_load_dword v17, v[26:27], off nt
	v_mad_i64_i32 v[18:19], s[48:49], v2, s45, 0
	v_or_b32_e32 v2, 17, v39
	v_mad_i64_i32 v[20:21], s[48:49], v2, s45, 0
	v_or_b32_e32 v2, 18, v39
	v_mad_i64_i32 v[24:25], s[48:49], v2, s45, 0
	v_or_b32_e32 v2, 19, v39
	v_mad_i64_i32 v[26:27], s[48:49], v2, s45, 0
	v_or_b32_e32 v2, 20, v39
	v_mad_i64_i32 v[42:43], s[48:49], v2, s45, 0
	v_or_b32_e32 v2, 21, v39
	v_mad_i64_i32 v[44:45], s[48:49], v2, s45, 0
	v_or_b32_e32 v2, 22, v39
	v_mad_i64_i32 v[46:47], s[48:49], v2, s45, 0
	v_or_b32_e32 v2, 23, v39
	v_lshl_add_u64 v[18:19], v[18:19], 2, v[40:41]
	v_lshl_add_u64 v[20:21], v[20:21], 2, v[40:41]
	v_lshl_add_u64 v[24:25], v[24:25], 2, v[40:41]
	v_lshl_add_u64 v[26:27], v[26:27], 2, v[40:41]
	v_lshl_add_u64 v[42:43], v[42:43], 2, v[40:41]
	v_mad_i64_i32 v[48:49], s[48:49], v2, s45, 0
	v_or_b32_e32 v2, 24, v39
	v_lshl_add_u64 v[44:45], v[44:45], 2, v[40:41]
	v_lshl_add_u64 v[46:47], v[46:47], 2, v[40:41]
	v_lshl_add_u64 v[48:49], v[48:49], 2, v[40:41]
	global_load_dword v18, v[18:19], off nt
	s_nop 0
	global_load_dword v19, v[20:21], off nt
	s_nop 0
	global_load_dword v20, v[24:25], off nt
	global_load_dword v21, v[26:27], off nt
	global_load_dword v23, v[42:43], off nt
	s_nop 0
	global_load_dword v24, v[44:45], off nt
	global_load_dword v25, v[46:47], off nt
	global_load_dword v26, v[48:49], off nt
	v_mad_i64_i32 v[42:43], s[48:49], v2, s45, 0
	v_or_b32_e32 v2, 25, v39
	v_mad_i64_i32 v[44:45], s[48:49], v2, s45, 0
	v_or_b32_e32 v2, 26, v39
	v_mad_i64_i32 v[46:47], s[48:49], v2, s45, 0
	v_or_b32_e32 v2, 27, v39
	v_mad_i64_i32 v[48:49], s[48:49], v2, s45, 0
	v_or_b32_e32 v2, 28, v39
	v_mad_i64_i32 v[50:51], s[48:49], v2, s45, 0
	v_or_b32_e32 v2, 29, v39
	v_mad_i64_i32 v[52:53], s[48:49], v2, s45, 0
	v_or_b32_e32 v2, 30, v39
	v_mad_i64_i32 v[54:55], s[48:49], v2, s45, 0
	v_or_b32_e32 v2, 31, v39
	v_lshl_add_u64 v[42:43], v[42:43], 2, v[40:41]
	v_lshl_add_u64 v[44:45], v[44:45], 2, v[40:41]
	v_mad_i64_i32 v[56:57], s[48:49], v2, s45, 0
	v_lshl_add_u64 v[46:47], v[46:47], 2, v[40:41]
	v_lshl_add_u64 v[48:49], v[48:49], 2, v[40:41]
	v_lshl_add_u64 v[50:51], v[50:51], 2, v[40:41]
	v_lshl_add_u64 v[52:53], v[52:53], 2, v[40:41]
	v_lshl_add_u64 v[54:55], v[54:55], 2, v[40:41]
	v_lshl_add_u64 v[56:57], v[56:57], 2, v[40:41]
	global_load_dword v27, v[42:43], off nt
	global_load_dword v39, v[44:45], off nt
	global_load_dword v40, v[46:47], off nt
	global_load_dword v41, v[48:49], off nt
	s_nop 0
	global_load_dword v42, v[50:51], off nt
	global_load_dword v43, v[52:53], off nt
	global_load_dword v44, v[54:55], off nt
	global_load_dword v45, v[56:57], off nt

.LBB2_14:
.LBB2_15:
	s_ashr_i32 s16, s46, 31
	s_mul_i32 s17, s46, s47
	s_mul_hi_u32 s18, s46, s7
	s_add_i32 s17, s18, s17
	s_mul_i32 s16, s16, s7
	s_add_i32 s17, s17, s16
	s_mul_i32 s16, s46, s7
	s_lshl_b64 s[16:17], s[16:17], 7
	s_add_u32 s46, s50, s16
	s_addc_u32 s47, s51, s17
	s_mul_hi_i32 s17, s61, s45
	s_mul_i32 s16, s61, s45
	s_lshl_b64 s[18:19], s[16:17], 2
	s_add_u32 s16, s20, s18
	s_addc_u32 s17, s21, s19
	s_add_u32 s18, s22, s18
	s_addc_u32 s19, s23, s19
	s_ashr_i32 s7, s6, 31
	s_lshl_b64 s[6:7], s[6:7], 1
	s_add_u32 s6, s46, s6
	s_addc_u32 s7, s47, s7
	v_lshlrev_b32_e32 v18, 1, v38
	v_mov_b32_e32 v19, 0
	v_lshl_add_u64 v[24:25], s[6:7], 0, v[18:19]
	ds_read_b128 v[18:21], v34
	v_or_b32_e32 v26, s60, v22
	v_mad_i64_i32 v[40:41], s[6:7], v26, s44, 0
	v_cndmask_b32_e64 v1, 0, 1, s[62:63]
	v_lshl_add_u64 v[40:41], v[40:41], 1, v[24:25]
	v_cmp_ne_u32_e64 s[6:7], 1, v1
	s_andn2_b64 vcc, exec, s[62:63]
	s_waitcnt lgkmcnt(0)
	global_store_dwordx4 v[40:41], v[18:21], off sc1
	s_cbranch_vccnz .LBB2_54
	s_waitcnt vmcnt(3)
	v_fma_mix_f32 v1, v6, v18, 0 op_sel_hi:[0,1,0]
	v_fma_mix_f32 v1, v7, v18, v1 op_sel:[0,1,0] op_sel_hi:[0,1,0]
	v_fma_mix_f32 v1, v8, v19, v1 op_sel_hi:[0,1,0]
	s_waitcnt vmcnt(1)
	v_fma_mix_f32 v23, v14, v18, 0 op_sel_hi:[0,1,0]
	v_fma_mix_f32 v1, v9, v19, v1 op_sel:[0,1,0] op_sel_hi:[0,1,0]
	v_fma_mix_f32 v18, v15, v18, v23 op_sel:[0,1,0] op_sel_hi:[0,1,0]
	v_fma_mix_f32 v1, v2, v20, v1 op_sel_hi:[0,1,0]
	v_fma_mix_f32 v18, v16, v19, v18 op_sel_hi:[0,1,0]
	v_fma_mix_f32 v1, v3, v20, v1 op_sel:[0,1,0] op_sel_hi:[0,1,0]
	v_fma_mix_f32 v18, v17, v19, v18 op_sel:[0,1,0] op_sel_hi:[0,1,0]
	v_fma_mix_f32 v1, v4, v21, v1 op_sel_hi:[0,1,0]
	v_fma_mix_f32 v18, v10, v20, v18 op_sel_hi:[0,1,0]
	v_fma_mix_f32 v19, v5, v21, v1 op_sel:[0,1,0] op_sel_hi:[0,1,0]
	v_mbcnt_lo_u32_b32 v1, -1, 0
	v_fma_mix_f32 v18, v11, v20, v18 op_sel:[0,1,0] op_sel_hi:[0,1,0]
	v_mbcnt_hi_u32_b32 v20, -1, v1
	v_and_b32_e32 v1, 64, v20
	v_add_u32_e32 v27, 64, v1
	v_xor_b32_e32 v1, 1, v20
	v_cmp_lt_i32_e32 vcc, v1, v27
	v_fma_mix_f32 v18, v12, v21, v18 op_sel_hi:[0,1,0]
	v_fma_mix_f32 v18, v13, v21, v18 op_sel:[0,1,0] op_sel_hi:[0,1,0]
	v_cndmask_b32_e32 v1, v20, v1, vcc
	v_lshlrev_b32_e32 v1, 2, v1
	ds_bpermute_b32 v21, v1, v19
	ds_bpermute_b32 v23, v1, v18
	s_waitcnt lgkmcnt(1)
	v_add_f32_e32 v19, v19, v21
	s_waitcnt lgkmcnt(0)
	v_add_f32_e32 v21, v18, v23
	v_xor_b32_e32 v18, 2, v20
	v_cmp_lt_i32_e32 vcc, v18, v27
	s_nop 1
	v_cndmask_b32_e32 v18, v20, v18, vcc
	v_lshlrev_b32_e32 v18, 2, v18
	ds_bpermute_b32 v23, v18, v19
	ds_bpermute_b32 v39, v18, v21
	s_waitcnt lgkmcnt(1)
	v_add_f32_e32 v23, v19, v23
	v_xor_b32_e32 v19, 4, v20
	v_cmp_lt_i32_e32 vcc, v19, v27
	s_waitcnt lgkmcnt(0)
	v_add_f32_e32 v39, v21, v39
	v_cndmask_b32_e32 v19, v20, v19, vcc
	v_lshlrev_b32_e32 v19, 2, v19
	ds_bpermute_b32 v21, v19, v23
	ds_bpermute_b32 v40, v19, v39
	s_waitcnt lgkmcnt(1)
	v_add_f32_e32 v21, v23, v21
	s_waitcnt lgkmcnt(0)
	v_add_f32_e32 v23, v39, v40
	v_xor_b32_e32 v39, 8, v20
	v_cmp_lt_i32_e32 vcc, v39, v27
	v_ashrrev_i32_e32 v27, 31, v26
	s_nop 0
	v_cndmask_b32_e32 v20, v20, v39, vcc
	v_lshlrev_b32_e32 v20, 2, v20
	ds_bpermute_b32 v39, v20, v21
	ds_bpermute_b32 v40, v20, v23
	v_cmp_gt_i32_e32 vcc, s45, v26
	s_and_b64 s[22:23], s[2:3], vcc
	s_and_saveexec_b64 s[20:21], s[22:23]
	s_cbranch_execz .LBB2_18
	v_lshlrev_b64 v[26:27], 2, v[26:27]
	s_waitcnt lgkmcnt(0)
	v_add_f32_e32 v23, v23, v40
	v_add_f32_e32 v21, v21, v39
	v_lshl_add_u64 v[40:41], s[18:19], 0, v[26:27]
	v_lshl_add_u64 v[26:27], s[16:17], 0, v[26:27]
	global_store_dword v[26:27], v21, off sc1
	global_store_dword v[40:41], v23, off sc1
.LBB2_18:
	s_or_b64 exec, exec, s[20:21]
	s_waitcnt lgkmcnt(0)
	ds_read_b128 v[40:43], v33
	s_waitcnt lgkmcnt(0)
	v_fma_mix_f32 v21, v6, v40, 0 op_sel_hi:[0,1,0]
	v_fma_mix_f32 v23, v14, v40, 0 op_sel_hi:[0,1,0]
	v_fma_mix_f32 v21, v7, v40, v21 op_sel:[0,1,0] op_sel_hi:[0,1,0]
	v_fma_mix_f32 v23, v15, v40, v23 op_sel:[0,1,0] op_sel_hi:[0,1,0]
	v_fma_mix_f32 v21, v8, v41, v21 op_sel_hi:[0,1,0]
	v_fma_mix_f32 v23, v16, v41, v23 op_sel_hi:[0,1,0]
	v_fma_mix_f32 v21, v9, v41, v21 op_sel:[0,1,0] op_sel_hi:[0,1,0]
	v_fma_mix_f32 v23, v17, v41, v23 op_sel:[0,1,0] op_sel_hi:[0,1,0]
	v_fma_mix_f32 v21, v2, v42, v21 op_sel_hi:[0,1,0]
	v_fma_mix_f32 v23, v10, v42, v23 op_sel_hi:[0,1,0]
	v_fma_mix_f32 v21, v3, v42, v21 op_sel:[0,1,0] op_sel_hi:[0,1,0]
	v_fma_mix_f32 v23, v11, v42, v23 op_sel:[0,1,0] op_sel_hi:[0,1,0]
	v_fma_mix_f32 v21, v4, v43, v21 op_sel_hi:[0,1,0]
	v_fma_mix_f32 v23, v12, v43, v23 op_sel_hi:[0,1,0]
	v_fma_mix_f32 v21, v5, v43, v21 op_sel:[0,1,0] op_sel_hi:[0,1,0]
	v_fma_mix_f32 v23, v13, v43, v23 op_sel:[0,1,0] op_sel_hi:[0,1,0]
	ds_bpermute_b32 v26, v1, v21
	ds_bpermute_b32 v1, v1, v23
	s_waitcnt lgkmcnt(1)
	v_add_f32_e32 v21, v21, v26
	s_waitcnt lgkmcnt(0)
	v_add_f32_e32 v1, v23, v1
	ds_bpermute_b32 v23, v18, v21
	ds_bpermute_b32 v18, v18, v1
	s_waitcnt lgkmcnt(1)
	v_add_f32_e32 v21, v21, v23
	s_waitcnt lgkmcnt(0)
	v_add_f32_e32 v18, v1, v18
	ds_bpermute_b32 v1, v19, v21
	ds_bpermute_b32 v19, v19, v18
	v_or_b32_e32 v23, s60, v30
	v_mad_i64_i32 v[26:27], s[20:21], v23, s44, 0
	s_waitcnt lgkmcnt(1)
	v_add_f32_e32 v1, v21, v1
	s_waitcnt lgkmcnt(0)
	v_add_f32_e32 v18, v18, v19
	ds_bpermute_b32 v19, v20, v1
	ds_bpermute_b32 v20, v20, v18
	v_cmp_gt_i32_e32 vcc, s45, v23
	v_lshl_add_u64 v[26:27], v[26:27], 1, v[24:25]
	s_and_b64 s[22:23], s[2:3], vcc
	global_store_dwordx4 v[26:27], v[40:43], off sc1
	s_and_saveexec_b64 s[20:21], s[22:23]
	s_cbranch_execz .LBB2_20
	s_ashr_i32 s61, s60, 31
	v_mov_b32_e32 v23, 0
	s_waitcnt lgkmcnt(0)
	v_add_f32_e32 v26, v18, v20
	v_add_f32_e32 v1, v1, v19
	v_lshl_add_u64 v[18:19], s[60:61], 0, v[22:23]
	v_lshlrev_b64 v[18:19], 2, v[18:19]
	v_lshl_add_u64 v[20:21], s[18:19], 0, v[18:19]
	v_lshl_add_u64 v[18:19], s[16:17], 0, v[18:19]
	global_store_dword v[18:19], v1, off offset:64 sc1
	global_store_dword v[20:21], v26, off offset:64 sc1

.LBB2_21:
	s_waitcnt lgkmcnt(0)
	ds_read_b128 v[18:21], v33
	v_or_b32_e32 v1, s60, v30
	v_mad_i64_i32 v[26:27], s[20:21], v1, s44, 0
	v_lshl_add_u64 v[26:27], v[26:27], 1, v[24:25]
	s_waitcnt lgkmcnt(0)
	global_store_dwordx4 v[26:27], v[18:21], off sc1
.LBB2_22:
	s_waitcnt lgkmcnt(0)
	ds_read_b128 v[18:21], v32
	v_or_b32_e32 v23, s60, v29
	v_mad_i64_i32 v[26:27], s[20:21], v23, s44, 0
	v_lshl_add_u64 v[26:27], v[26:27], 1, v[24:25]
	s_and_b64 vcc, exec, s[6:7]
	s_waitcnt lgkmcnt(0)
	global_store_dwordx4 v[26:27], v[18:21], off sc1
	s_cbranch_vccnz .LBB2_55
	s_waitcnt vmcnt(4)
	v_fma_mix_f32 v1, v6, v18, 0 op_sel_hi:[0,1,0]
	v_fma_mix_f32 v1, v7, v18, v1 op_sel:[0,1,0] op_sel_hi:[0,1,0]
	v_fma_mix_f32 v1, v8, v19, v1 op_sel_hi:[0,1,0]
	s_waitcnt vmcnt(2)
	v_fma_mix_f32 v26, v14, v18, 0 op_sel_hi:[0,1,0]
	v_fma_mix_f32 v1, v9, v19, v1 op_sel:[0,1,0] op_sel_hi:[0,1,0]
	v_fma_mix_f32 v18, v15, v18, v26 op_sel:[0,1,0] op_sel_hi:[0,1,0]
	v_fma_mix_f32 v1, v2, v20, v1 op_sel_hi:[0,1,0]
	v_fma_mix_f32 v18, v16, v19, v18 op_sel_hi:[0,1,0]
	v_fma_mix_f32 v1, v3, v20, v1 op_sel:[0,1,0] op_sel_hi:[0,1,0]
	v_fma_mix_f32 v18, v17, v19, v18 op_sel:[0,1,0] op_sel_hi:[0,1,0]
	v_fma_mix_f32 v1, v4, v21, v1 op_sel_hi:[0,1,0]
	v_fma_mix_f32 v18, v10, v20, v18 op_sel_hi:[0,1,0]
	v_fma_mix_f32 v19, v5, v21, v1 op_sel:[0,1,0] op_sel_hi:[0,1,0]
	v_mbcnt_lo_u32_b32 v1, -1, 0
	v_fma_mix_f32 v18, v11, v20, v18 op_sel:[0,1,0] op_sel_hi:[0,1,0]
	v_mbcnt_hi_u32_b32 v20, -1, v1
	v_and_b32_e32 v1, 64, v20
	v_add_u32_e32 v27, 64, v1
	v_xor_b32_e32 v1, 1, v20
	v_cmp_lt_i32_e32 vcc, v1, v27
	v_fma_mix_f32 v18, v12, v21, v18 op_sel_hi:[0,1,0]
	v_fma_mix_f32 v18, v13, v21, v18 op_sel:[0,1,0] op_sel_hi:[0,1,0]
	v_cndmask_b32_e32 v1, v20, v1, vcc
	v_lshlrev_b32_e32 v1, 2, v1
	ds_bpermute_b32 v21, v1, v19
	ds_bpermute_b32 v26, v1, v18
	s_waitcnt lgkmcnt(1)
	v_add_f32_e32 v19, v19, v21
	s_waitcnt lgkmcnt(0)
	v_add_f32_e32 v21, v18, v26
	v_xor_b32_e32 v18, 2, v20
	v_cmp_lt_i32_e32 vcc, v18, v27
	s_nop 1
	v_cndmask_b32_e32 v18, v20, v18, vcc
	v_lshlrev_b32_e32 v18, 2, v18
	ds_bpermute_b32 v26, v18, v19
	ds_bpermute_b32 v39, v18, v21
	s_waitcnt lgkmcnt(1)
	v_add_f32_e32 v26, v19, v26
	v_xor_b32_e32 v19, 4, v20
	v_cmp_lt_i32_e32 vcc, v19, v27
	s_waitcnt lgkmcnt(0)
	v_add_f32_e32 v39, v21, v39
	v_cndmask_b32_e32 v19, v20, v19, vcc
	v_lshlrev_b32_e32 v19, 2, v19
	ds_bpermute_b32 v21, v19, v26
	ds_bpermute_b32 v40, v19, v39
	s_waitcnt lgkmcnt(1)
	v_add_f32_e32 v21, v26, v21
	s_waitcnt lgkmcnt(0)
	v_add_f32_e32 v26, v39, v40
	v_xor_b32_e32 v39, 8, v20
	v_cmp_lt_i32_e32 vcc, v39, v27
	s_nop 1
	v_cndmask_b32_e32 v20, v20, v39, vcc
	v_lshlrev_b32_e32 v20, 2, v20
	ds_bpermute_b32 v27, v20, v21
	ds_bpermute_b32 v39, v20, v26
	v_cmp_gt_i32_e32 vcc, s45, v23
	s_and_b64 s[20:21], s[2:3], vcc
	s_and_saveexec_b64 s[6:7], s[20:21]
	s_cbranch_execz .LBB2_25
	s_ashr_i32 s61, s60, 31
	v_mov_b32_e32 v23, 0
	s_waitcnt lgkmcnt(0)
	v_add_f32_e32 v39, v26, v39
	v_add_f32_e32 v21, v21, v27
	v_lshl_add_u64 v[26:27], s[60:61], 0, v[22:23]
	v_lshlrev_b64 v[26:27], 2, v[26:27]
	v_lshl_add_u64 v[40:41], s[18:19], 0, v[26:27]
	v_lshl_add_u64 v[26:27], s[16:17], 0, v[26:27]
	global_store_dword v[26:27], v21, off offset:128 sc1
	global_store_dword v[40:41], v39, off offset:128 sc1
.LBB2_25:
	s_or_b64 exec, exec, s[6:7]
	ds_read_b128 v[40:43], v31
	s_waitcnt lgkmcnt(0)
	v_fma_mix_f32 v6, v6, v40, 0 op_sel_hi:[0,1,0]
	v_fma_mix_f32 v14, v14, v40, 0 op_sel_hi:[0,1,0]
	v_fma_mix_f32 v6, v7, v40, v6 op_sel:[0,1,0] op_sel_hi:[0,1,0]
	v_fma_mix_f32 v7, v15, v40, v14 op_sel:[0,1,0] op_sel_hi:[0,1,0]
	v_fma_mix_f32 v6, v8, v41, v6 op_sel_hi:[0,1,0]
	v_fma_mix_f32 v7, v16, v41, v7 op_sel_hi:[0,1,0]
	v_fma_mix_f32 v6, v9, v41, v6 op_sel:[0,1,0] op_sel_hi:[0,1,0]
	v_fma_mix_f32 v7, v17, v41, v7 op_sel:[0,1,0] op_sel_hi:[0,1,0]
	v_fma_mix_f32 v2, v2, v42, v6 op_sel_hi:[0,1,0]
	v_fma_mix_f32 v6, v10, v42, v7 op_sel_hi:[0,1,0]
	v_fma_mix_f32 v2, v3, v42, v2 op_sel:[0,1,0] op_sel_hi:[0,1,0]
	v_fma_mix_f32 v3, v11, v42, v6 op_sel:[0,1,0] op_sel_hi:[0,1,0]
	v_fma_mix_f32 v2, v4, v43, v2 op_sel_hi:[0,1,0]
	v_fma_mix_f32 v3, v12, v43, v3 op_sel_hi:[0,1,0]
	v_fma_mix_f32 v2, v5, v43, v2 op_sel:[0,1,0] op_sel_hi:[0,1,0]
	v_fma_mix_f32 v3, v13, v43, v3 op_sel:[0,1,0] op_sel_hi:[0,1,0]
	ds_bpermute_b32 v4, v1, v2
	ds_bpermute_b32 v1, v1, v3
	v_or_b32_e32 v5, s60, v28
	v_mad_i64_i32 v[6:7], s[6:7], v5, s44, 0
	s_waitcnt lgkmcnt(1)
	v_add_f32_e32 v2, v2, v4
	s_waitcnt lgkmcnt(0)
	v_add_f32_e32 v1, v3, v1
	ds_bpermute_b32 v3, v18, v2
	ds_bpermute_b32 v4, v18, v1
	v_cmp_gt_i32_e32 vcc, s45, v5
	v_lshl_add_u64 v[6:7], v[6:7], 1, v[24:25]
	s_and_b64 s[20:21], s[2:3], vcc
	s_waitcnt lgkmcnt(1)
	v_add_f32_e32 v2, v2, v3
	s_waitcnt lgkmcnt(0)
	v_add_f32_e32 v3, v1, v4
	ds_bpermute_b32 v1, v19, v2
	ds_bpermute_b32 v4, v19, v3
	global_store_dwordx4 v[6:7], v[40:43], off sc1
	s_waitcnt lgkmcnt(1)
	v_add_f32_e32 v1, v2, v1
	s_waitcnt lgkmcnt(0)
	v_add_f32_e32 v2, v3, v4
	ds_bpermute_b32 v3, v20, v1
	ds_bpermute_b32 v4, v20, v2
	s_and_saveexec_b64 s[6:7], s[20:21]
	s_cbranch_execz .LBB2_27
	s_ashr_i32 s61, s60, 31
	v_mov_b32_e32 v23, 0
	s_waitcnt lgkmcnt(0)
	v_add_f32_e32 v6, v2, v4
	v_add_f32_e32 v1, v1, v3
	v_lshl_add_u64 v[2:3], s[60:61], 0, v[22:23]
	v_lshlrev_b64 v[2:3], 2, v[2:3]
	v_lshl_add_u64 v[4:5], s[18:19], 0, v[2:3]
	v_lshl_add_u64 v[2:3], s[16:17], 0, v[2:3]
	global_store_dword v[2:3], v1, off offset:192 sc1
	global_store_dword v[4:5], v6, off offset:192 sc1

.LBB2_28:
	s_waitcnt vmcnt(5) lgkmcnt(0)
	ds_read_b128 v[2:5], v31
	v_or_b32_e32 v1, s60, v28
	s_waitcnt vmcnt(4)
	v_mad_i64_i32 v[6:7], s[6:7], v1, s44, 0
	v_lshl_add_u64 v[6:7], v[6:7], 1, v[24:25]
	s_waitcnt lgkmcnt(0)
	global_store_dwordx4 v[6:7], v[2:5], off sc1

.LBB2_35:
.LBB2_36:
	s_abs_i32 s6, s43
	v_cvt_f32_u32_e32 v0, s6
	s_add_i32 s7, s62, s57
	s_sub_i32 s57, 0, s6
	s_abs_i32 s56, s7
	v_rcp_iflag_f32_e32 v0, v0
	s_xor_b32 s33, s7, s43
	s_ashr_i32 s33, s33, 31
	v_mul_f32_e32 v0, 0x4f7ffffe, v0
	v_cvt_u32_f32_e32 v0, v0
	s_nop 0
	v_readfirstlane_b32 s58, v0
	s_mul_i32 s57, s57, s58
	s_mul_hi_u32 s57, s58, s57
	s_add_i32 s58, s58, s57
	s_mul_hi_u32 s57, s56, s58
	s_mul_i32 s58, s57, s6
	s_sub_i32 s56, s56, s58
	s_add_i32 s59, s57, 1
	s_sub_i32 s58, s56, s6
	s_cmp_ge_u32 s56, s6
	s_cselect_b32 s57, s59, s57
	s_cselect_b32 s56, s58, s56
	s_add_i32 s58, s57, 1
	s_cmp_ge_u32 s56, s6
	s_cselect_b32 s6, s58, s57
	s_abs_i32 s56, s42
	v_cvt_f32_u32_e32 v0, s56
	s_xor_b32 s6, s6, s33
	s_sub_i32 s57, 0, s56
	s_sub_i32 s6, s6, s33
	v_rcp_iflag_f32_e32 v0, v0
	s_mul_i32 s33, s6, s43
	s_sub_i32 s7, s7, s33
	s_abs_i32 s43, s7
	v_mul_f32_e32 v0, 0x4f7ffffe, v0
	v_cvt_u32_f32_e32 v0, v0
	s_xor_b32 s33, s7, s42
	s_ashr_i32 s33, s33, 31
	v_readfirstlane_b32 s58, v0
	s_mul_i32 s57, s57, s58
	s_mul_hi_u32 s57, s58, s57
	s_add_i32 s58, s58, s57
	s_mul_hi_u32 s57, s43, s58
	s_mul_i32 s58, s57, s56
	s_sub_i32 s43, s43, s58
	s_add_i32 s59, s57, 1
	s_sub_i32 s58, s43, s56
	s_cmp_ge_u32 s43, s56
	s_cselect_b32 s57, s59, s57
	s_cselect_b32 s43, s58, s43
	s_add_i32 s58, s57, 1
	s_cmp_ge_u32 s43, s56
	s_cselect_b32 s43, s58, s57
	s_xor_b32 s43, s43, s33
	s_sub_i32 s56, s43, s33
	s_mul_i32 s33, s56, s42
	s_sub_i32 s33, s7, s33
	s_mul_hi_i32 s43, s6, s40
	s_mul_i32 s7, s6, s40
	s_lshl_b32 s33, s33, 6
	s_lshl_b32 s6, s56, 7
	s_and_saveexec_b64 s[56:57], s[4:5]
	s_cbranch_execz .LBB2_40
	v_or_b32_e32 v0, s33, v37
	v_cmp_gt_i32_e32 vcc, s41, v0
	v_mov_b32_e32 v1, 0
	s_waitcnt vmcnt(5)
	v_mov_b32_e32 v2, 0
	v_mov_b32_e32 v3, 0
	v_mov_b32_e32 v4, 0
	v_mov_b32_e32 v5, 0
	s_waitcnt vmcnt(4)
	v_mov_b32_e32 v6, 0
	v_mov_b32_e32 v7, 0
	v_mov_b32_e32 v8, 0
	v_mov_b32_e32 v9, 0
	s_waitcnt vmcnt(3)
	v_mov_b32_e32 v10, 0
	v_mov_b32_e32 v11, 0
	v_mov_b32_e32 v12, 0
	v_mov_b32_e32 v13, 0
	s_waitcnt vmcnt(2)
	v_mov_b32_e32 v14, 0
	v_mov_b32_e32 v15, 0
	v_mov_b32_e32 v16, 0
	v_mov_b32_e32 v17, 0
	v_mov_b32_e32 v18, 0
	v_mov_b32_e32 v19, 0
	v_mov_b32_e32 v20, 0
	v_mov_b32_e32 v21, 0
	v_mov_b32_e32 v23, 0
	v_mov_b32_e32 v24, 0
	v_mov_b32_e32 v25, 0
	v_mov_b32_e32 v27, 0
	v_mov_b32_e32 v39, 0
	v_mov_b32_e32 v40, 0
	v_mov_b32_e32 v41, 0
	v_mov_b32_e32 v42, 0
	v_mov_b32_e32 v43, 0
	v_mov_b32_e32 v44, 0
	v_mov_b32_e32 v45, 0
	s_and_saveexec_b64 s[58:59], vcc
	s_cbranch_execz .LBB2_39
	s_ashr_i32 s60, s41, 31
	s_mul_hi_u32 s61, s7, s41
	s_mul_i32 s60, s7, s60
	s_add_i32 s60, s61, s60
	s_mul_i32 s61, s43, s41
	s_add_i32 s61, s60, s61
	s_mul_i32 s60, s7, s41
	s_lshl_b64 s[60:61], s[60:61], 2
	s_add_u32 s48, s48, s60
	v_or_b32_e32 v27, s6, v36
	s_addc_u32 s49, s49, s61
	v_ashrrev_i32_e32 v1, 31, v0
	v_or_b32_e32 v2, 1, v27
	v_or_b32_e32 v4, 2, v27
	v_or_b32_e32 v6, 3, v27
	v_or_b32_e32 v8, 4, v27
	v_lshl_add_u64 v[40:41], v[0:1], 2, s[48:49]
	v_mad_i64_i32 v[0:1], s[48:49], v27, s41, 0
	v_mad_i64_i32 v[2:3], s[48:49], v2, s41, 0
	v_mad_i64_i32 v[4:5], s[48:49], v4, s41, 0
	v_mad_i64_i32 v[6:7], s[48:49], v6, s41, 0
	v_mad_i64_i32 v[8:9], s[48:49], v8, s41, 0
	v_or_b32_e32 v10, 5, v27
	v_or_b32_e32 v12, 6, v27
	v_or_b32_e32 v14, 7, v27
	v_lshl_add_u64 v[0:1], v[0:1], 2, v[40:41]
	v_lshl_add_u64 v[2:3], v[2:3], 2, v[40:41]
	v_lshl_add_u64 v[4:5], v[4:5], 2, v[40:41]
	v_lshl_add_u64 v[6:7], v[6:7], 2, v[40:41]
	v_lshl_add_u64 v[8:9], v[8:9], 2, v[40:41]
	v_mad_i64_i32 v[10:11], s[48:49], v10, s41, 0
	v_mad_i64_i32 v[12:13], s[48:49], v12, s41, 0
	v_mad_i64_i32 v[14:15], s[48:49], v14, s41, 0
	v_lshl_add_u64 v[10:11], v[10:11], 2, v[40:41]
	v_lshl_add_u64 v[12:13], v[12:13], 2, v[40:41]
	v_lshl_add_u64 v[14:15], v[14:15], 2, v[40:41]
	global_load_dword v1, v[0:1], off nt
	s_nop 0
	global_load_dword v2, v[2:3], off nt
	s_nop 0
	global_load_dword v3, v[4:5], off nt
	s_nop 0
	global_load_dword v4, v[6:7], off nt
	global_load_dword v5, v[8:9], off nt
	s_nop 0
	global_load_dword v6, v[10:11], off nt
	global_load_dword v7, v[12:13], off nt
	global_load_dword v8, v[14:15], off nt
	v_or_b32_e32 v0, 8, v27
	v_mad_i64_i32 v[10:11], s[48:49], v0, s41, 0
	v_or_b32_e32 v0, 9, v27
	v_mad_i64_i32 v[12:13], s[48:49], v0, s41, 0
	v_or_b32_e32 v0, 10, v27
	v_mad_i64_i32 v[14:15], s[48:49], v0, s41, 0
	v_or_b32_e32 v0, 11, v27
	v_mad_i64_i32 v[16:17], s[48:49], v0, s41, 0
	v_or_b32_e32 v0, 12, v27
	v_mad_i64_i32 v[18:19], s[48:49], v0, s41, 0
	v_or_b32_e32 v0, 13, v27
	v_mad_i64_i32 v[20:21], s[48:49], v0, s41, 0
	v_or_b32_e32 v0, 14, v27
	v_mad_i64_i32 v[24:25], s[48:49], v0, s41, 0
	v_or_b32_e32 v0, 15, v27
	v_lshl_add_u64 v[10:11], v[10:11], 2, v[40:41]
	v_lshl_add_u64 v[12:13], v[12:13], 2, v[40:41]
	v_lshl_add_u64 v[14:15], v[14:15], 2, v[40:41]
	v_lshl_add_u64 v[16:17], v[16:17], 2, v[40:41]
	v_lshl_add_u64 v[18:19], v[18:19], 2, v[40:41]
	v_mad_i64_i32 v[42:43], s[48:49], v0, s41, 0
	v_or_b32_e32 v0, 16, v27
	v_lshl_add_u64 v[20:21], v[20:21], 2, v[40:41]
	v_lshl_add_u64 v[24:25], v[24:25], 2, v[40:41]
	v_lshl_add_u64 v[42:43], v[42:43], 2, v[40:41]
	global_load_dword v9, v[10:11], off nt
	s_nop 0
	global_load_dword v10, v[12:13], off nt
	global_load_dword v11, v[14:15], off nt
	s_nop 0
	global_load_dword v12, v[16:17], off nt
	global_load_dword v13, v[18:19], off nt
	global_load_dword v14, v[20:21], off nt
	global_load_dword v15, v[24:25], off nt
	s_nop 0
	global_load_dword v16, v[42:43], off nt
	v_mad_i64_i32 v[18:19], s[48:49], v0, s41, 0
	v_or_b32_e32 v0, 17, v27
	v_mad_i64_i32 v[20:21], s[48:49], v0, s41, 0
	v_or_b32_e32 v0, 18, v27
	v_mad_i64_i32 v[24:25], s[48:49], v0, s41, 0
	v_or_b32_e32 v0, 19, v27
	v_mad_i64_i32 v[42:43], s[48:49], v0, s41, 0
	v_or_b32_e32 v0, 20, v27
	v_mad_i64_i32 v[44:45], s[48:49], v0, s41, 0
	v_or_b32_e32 v0, 21, v27
	v_mad_i64_i32 v[46:47], s[48:49], v0, s41, 0
	v_or_b32_e32 v0, 22, v27
	v_mad_i64_i32 v[48:49], s[48:49], v0, s41, 0
	v_or_b32_e32 v0, 23, v27
	v_lshl_add_u64 v[18:19], v[18:19], 2, v[40:41]
	v_lshl_add_u64 v[20:21], v[20:21], 2, v[40:41]
	v_lshl_add_u64 v[24:25], v[24:25], 2, v[40:41]
	v_lshl_add_u64 v[42:43], v[42:43], 2, v[40:41]
	v_mad_i64_i32 v[50:51], s[48:49], v0, s41, 0
	v_or_b32_e32 v0, 24, v27
	v_lshl_add_u64 v[44:45], v[44:45], 2, v[40:41]
	v_lshl_add_u64 v[46:47], v[46:47], 2, v[40:41]
	v_lshl_add_u64 v[48:49], v[48:49], 2, v[40:41]
	v_lshl_add_u64 v[50:51], v[50:51], 2, v[40:41]
	global_load_dword v17, v[18:19], off nt
	s_nop 0
	global_load_dword v18, v[20:21], off nt
	global_load_dword v19, v[24:25], off nt
	s_nop 0
	global_load_dword v20, v[42:43], off nt
	global_load_dword v21, v[44:45], off nt
	global_load_dword v23, v[46:47], off nt
	global_load_dword v24, v[48:49], off nt
	global_load_dword v25, v[50:51], off nt
	v_mad_i64_i32 v[42:43], s[48:49], v0, s41, 0
	v_or_b32_e32 v0, 25, v27
	v_mad_i64_i32 v[44:45], s[48:49], v0, s41, 0
	v_or_b32_e32 v0, 26, v27
	v_mad_i64_i32 v[46:47], s[48:49], v0, s41, 0
	v_or_b32_e32 v0, 27, v27
	v_mad_i64_i32 v[48:49], s[48:49], v0, s41, 0
	v_or_b32_e32 v0, 28, v27
	v_mad_i64_i32 v[50:51], s[48:49], v0, s41, 0
	v_or_b32_e32 v0, 29, v27
	v_mad_i64_i32 v[52:53], s[48:49], v0, s41, 0
	v_or_b32_e32 v0, 30, v27
	v_mad_i64_i32 v[54:55], s[48:49], v0, s41, 0
	v_or_b32_e32 v0, 31, v27
	v_lshl_add_u64 v[42:43], v[42:43], 2, v[40:41]
	v_lshl_add_u64 v[44:45], v[44:45], 2, v[40:41]
	v_mad_i64_i32 v[56:57], s[48:49], v0, s41, 0
	v_lshl_add_u64 v[46:47], v[46:47], 2, v[40:41]
	v_lshl_add_u64 v[48:49], v[48:49], 2, v[40:41]
	v_lshl_add_u64 v[50:51], v[50:51], 2, v[40:41]
	v_lshl_add_u64 v[52:53], v[52:53], 2, v[40:41]
	v_lshl_add_u64 v[54:55], v[54:55], 2, v[40:41]
	v_lshl_add_u64 v[56:57], v[56:57], 2, v[40:41]
	global_load_dword v27, v[42:43], off nt
	global_load_dword v39, v[44:45], off nt
	global_load_dword v40, v[46:47], off nt
	global_load_dword v41, v[48:49], off nt
	s_nop 0
	global_load_dword v42, v[50:51], off nt
	global_load_dword v43, v[52:53], off nt
	global_load_dword v44, v[54:55], off nt
	global_load_dword v45, v[56:57], off nt

.LBB2_40:
	s_or_b64 exec, exec, s[56:57]
	s_waitcnt lgkmcnt(0)
	s_barrier
	s_and_saveexec_b64 s[48:49], s[4:5]
	s_cbranch_execz .LBB2_42
	s_ashr_i32 s41, s42, 31
	s_mul_i32 s43, s42, s43
	s_mul_hi_u32 s56, s42, s7
	s_add_i32 s43, s56, s43
	s_mul_i32 s41, s41, s7
	s_add_i32 s43, s43, s41
	s_mul_i32 s42, s42, s7
	s_lshl_b64 s[42:43], s[42:43], 7
	s_add_u32 s41, s50, s42
	s_addc_u32 s42, s51, s43
	s_ashr_i32 s7, s6, 31
	s_lshl_b64 s[6:7], s[6:7], 1
	s_add_u32 s6, s41, s6
	s_addc_u32 s7, s42, s7
	v_lshlrev_b32_e32 v0, 1, v26
	v_mov_b32_e32 v1, 0
	s_waitcnt vmcnt(4)
	v_lshl_add_u64 v[8:9], s[6:7], 0, v[0:1]
	ds_read_b128 v[0:3], v34
	v_or_b32_e32 v4, s33, v22
	v_mad_i64_i32 v[4:5], s[6:7], v4, s40, 0
	s_waitcnt vmcnt(3)
	v_lshl_add_u64 v[10:11], v[4:5], 1, v[8:9]
	ds_read_b128 v[4:7], v33
	s_waitcnt lgkmcnt(1)
	global_store_dwordx4 v[10:11], v[0:3], off sc1
	s_nop 1
	v_or_b32_e32 v0, s33, v30
	v_mad_i64_i32 v[0:1], s[6:7], v0, s40, 0
	v_lshl_add_u64 v[0:1], v[0:1], 1, v[8:9]
	s_waitcnt lgkmcnt(0)
	global_store_dwordx4 v[0:1], v[4:7], off sc1
	ds_read_b128 v[0:3], v32
	s_nop 0
	v_or_b32_e32 v4, s33, v29
	v_mad_i64_i32 v[4:5], s[6:7], v4, s40, 0
	v_lshl_add_u64 v[10:11], v[4:5], 1, v[8:9]
	ds_read_b128 v[4:7], v31
	s_waitcnt lgkmcnt(1)
	global_store_dwordx4 v[10:11], v[0:3], off sc1
	s_nop 1
	v_or_b32_e32 v0, s33, v28
	v_mad_i64_i32 v[0:1], s[6:7], v0, s40, 0
	v_lshl_add_u64 v[0:1], v[0:1], 1, v[8:9]
	s_waitcnt lgkmcnt(0)
	global_store_dwordx4 v[0:1], v[4:7], off sc1

.LBB2_46:
.LBB2_47:
	s_abs_i32 s0, s39
	v_cvt_f32_u32_e32 v0, s0
	s_sub_i32 s42, 0, s0
	s_add_i32 s1, s33, s55
	s_abs_i32 s41, s1
	v_rcp_iflag_f32_e32 v0, v0
	s_xor_b32 s40, s1, s39
	s_ashr_i32 s40, s40, 31
	v_mul_f32_e32 v0, 0x4f7ffffe, v0
	v_cvt_u32_f32_e32 v0, v0
	s_nop 0
	v_readfirstlane_b32 s43, v0
	s_mul_i32 s42, s42, s43
	s_mul_hi_u32 s42, s43, s42
	s_add_i32 s43, s43, s42
	s_mul_hi_u32 s42, s41, s43
	s_mul_i32 s43, s42, s0
	s_sub_i32 s41, s41, s43
	s_add_i32 s48, s42, 1
	s_sub_i32 s43, s41, s0
	s_cmp_ge_u32 s41, s0
	s_cselect_b32 s42, s48, s42
	s_cselect_b32 s41, s43, s41
	s_add_i32 s43, s42, 1
	s_cmp_ge_u32 s41, s0
	s_cselect_b32 s0, s43, s42
	s_abs_i32 s41, s38
	v_cvt_f32_u32_e32 v0, s41
	s_xor_b32 s0, s0, s40
	s_sub_i32 s42, 0, s41
	s_sub_i32 s0, s0, s40
	v_rcp_iflag_f32_e32 v0, v0
	s_mul_i32 s39, s0, s39
	s_sub_i32 s39, s1, s39
	s_abs_i32 s40, s39
	v_mul_f32_e32 v0, 0x4f7ffffe, v0
	v_cvt_u32_f32_e32 v0, v0
	s_xor_b32 s1, s39, s38
	s_ashr_i32 s1, s1, 31
	v_readfirstlane_b32 s43, v0
	s_mul_i32 s42, s42, s43
	s_mul_hi_u32 s42, s43, s42
	s_add_i32 s43, s43, s42
	s_mul_hi_u32 s42, s40, s43
	s_mul_i32 s43, s42, s41
	s_sub_i32 s40, s40, s43
	s_add_i32 s48, s42, 1
	s_sub_i32 s43, s40, s41
	s_cmp_ge_u32 s40, s41
	s_cselect_b32 s42, s48, s42
	s_cselect_b32 s40, s43, s40
	s_add_i32 s43, s42, 1
	s_cmp_ge_u32 s40, s41
	s_cselect_b32 s40, s43, s42
	s_xor_b32 s40, s40, s1
	s_sub_i32 s1, s40, s1
	s_mul_i32 s40, s1, s38
	s_sub_i32 s40, s39, s40
	s_mul_hi_i32 s41, s0, s36
	s_mul_i32 s39, s0, s36
	s_ashr_i32 s50, s37, 31
	s_lshl_b32 s40, s40, 6
	s_lshl_b32 s0, s1, 7
	s_and_saveexec_b64 s[42:43], s[4:5]
	s_cbranch_execz .LBB2_51
	v_or_b32_e32 v0, s40, v37
	v_cmp_gt_i32_e32 vcc, s37, v0
	v_mov_b32_e32 v1, 0
	s_waitcnt vmcnt(5)
	v_mov_b32_e32 v2, 0
	v_mov_b32_e32 v3, 0
	v_mov_b32_e32 v4, 0
	v_mov_b32_e32 v5, 0
	s_waitcnt vmcnt(4)
	v_mov_b32_e32 v6, 0
	v_mov_b32_e32 v7, 0
	v_mov_b32_e32 v8, 0
	v_mov_b32_e32 v9, 0
	s_waitcnt vmcnt(3)
	v_mov_b32_e32 v10, 0
	v_mov_b32_e32 v11, 0
	v_mov_b32_e32 v12, 0
	v_mov_b32_e32 v13, 0
	s_waitcnt vmcnt(2)
	v_mov_b32_e32 v14, 0
	v_mov_b32_e32 v15, 0
	v_mov_b32_e32 v16, 0
	v_mov_b32_e32 v17, 0
	v_mov_b32_e32 v18, 0
	v_mov_b32_e32 v19, 0
	v_mov_b32_e32 v20, 0
	v_mov_b32_e32 v21, 0
	v_mov_b32_e32 v23, 0
	v_mov_b32_e32 v24, 0
	v_mov_b32_e32 v25, 0
	v_mov_b32_e32 v27, 0
	v_mov_b32_e32 v39, 0
	v_mov_b32_e32 v40, 0
	v_mov_b32_e32 v41, 0
	v_mov_b32_e32 v42, 0
	v_mov_b32_e32 v43, 0
	v_mov_b32_e32 v44, 0
	v_mov_b32_e32 v45, 0
	s_and_saveexec_b64 s[48:49], vcc
	s_cbranch_execz .LBB2_50
	s_mul_i32 s50, s39, s50
	s_mul_hi_u32 s51, s39, s37
	s_add_i32 s50, s51, s50
	s_mul_i32 s51, s41, s37
	s_add_i32 s51, s50, s51
	s_mul_i32 s50, s39, s37
	s_lshl_b64 s[50:51], s[50:51], 2
	s_add_u32 s44, s44, s50
	s_addc_u32 s45, s45, s51
	v_or_b32_e32 v27, s0, v36
	v_ashrrev_i32_e32 v1, 31, v0
	v_lshl_add_u64 v[40:41], v[0:1], 2, s[44:45]
	v_mad_i64_i32 v[0:1], s[44:45], v27, s37, 0
	v_lshl_add_u64 v[10:11], v[0:1], 2, v[40:41]
	v_or_b32_e32 v0, 1, v27
	v_mad_i64_i32 v[0:1], s[44:45], v0, s37, 0
	v_lshl_add_u64 v[12:13], v[0:1], 2, v[40:41]
	v_or_b32_e32 v0, 2, v27
	v_mad_i64_i32 v[0:1], s[44:45], v0, s37, 0
	v_lshl_add_u64 v[14:15], v[0:1], 2, v[40:41]
	v_or_b32_e32 v0, 3, v27
	v_mad_i64_i32 v[0:1], s[44:45], v0, s37, 0
	v_lshl_add_u64 v[16:17], v[0:1], 2, v[40:41]
	v_or_b32_e32 v0, 4, v27
	v_mad_i64_i32 v[0:1], s[44:45], v0, s37, 0
	v_lshl_add_u64 v[18:19], v[0:1], 2, v[40:41]
	v_or_b32_e32 v0, 5, v27
	v_mad_i64_i32 v[0:1], s[44:45], v0, s37, 0
	v_lshl_add_u64 v[20:21], v[0:1], 2, v[40:41]
	v_or_b32_e32 v0, 6, v27
	v_mad_i64_i32 v[0:1], s[44:45], v0, s37, 0
	v_lshl_add_u64 v[24:25], v[0:1], 2, v[40:41]
	v_or_b32_e32 v0, 7, v27
	v_mad_i64_i32 v[0:1], s[44:45], v0, s37, 0
	v_lshl_add_u64 v[42:43], v[0:1], 2, v[40:41]
	v_or_b32_e32 v0, 8, v27
	global_load_dword v1, v[10:11], off nt
	global_load_dword v2, v[12:13], off nt
	global_load_dword v3, v[14:15], off nt
	global_load_dword v4, v[16:17], off nt
	global_load_dword v5, v[18:19], off nt
	global_load_dword v6, v[20:21], off nt
	global_load_dword v7, v[24:25], off nt
	global_load_dword v8, v[42:43], off nt
	v_mad_i64_i32 v[10:11], s[44:45], v0, s37, 0
	v_or_b32_e32 v0, 9, v27
	v_mad_i64_i32 v[12:13], s[44:45], v0, s37, 0
	v_or_b32_e32 v0, 10, v27
	v_lshl_add_u64 v[18:19], v[12:13], 2, v[40:41]
	v_mad_i64_i32 v[12:13], s[44:45], v0, s37, 0
	v_or_b32_e32 v0, 11, v27
	v_lshl_add_u64 v[20:21], v[12:13], 2, v[40:41]
	v_mad_i64_i32 v[12:13], s[44:45], v0, s37, 0
	v_or_b32_e32 v0, 12, v27
	v_lshl_add_u64 v[24:25], v[12:13], 2, v[40:41]
	v_mad_i64_i32 v[12:13], s[44:45], v0, s37, 0
	v_or_b32_e32 v0, 13, v27
	v_lshl_add_u64 v[42:43], v[12:13], 2, v[40:41]
	v_mad_i64_i32 v[12:13], s[44:45], v0, s37, 0
	v_or_b32_e32 v0, 14, v27
	v_lshl_add_u64 v[44:45], v[12:13], 2, v[40:41]
	v_mad_i64_i32 v[12:13], s[44:45], v0, s37, 0
	v_or_b32_e32 v0, 15, v27
	v_lshl_add_u64 v[10:11], v[10:11], 2, v[40:41]
	v_lshl_add_u64 v[46:47], v[12:13], 2, v[40:41]
	v_mad_i64_i32 v[12:13], s[44:45], v0, s37, 0
	v_or_b32_e32 v0, 16, v27
	v_lshl_add_u64 v[48:49], v[12:13], 2, v[40:41]
	global_load_dword v9, v[10:11], off nt
	s_nop 0
	global_load_dword v10, v[18:19], off nt
	global_load_dword v11, v[20:21], off nt
	global_load_dword v12, v[24:25], off nt
	global_load_dword v13, v[42:43], off nt
	global_load_dword v14, v[44:45], off nt
	global_load_dword v15, v[46:47], off nt
	global_load_dword v16, v[48:49], off nt
	v_mad_i64_i32 v[18:19], s[44:45], v0, s37, 0
	v_or_b32_e32 v0, 17, v27
	v_mad_i64_i32 v[20:21], s[44:45], v0, s37, 0
	v_or_b32_e32 v0, 18, v27
	v_lshl_add_u64 v[42:43], v[20:21], 2, v[40:41]
	v_mad_i64_i32 v[20:21], s[44:45], v0, s37, 0
	v_or_b32_e32 v0, 19, v27
	v_lshl_add_u64 v[44:45], v[20:21], 2, v[40:41]
	v_mad_i64_i32 v[20:21], s[44:45], v0, s37, 0
	v_or_b32_e32 v0, 20, v27
	v_lshl_add_u64 v[46:47], v[20:21], 2, v[40:41]
	v_mad_i64_i32 v[20:21], s[44:45], v0, s37, 0
	v_or_b32_e32 v0, 21, v27
	v_lshl_add_u64 v[48:49], v[20:21], 2, v[40:41]
	v_mad_i64_i32 v[20:21], s[44:45], v0, s37, 0
	v_or_b32_e32 v0, 22, v27
	v_lshl_add_u64 v[50:51], v[20:21], 2, v[40:41]
	v_mad_i64_i32 v[20:21], s[44:45], v0, s37, 0
	v_or_b32_e32 v0, 23, v27
	v_lshl_add_u64 v[18:19], v[18:19], 2, v[40:41]
	v_lshl_add_u64 v[52:53], v[20:21], 2, v[40:41]
	v_mad_i64_i32 v[20:21], s[44:45], v0, s37, 0
	v_or_b32_e32 v0, 24, v27
	v_lshl_add_u64 v[54:55], v[20:21], 2, v[40:41]
	global_load_dword v17, v[18:19], off nt
	s_nop 0
	global_load_dword v18, v[42:43], off nt
	global_load_dword v19, v[44:45], off nt
	global_load_dword v20, v[46:47], off nt
	global_load_dword v21, v[48:49], off nt
	global_load_dword v23, v[50:51], off nt
	global_load_dword v24, v[52:53], off nt
	global_load_dword v25, v[54:55], off nt
	v_mad_i64_i32 v[42:43], s[44:45], v0, s37, 0
	v_or_b32_e32 v0, 25, v27
	v_mad_i64_i32 v[44:45], s[44:45], v0, s37, 0
	v_or_b32_e32 v0, 26, v27
	v_lshl_add_u64 v[46:47], v[44:45], 2, v[40:41]
	v_mad_i64_i32 v[44:45], s[44:45], v0, s37, 0
	v_or_b32_e32 v0, 27, v27
	v_lshl_add_u64 v[48:49], v[44:45], 2, v[40:41]
	v_mad_i64_i32 v[44:45], s[44:45], v0, s37, 0
	v_or_b32_e32 v0, 28, v27
	v_lshl_add_u64 v[50:51], v[44:45], 2, v[40:41]
	v_mad_i64_i32 v[44:45], s[44:45], v0, s37, 0
	v_or_b32_e32 v0, 29, v27
	v_lshl_add_u64 v[52:53], v[44:45], 2, v[40:41]
	v_mad_i64_i32 v[44:45], s[44:45], v0, s37, 0
	v_or_b32_e32 v0, 30, v27
	v_lshl_add_u64 v[54:55], v[44:45], 2, v[40:41]
	v_mad_i64_i32 v[44:45], s[44:45], v0, s37, 0
	v_or_b32_e32 v0, 31, v27
	v_lshl_add_u64 v[42:43], v[42:43], 2, v[40:41]
	v_lshl_add_u64 v[56:57], v[44:45], 2, v[40:41]
	v_mad_i64_i32 v[44:45], s[44:45], v0, s37, 0
	v_lshl_add_u64 v[58:59], v[44:45], 2, v[40:41]
	global_load_dword v27, v[42:43], off nt
	global_load_dword v39, v[46:47], off nt
	global_load_dword v40, v[48:49], off nt
	global_load_dword v41, v[50:51], off nt
	s_nop 0
	global_load_dword v42, v[52:53], off nt
	global_load_dword v43, v[54:55], off nt
	global_load_dword v44, v[56:57], off nt
	global_load_dword v45, v[58:59], off nt

.LBB2_56:
.LBB2_57:
	s_ashr_i32 s8, s38, 31
	s_mul_i32 s9, s38, s41
	s_mul_hi_u32 s10, s38, s39
	s_add_i32 s9, s10, s9
	s_mul_i32 s8, s8, s39
	s_add_i32 s9, s9, s8
	s_mul_i32 s8, s38, s39
	s_lshl_b64 s[8:9], s[8:9], 7
	s_add_u32 s38, s46, s8
	s_addc_u32 s39, s47, s9
	s_mul_hi_i32 s9, s1, s37
	s_mul_i32 s8, s1, s37
	s_lshl_b64 s[10:11], s[8:9], 2
	s_add_u32 s8, s12, s10
	s_addc_u32 s9, s13, s11
	s_add_u32 s10, s14, s10
	s_addc_u32 s11, s15, s11
	s_ashr_i32 s1, s0, 31
	s_lshl_b64 s[0:1], s[0:1], 1
	s_add_u32 s0, s38, s0
	s_addc_u32 s1, s39, s1
	s_waitcnt vmcnt(2)
	v_lshlrev_b32_e32 v16, 1, v38
	v_mov_b32_e32 v17, 0
	v_lshl_add_u64 v[20:21], s[0:1], 0, v[16:17]
	ds_read_b128 v[16:19], v34
	v_or_b32_e32 v24, s40, v22
	v_mad_i64_i32 v[38:39], s[0:1], v24, s36, 0
	v_cndmask_b32_e64 v23, 0, 1, s[44:45]
	v_lshl_add_u64 v[38:39], v[38:39], 1, v[20:21]
	v_cmp_ne_u32_e64 s[0:1], 1, v23
	s_andn2_b64 vcc, exec, s[44:45]
	v_mbcnt_lo_u32_b32 v27, -1, 0
	s_waitcnt lgkmcnt(0)
	global_store_dwordx4 v[38:39], v[16:19], off sc1
	s_cbranch_vccnz .LBB2_63
	v_fma_mix_f32 v23, v4, v16, 0 op_sel_hi:[0,1,0]
	s_waitcnt vmcnt(1)
	v_fma_mix_f32 v25, v12, v16, 0 op_sel_hi:[0,1,0]
	v_fma_mix_f32 v23, v5, v16, v23 op_sel:[0,1,0] op_sel_hi:[0,1,0]
	v_fma_mix_f32 v16, v13, v16, v25 op_sel:[0,1,0] op_sel_hi:[0,1,0]
	v_fma_mix_f32 v23, v6, v17, v23 op_sel_hi:[0,1,0]
	v_fma_mix_f32 v16, v14, v17, v16 op_sel_hi:[0,1,0]
	v_fma_mix_f32 v23, v7, v17, v23 op_sel:[0,1,0] op_sel_hi:[0,1,0]
	v_fma_mix_f32 v16, v15, v17, v16 op_sel:[0,1,0] op_sel_hi:[0,1,0]
	v_fma_mix_f32 v17, v0, v18, v23 op_sel_hi:[0,1,0]
	v_fma_mix_f32 v16, v8, v18, v16 op_sel_hi:[0,1,0]
	v_fma_mix_f32 v17, v1, v18, v17 op_sel:[0,1,0] op_sel_hi:[0,1,0]
	v_fma_mix_f32 v16, v9, v18, v16 op_sel:[0,1,0] op_sel_hi:[0,1,0]
	v_fma_mix_f32 v17, v2, v19, v17 op_sel_hi:[0,1,0]
	v_fma_mix_f32 v16, v10, v19, v16 op_sel_hi:[0,1,0]
	v_fma_mix_f32 v17, v3, v19, v17 op_sel:[0,1,0] op_sel_hi:[0,1,0]
	v_fma_mix_f32 v18, v11, v19, v16 op_sel:[0,1,0] op_sel_hi:[0,1,0]
	v_mbcnt_hi_u32_b32 v19, -1, v27
	v_and_b32_e32 v16, 64, v19
	v_add_u32_e32 v25, 64, v16
	v_xor_b32_e32 v16, 1, v19
	v_cmp_lt_i32_e32 vcc, v16, v25
	s_nop 1
	v_cndmask_b32_e32 v16, v19, v16, vcc
	v_lshlrev_b32_e32 v16, 2, v16
	ds_bpermute_b32 v23, v16, v17
	ds_bpermute_b32 v38, v16, v18
	s_waitcnt lgkmcnt(1)
	v_add_f32_e32 v23, v17, v23
	v_xor_b32_e32 v17, 2, v19
	v_cmp_lt_i32_e32 vcc, v17, v25
	s_waitcnt lgkmcnt(0)
	v_add_f32_e32 v18, v18, v38
	v_cndmask_b32_e32 v17, v19, v17, vcc
	v_lshlrev_b32_e32 v17, 2, v17
	ds_bpermute_b32 v38, v17, v23
	ds_bpermute_b32 v39, v17, v18
	s_waitcnt lgkmcnt(1)
	v_add_f32_e32 v23, v23, v38
	s_waitcnt lgkmcnt(0)
	v_add_f32_e32 v38, v18, v39
	v_xor_b32_e32 v18, 4, v19
	v_cmp_lt_i32_e32 vcc, v18, v25
	s_nop 1
	v_cndmask_b32_e32 v18, v19, v18, vcc
	v_lshlrev_b32_e32 v18, 2, v18
	ds_bpermute_b32 v39, v18, v23
	ds_bpermute_b32 v40, v18, v38
	s_waitcnt lgkmcnt(1)
	v_add_f32_e32 v23, v23, v39
	v_xor_b32_e32 v39, 8, v19
	v_cmp_lt_i32_e32 vcc, v39, v25
	s_waitcnt lgkmcnt(0)
	v_add_f32_e32 v38, v38, v40
	v_ashrrev_i32_e32 v25, 31, v24
	v_cndmask_b32_e32 v19, v19, v39, vcc
	v_lshlrev_b32_e32 v19, 2, v19
	ds_bpermute_b32 v39, v19, v23
	ds_bpermute_b32 v40, v19, v38
	v_cmp_gt_i32_e32 vcc, s37, v24
	s_and_b64 s[14:15], s[2:3], vcc
	s_and_saveexec_b64 s[12:13], s[14:15]
	s_cbranch_execz .LBB2_60
	v_lshlrev_b64 v[24:25], 2, v[24:25]
	s_waitcnt lgkmcnt(0)
	v_add_f32_e32 v40, v38, v40
	v_add_f32_e32 v23, v23, v39
	v_lshl_add_u64 v[38:39], s[10:11], 0, v[24:25]
	v_lshl_add_u64 v[24:25], s[8:9], 0, v[24:25]
	global_store_dword v[24:25], v23, off sc1
	global_store_dword v[38:39], v40, off sc1
.LBB2_60:
	s_or_b64 exec, exec, s[12:13]
	s_waitcnt lgkmcnt(0)
	ds_read_b128 v[38:41], v33
	v_or_b32_e32 v42, s40, v30
	v_cmp_gt_i32_e32 vcc, s37, v42
	s_and_b64 s[14:15], s[2:3], vcc
	s_waitcnt lgkmcnt(0)
	v_fma_mix_f32 v23, v4, v38, 0 op_sel_hi:[0,1,0]
	v_fma_mix_f32 v24, v12, v38, 0 op_sel_hi:[0,1,0]
	v_fma_mix_f32 v23, v5, v38, v23 op_sel:[0,1,0] op_sel_hi:[0,1,0]
	v_fma_mix_f32 v24, v13, v38, v24 op_sel:[0,1,0] op_sel_hi:[0,1,0]
	v_fma_mix_f32 v23, v6, v39, v23 op_sel_hi:[0,1,0]
	v_fma_mix_f32 v24, v14, v39, v24 op_sel_hi:[0,1,0]
	v_fma_mix_f32 v23, v7, v39, v23 op_sel:[0,1,0] op_sel_hi:[0,1,0]
	v_fma_mix_f32 v24, v15, v39, v24 op_sel:[0,1,0] op_sel_hi:[0,1,0]
	v_fma_mix_f32 v23, v0, v40, v23 op_sel_hi:[0,1,0]
	v_fma_mix_f32 v24, v8, v40, v24 op_sel_hi:[0,1,0]
	v_fma_mix_f32 v23, v1, v40, v23 op_sel:[0,1,0] op_sel_hi:[0,1,0]
	v_fma_mix_f32 v24, v9, v40, v24 op_sel:[0,1,0] op_sel_hi:[0,1,0]
	v_fma_mix_f32 v23, v2, v41, v23 op_sel_hi:[0,1,0]
	v_fma_mix_f32 v24, v10, v41, v24 op_sel_hi:[0,1,0]
	v_fma_mix_f32 v23, v3, v41, v23 op_sel:[0,1,0] op_sel_hi:[0,1,0]
	v_fma_mix_f32 v24, v11, v41, v24 op_sel:[0,1,0] op_sel_hi:[0,1,0]
	ds_bpermute_b32 v25, v16, v23
	ds_bpermute_b32 v16, v16, v24
	s_waitcnt lgkmcnt(1)
	v_add_f32_e32 v23, v23, v25
	s_waitcnt lgkmcnt(0)
	v_add_f32_e32 v16, v24, v16
	ds_bpermute_b32 v24, v17, v23
	ds_bpermute_b32 v17, v17, v16
	s_waitcnt lgkmcnt(1)
	v_add_f32_e32 v23, v23, v24
	s_waitcnt lgkmcnt(0)
	v_add_f32_e32 v17, v16, v17
	ds_bpermute_b32 v16, v18, v23
	ds_bpermute_b32 v18, v18, v17
	v_mad_i64_i32 v[24:25], s[12:13], v42, s36, 0
	v_lshl_add_u64 v[24:25], v[24:25], 1, v[20:21]
	s_waitcnt lgkmcnt(1)
	v_add_f32_e32 v16, v23, v16
	s_waitcnt lgkmcnt(0)
	v_add_f32_e32 v17, v17, v18
	ds_bpermute_b32 v18, v19, v16
	ds_bpermute_b32 v19, v19, v17
	global_store_dwordx4 v[24:25], v[38:41], off sc1
	s_and_saveexec_b64 s[12:13], s[14:15]
	s_cbranch_execz .LBB2_62
	s_ashr_i32 s41, s40, 31
	v_mov_b32_e32 v23, 0
	s_waitcnt lgkmcnt(0)
	v_add_f32_e32 v24, v17, v19
	v_add_f32_e32 v25, v16, v18
	v_lshl_add_u64 v[16:17], s[40:41], 0, v[22:23]
	v_lshlrev_b64 v[16:17], 2, v[16:17]
	v_lshl_add_u64 v[18:19], s[10:11], 0, v[16:17]
	v_lshl_add_u64 v[16:17], s[8:9], 0, v[16:17]
	global_store_dword v[16:17], v25, off offset:64 sc1
	global_store_dword v[18:19], v24, off offset:64 sc1

.LBB2_64:
	s_and_b64 vcc, exec, s[12:13]
	s_cbranch_vccz .LBB2_66
	s_waitcnt lgkmcnt(0)
	ds_read_b128 v[16:19], v33
	v_or_b32_e32 v23, s40, v30
	v_mad_i64_i32 v[24:25], s[12:13], v23, s36, 0
	v_lshl_add_u64 v[24:25], v[24:25], 1, v[20:21]
	s_waitcnt lgkmcnt(0)
	global_store_dwordx4 v[24:25], v[16:19], off sc1
.LBB2_66:
	s_waitcnt lgkmcnt(0)
	ds_read_b128 v[16:19], v32
	v_or_b32_e32 v23, s40, v29
	v_mad_i64_i32 v[24:25], s[12:13], v23, s36, 0
	v_lshl_add_u64 v[24:25], v[24:25], 1, v[20:21]
	s_and_b64 vcc, exec, s[0:1]
	s_waitcnt lgkmcnt(0)
	global_store_dwordx4 v[24:25], v[16:19], off sc1
	s_cbranch_vccnz .LBB2_72
	v_fma_mix_f32 v24, v4, v16, 0 op_sel_hi:[0,1,0]
	s_waitcnt vmcnt(2)
	v_fma_mix_f32 v25, v12, v16, 0 op_sel_hi:[0,1,0]
	v_fma_mix_f32 v24, v5, v16, v24 op_sel:[0,1,0] op_sel_hi:[0,1,0]
	v_fma_mix_f32 v16, v13, v16, v25 op_sel:[0,1,0] op_sel_hi:[0,1,0]
	v_fma_mix_f32 v24, v6, v17, v24 op_sel_hi:[0,1,0]
	v_fma_mix_f32 v16, v14, v17, v16 op_sel_hi:[0,1,0]
	v_fma_mix_f32 v24, v7, v17, v24 op_sel:[0,1,0] op_sel_hi:[0,1,0]
	v_fma_mix_f32 v16, v15, v17, v16 op_sel:[0,1,0] op_sel_hi:[0,1,0]
	v_fma_mix_f32 v17, v0, v18, v24 op_sel_hi:[0,1,0]
	v_fma_mix_f32 v16, v8, v18, v16 op_sel_hi:[0,1,0]
	v_fma_mix_f32 v17, v1, v18, v17 op_sel:[0,1,0] op_sel_hi:[0,1,0]
	v_fma_mix_f32 v16, v9, v18, v16 op_sel:[0,1,0] op_sel_hi:[0,1,0]
	v_fma_mix_f32 v17, v2, v19, v17 op_sel_hi:[0,1,0]
	v_fma_mix_f32 v16, v10, v19, v16 op_sel_hi:[0,1,0]
	v_fma_mix_f32 v17, v3, v19, v17 op_sel:[0,1,0] op_sel_hi:[0,1,0]
	v_fma_mix_f32 v18, v11, v19, v16 op_sel:[0,1,0] op_sel_hi:[0,1,0]
	v_mbcnt_hi_u32_b32 v19, -1, v27
	v_and_b32_e32 v16, 64, v19
	v_add_u32_e32 v27, 64, v16
	v_xor_b32_e32 v16, 1, v19
	v_cmp_lt_i32_e32 vcc, v16, v27
	s_nop 1
	v_cndmask_b32_e32 v16, v19, v16, vcc
	v_lshlrev_b32_e32 v16, 2, v16
	ds_bpermute_b32 v24, v16, v17
	ds_bpermute_b32 v25, v16, v18
	s_waitcnt lgkmcnt(1)
	v_add_f32_e32 v24, v17, v24
	v_xor_b32_e32 v17, 2, v19
	v_cmp_lt_i32_e32 vcc, v17, v27
	s_waitcnt lgkmcnt(0)
	v_add_f32_e32 v18, v18, v25
	v_cndmask_b32_e32 v17, v19, v17, vcc
	v_lshlrev_b32_e32 v17, 2, v17
	ds_bpermute_b32 v25, v17, v24
	ds_bpermute_b32 v38, v17, v18
	s_waitcnt lgkmcnt(1)
	v_add_f32_e32 v24, v24, v25
	s_waitcnt lgkmcnt(0)
	v_add_f32_e32 v25, v18, v38
	v_xor_b32_e32 v18, 4, v19
	v_cmp_lt_i32_e32 vcc, v18, v27
	s_nop 1
	v_cndmask_b32_e32 v18, v19, v18, vcc
	v_lshlrev_b32_e32 v18, 2, v18
	ds_bpermute_b32 v38, v18, v24
	ds_bpermute_b32 v39, v18, v25
	s_waitcnt lgkmcnt(1)
	v_add_f32_e32 v24, v24, v38
	v_xor_b32_e32 v38, 8, v19
	v_cmp_lt_i32_e32 vcc, v38, v27
	s_waitcnt lgkmcnt(0)
	v_add_f32_e32 v25, v25, v39
	v_cndmask_b32_e32 v19, v19, v38, vcc
	v_lshlrev_b32_e32 v19, 2, v19
	ds_bpermute_b32 v27, v19, v24
	ds_bpermute_b32 v38, v19, v25
	v_cmp_gt_i32_e32 vcc, s37, v23
	s_and_b64 s[12:13], s[2:3], vcc
	s_and_saveexec_b64 s[0:1], s[12:13]
	s_cbranch_execz .LBB2_69
	s_ashr_i32 s41, s40, 31
	v_mov_b32_e32 v23, 0
	s_waitcnt lgkmcnt(0)
	v_add_f32_e32 v40, v25, v38
	v_add_f32_e32 v27, v24, v27
	v_lshl_add_u64 v[24:25], s[40:41], 0, v[22:23]
	v_lshlrev_b64 v[24:25], 2, v[24:25]
	v_lshl_add_u64 v[38:39], s[10:11], 0, v[24:25]
	v_lshl_add_u64 v[24:25], s[8:9], 0, v[24:25]
	global_store_dword v[24:25], v27, off offset:128 sc1
	global_store_dword v[38:39], v40, off offset:128 sc1
.LBB2_69:
	s_or_b64 exec, exec, s[0:1]
	s_waitcnt lgkmcnt(0)
	ds_read_b128 v[38:41], v31
	s_waitcnt lgkmcnt(0)
	v_fma_mix_f32 v4, v4, v38, 0 op_sel_hi:[0,1,0]
	v_fma_mix_f32 v12, v12, v38, 0 op_sel_hi:[0,1,0]
	v_fma_mix_f32 v4, v5, v38, v4 op_sel:[0,1,0] op_sel_hi:[0,1,0]
	v_fma_mix_f32 v5, v13, v38, v12 op_sel:[0,1,0] op_sel_hi:[0,1,0]
	v_fma_mix_f32 v4, v6, v39, v4 op_sel_hi:[0,1,0]
	v_fma_mix_f32 v5, v14, v39, v5 op_sel_hi:[0,1,0]
	v_fma_mix_f32 v4, v7, v39, v4 op_sel:[0,1,0] op_sel_hi:[0,1,0]
	v_fma_mix_f32 v5, v15, v39, v5 op_sel:[0,1,0] op_sel_hi:[0,1,0]
	v_fma_mix_f32 v0, v0, v40, v4 op_sel_hi:[0,1,0]
	v_fma_mix_f32 v4, v8, v40, v5 op_sel_hi:[0,1,0]
	v_fma_mix_f32 v0, v1, v40, v0 op_sel:[0,1,0] op_sel_hi:[0,1,0]
	v_fma_mix_f32 v1, v9, v40, v4 op_sel:[0,1,0] op_sel_hi:[0,1,0]
	v_fma_mix_f32 v0, v2, v41, v0 op_sel_hi:[0,1,0]
	v_fma_mix_f32 v1, v10, v41, v1 op_sel_hi:[0,1,0]
	v_fma_mix_f32 v0, v3, v41, v0 op_sel:[0,1,0] op_sel_hi:[0,1,0]
	v_fma_mix_f32 v1, v11, v41, v1 op_sel:[0,1,0] op_sel_hi:[0,1,0]
	ds_bpermute_b32 v2, v16, v0
	ds_bpermute_b32 v3, v16, v1
	v_or_b32_e32 v6, s40, v28
	v_mad_i64_i32 v[4:5], s[0:1], v6, s36, 0
	s_waitcnt lgkmcnt(1)
	v_add_f32_e32 v0, v0, v2
	s_waitcnt lgkmcnt(0)
	v_add_f32_e32 v1, v1, v3
	ds_bpermute_b32 v2, v17, v0
	ds_bpermute_b32 v3, v17, v1
	v_cmp_gt_i32_e32 vcc, s37, v6
	v_lshl_add_u64 v[4:5], v[4:5], 1, v[20:21]
	s_and_b64 s[2:3], s[2:3], vcc
	s_waitcnt lgkmcnt(1)
	v_add_f32_e32 v0, v0, v2
	s_waitcnt lgkmcnt(0)
	v_add_f32_e32 v1, v1, v3
	ds_bpermute_b32 v2, v18, v0
	ds_bpermute_b32 v3, v18, v1
	global_store_dwordx4 v[4:5], v[38:41], off sc1
	s_waitcnt lgkmcnt(1)
	v_add_f32_e32 v0, v0, v2
	s_waitcnt lgkmcnt(0)
	v_add_f32_e32 v1, v1, v3
	ds_bpermute_b32 v2, v19, v0
	ds_bpermute_b32 v3, v19, v1
	s_and_saveexec_b64 s[0:1], s[2:3]
	s_cbranch_execz .LBB2_71
	s_ashr_i32 s41, s40, 31
	v_mov_b32_e32 v23, 0
	s_waitcnt lgkmcnt(0)
	v_add_f32_e32 v4, v1, v3
	v_add_f32_e32 v5, v0, v2
	v_lshl_add_u64 v[0:1], s[40:41], 0, v[22:23]
	v_lshlrev_b64 v[0:1], 2, v[0:1]
	v_lshl_add_u64 v[2:3], s[10:11], 0, v[0:1]
	v_lshl_add_u64 v[0:1], s[8:9], 0, v[0:1]
	global_store_dword v[0:1], v5, off offset:192 sc1
	global_store_dword v[2:3], v4, off offset:192 sc1

.LBB2_73:
	s_and_b64 vcc, exec, s[0:1]
	s_cbranch_vccz .LBB2_75
	s_waitcnt lgkmcnt(0)
	ds_read_b128 v[0:3], v31
	v_or_b32_e32 v4, s40, v28
	v_mad_i64_i32 v[4:5], s[0:1], v4, s36, 0
	v_lshl_add_u64 v[4:5], v[4:5], 1, v[20:21]
	s_waitcnt lgkmcnt(0)
	global_store_dwordx4 v[4:5], v[0:3], off sc1

.LBB2_76:
	s_cmp_ge_i32 s40, s52
	s_cselect_b64 s[0:1], -1, 0
	s_cmp_lt_i32 s40, s52
	s_mov_b64 s[2:3], -1
	s_cbranch_scc0 .LBB2_84
	s_abs_i32 s2, s31
	v_cvt_f32_u32_e32 v0, s2
	s_sub_i32 s8, 0, s2
	s_add_i32 s3, s40, s53
	s_abs_i32 s7, s3
	v_rcp_iflag_f32_e32 v0, v0
	s_xor_b32 s6, s3, s31
	s_ashr_i32 s6, s6, 31
	v_mul_f32_e32 v0, 0x4f7ffffe, v0
	v_cvt_u32_f32_e32 v0, v0
	s_nop 0
	v_readfirstlane_b32 s9, v0
	s_mul_i32 s8, s8, s9
	s_mul_hi_u32 s8, s9, s8
	s_add_i32 s9, s9, s8
	s_mul_hi_u32 s8, s7, s9
	s_mul_i32 s9, s8, s2
	s_sub_i32 s7, s7, s9
	s_add_i32 s10, s8, 1
	s_sub_i32 s9, s7, s2
	s_cmp_ge_u32 s7, s2
	s_cselect_b32 s8, s10, s8
	s_cselect_b32 s7, s9, s7
	s_add_i32 s9, s8, 1
	s_cmp_ge_u32 s7, s2
	s_cselect_b32 s2, s9, s8
	s_abs_i32 s7, s30
	v_cvt_f32_u32_e32 v0, s7
	s_xor_b32 s2, s2, s6
	s_sub_i32 s8, 0, s7
	s_sub_i32 s2, s2, s6
	v_rcp_iflag_f32_e32 v0, v0
	s_mul_i32 s6, s2, s31
	s_sub_i32 s3, s3, s6
	s_abs_i32 s9, s3
	v_mul_f32_e32 v0, 0x4f7ffffe, v0
	v_cvt_u32_f32_e32 v0, v0
	s_xor_b32 s6, s3, s30
	s_ashr_i32 s6, s6, 31
	v_readfirstlane_b32 s10, v0
	s_mul_i32 s8, s8, s10
	s_mul_hi_u32 s8, s10, s8
	s_add_i32 s10, s10, s8
	s_mul_hi_u32 s8, s9, s10
	s_mul_i32 s10, s8, s7
	s_sub_i32 s9, s9, s10
	s_add_i32 s11, s8, 1
	s_sub_i32 s10, s9, s7
	s_cmp_ge_u32 s9, s7
	s_cselect_b32 s8, s11, s8
	s_cselect_b32 s9, s10, s9
	s_add_i32 s10, s8, 1
	s_cmp_ge_u32 s9, s7
	s_cselect_b32 s7, s10, s8
	s_xor_b32 s7, s7, s6
	s_sub_i32 s6, s7, s6
	s_mul_i32 s7, s6, s30
	s_sub_i32 s7, s3, s7
	s_mul_hi_i32 s11, s2, s28
	s_mul_i32 s3, s2, s28
	s_lshl_b32 s10, s7, 6
	s_lshl_b32 s2, s6, 7
	s_and_saveexec_b64 s[6:7], s[4:5]
	s_cbranch_execz .LBB2_81
	v_or_b32_e32 v0, s10, v37
	v_cmp_gt_i32_e32 vcc, s29, v0
	v_mov_b32_e32 v1, 0
	s_waitcnt vmcnt(5) lgkmcnt(0)
	v_mov_b32_e32 v2, 0
	v_mov_b32_e32 v3, 0
	v_mov_b32_e32 v4, 0
	v_mov_b32_e32 v5, 0
	s_waitcnt vmcnt(4)
	v_mov_b32_e32 v6, 0
	v_mov_b32_e32 v7, 0
	s_waitcnt vmcnt(3)
	v_mov_b32_e32 v8, 0
	v_mov_b32_e32 v9, 0
	v_mov_b32_e32 v10, 0
	v_mov_b32_e32 v11, 0
	s_waitcnt vmcnt(2)
	v_mov_b32_e32 v12, 0
	v_mov_b32_e32 v13, 0
	v_mov_b32_e32 v14, 0
	v_mov_b32_e32 v15, 0
	v_mov_b32_e32 v16, 0
	v_mov_b32_e32 v17, 0
	v_mov_b32_e32 v18, 0
	v_mov_b32_e32 v19, 0
	v_mov_b32_e32 v20, 0
	v_mov_b32_e32 v21, 0
	v_mov_b32_e32 v23, 0
	v_mov_b32_e32 v24, 0
	v_mov_b32_e32 v25, 0
	v_mov_b32_e32 v27, 0
	v_mov_b32_e32 v38, 0
	v_mov_b32_e32 v39, 0
	v_mov_b32_e32 v40, 0
	v_mov_b32_e32 v41, 0
	v_mov_b32_e32 v42, 0
	v_mov_b32_e32 v43, 0
	v_mov_b32_e32 v44, 0
	s_and_saveexec_b64 s[8:9], vcc
	s_cbranch_execz .LBB2_80
	s_ashr_i32 s12, s29, 31
	s_mul_hi_u32 s13, s3, s29
	s_mul_i32 s12, s3, s12
	s_add_i32 s12, s13, s12
	s_mul_i32 s13, s11, s29
	s_add_i32 s13, s12, s13
	s_mul_i32 s12, s3, s29
	s_lshl_b64 s[12:13], s[12:13], 2
	s_add_u32 s12, s20, s12
	s_addc_u32 s13, s21, s13
	v_or_b32_e32 v27, s2, v36
	v_ashrrev_i32_e32 v1, 31, v0
	v_lshl_add_u64 v[38:39], v[0:1], 2, s[12:13]
	v_mad_i64_i32 v[0:1], s[12:13], v27, s29, 0
	v_lshl_add_u64 v[10:11], v[0:1], 2, v[38:39]
	v_or_b32_e32 v0, 1, v27
	v_mad_i64_i32 v[0:1], s[12:13], v0, s29, 0
	v_lshl_add_u64 v[12:13], v[0:1], 2, v[38:39]
	v_or_b32_e32 v0, 2, v27
	v_mad_i64_i32 v[0:1], s[12:13], v0, s29, 0
	v_lshl_add_u64 v[14:15], v[0:1], 2, v[38:39]
	v_or_b32_e32 v0, 3, v27
	v_mad_i64_i32 v[0:1], s[12:13], v0, s29, 0
	v_lshl_add_u64 v[16:17], v[0:1], 2, v[38:39]
	v_or_b32_e32 v0, 4, v27
	v_mad_i64_i32 v[0:1], s[12:13], v0, s29, 0
	v_lshl_add_u64 v[18:19], v[0:1], 2, v[38:39]
	v_or_b32_e32 v0, 5, v27
	v_mad_i64_i32 v[0:1], s[12:13], v0, s29, 0
	v_lshl_add_u64 v[20:21], v[0:1], 2, v[38:39]
	v_or_b32_e32 v0, 6, v27
	v_mad_i64_i32 v[0:1], s[12:13], v0, s29, 0
	v_lshl_add_u64 v[24:25], v[0:1], 2, v[38:39]
	v_or_b32_e32 v0, 7, v27
	v_mad_i64_i32 v[0:1], s[12:13], v0, s29, 0
	v_lshl_add_u64 v[40:41], v[0:1], 2, v[38:39]
	v_or_b32_e32 v0, 8, v27
	global_load_dword v1, v[10:11], off nt
	global_load_dword v2, v[12:13], off nt
	global_load_dword v3, v[14:15], off nt
	global_load_dword v4, v[16:17], off nt
	global_load_dword v5, v[18:19], off nt
	global_load_dword v6, v[20:21], off nt
	global_load_dword v7, v[24:25], off nt
	global_load_dword v8, v[40:41], off nt
	v_mad_i64_i32 v[10:11], s[12:13], v0, s29, 0
	v_or_b32_e32 v0, 9, v27
	v_lshl_add_u64 v[18:19], v[10:11], 2, v[38:39]
	v_mad_i64_i32 v[10:11], s[12:13], v0, s29, 0
	v_or_b32_e32 v0, 10, v27
	v_lshl_add_u64 v[20:21], v[10:11], 2, v[38:39]
	v_mad_i64_i32 v[10:11], s[12:13], v0, s29, 0
	v_or_b32_e32 v0, 11, v27
	v_lshl_add_u64 v[24:25], v[10:11], 2, v[38:39]
	v_mad_i64_i32 v[10:11], s[12:13], v0, s29, 0
	v_or_b32_e32 v0, 12, v27
	v_lshl_add_u64 v[40:41], v[10:11], 2, v[38:39]
	v_mad_i64_i32 v[10:11], s[12:13], v0, s29, 0
	v_or_b32_e32 v0, 13, v27
	v_lshl_add_u64 v[42:43], v[10:11], 2, v[38:39]
	v_mad_i64_i32 v[10:11], s[12:13], v0, s29, 0
	v_or_b32_e32 v0, 14, v27
	v_lshl_add_u64 v[44:45], v[10:11], 2, v[38:39]
	v_mad_i64_i32 v[10:11], s[12:13], v0, s29, 0
	v_or_b32_e32 v0, 15, v27
	v_lshl_add_u64 v[46:47], v[10:11], 2, v[38:39]
	v_mad_i64_i32 v[10:11], s[12:13], v0, s29, 0
	v_or_b32_e32 v0, 16, v27
	v_lshl_add_u64 v[48:49], v[10:11], 2, v[38:39]
	global_load_dword v9, v[18:19], off nt
	global_load_dword v10, v[20:21], off nt
	global_load_dword v11, v[24:25], off nt
	global_load_dword v12, v[40:41], off nt
	global_load_dword v13, v[42:43], off nt
	global_load_dword v14, v[44:45], off nt
	global_load_dword v15, v[46:47], off nt
	global_load_dword v16, v[48:49], off nt
	v_mad_i64_i32 v[18:19], s[12:13], v0, s29, 0
	v_or_b32_e32 v0, 17, v27
	v_lshl_add_u64 v[40:41], v[18:19], 2, v[38:39]
	v_mad_i64_i32 v[18:19], s[12:13], v0, s29, 0
	v_or_b32_e32 v0, 18, v27
	v_lshl_add_u64 v[42:43], v[18:19], 2, v[38:39]
	v_mad_i64_i32 v[18:19], s[12:13], v0, s29, 0
	v_or_b32_e32 v0, 19, v27
	v_lshl_add_u64 v[44:45], v[18:19], 2, v[38:39]
	v_mad_i64_i32 v[18:19], s[12:13], v0, s29, 0
	v_or_b32_e32 v0, 20, v27
	v_lshl_add_u64 v[46:47], v[18:19], 2, v[38:39]
	v_mad_i64_i32 v[18:19], s[12:13], v0, s29, 0
	v_or_b32_e32 v0, 21, v27
	v_lshl_add_u64 v[48:49], v[18:19], 2, v[38:39]
	v_mad_i64_i32 v[18:19], s[12:13], v0, s29, 0
	v_or_b32_e32 v0, 22, v27
	v_lshl_add_u64 v[50:51], v[18:19], 2, v[38:39]
	v_mad_i64_i32 v[18:19], s[12:13], v0, s29, 0
	v_or_b32_e32 v0, 23, v27
	v_lshl_add_u64 v[52:53], v[18:19], 2, v[38:39]
	v_mad_i64_i32 v[18:19], s[12:13], v0, s29, 0
	v_or_b32_e32 v0, 24, v27
	v_lshl_add_u64 v[54:55], v[18:19], 2, v[38:39]
	global_load_dword v17, v[40:41], off nt
	global_load_dword v18, v[42:43], off nt
	global_load_dword v19, v[44:45], off nt
	global_load_dword v20, v[46:47], off nt
	global_load_dword v21, v[48:49], off nt
	global_load_dword v23, v[50:51], off nt
	global_load_dword v24, v[52:53], off nt
	global_load_dword v25, v[54:55], off nt
	v_mad_i64_i32 v[40:41], s[12:13], v0, s29, 0
	v_or_b32_e32 v0, 25, v27
	v_lshl_add_u64 v[46:47], v[40:41], 2, v[38:39]
	v_mad_i64_i32 v[40:41], s[12:13], v0, s29, 0
	v_or_b32_e32 v0, 26, v27
	v_lshl_add_u64 v[48:49], v[40:41], 2, v[38:39]
	v_mad_i64_i32 v[40:41], s[12:13], v0, s29, 0
	v_or_b32_e32 v0, 27, v27
	v_lshl_add_u64 v[50:51], v[40:41], 2, v[38:39]
	v_mad_i64_i32 v[40:41], s[12:13], v0, s29, 0
	v_or_b32_e32 v0, 28, v27
	v_lshl_add_u64 v[52:53], v[40:41], 2, v[38:39]
	v_mad_i64_i32 v[40:41], s[12:13], v0, s29, 0
	v_or_b32_e32 v0, 29, v27
	v_lshl_add_u64 v[54:55], v[40:41], 2, v[38:39]
	v_mad_i64_i32 v[40:41], s[12:13], v0, s29, 0
	v_or_b32_e32 v0, 30, v27
	v_lshl_add_u64 v[56:57], v[40:41], 2, v[38:39]
	v_mad_i64_i32 v[40:41], s[12:13], v0, s29, 0
	v_or_b32_e32 v0, 31, v27
	v_lshl_add_u64 v[58:59], v[40:41], 2, v[38:39]
	v_mad_i64_i32 v[40:41], s[12:13], v0, s29, 0
	v_lshl_add_u64 v[60:61], v[40:41], 2, v[38:39]
	global_load_dword v27, v[46:47], off nt
	global_load_dword v38, v[48:49], off nt
	global_load_dword v39, v[50:51], off nt
	global_load_dword v40, v[52:53], off nt
	global_load_dword v41, v[54:55], off nt
	global_load_dword v42, v[56:57], off nt
	global_load_dword v43, v[58:59], off nt
	global_load_dword v44, v[60:61], off nt

.LBB2_81:
	s_or_b64 exec, exec, s[6:7]
	s_waitcnt lgkmcnt(0)
	s_barrier
	s_and_saveexec_b64 s[6:7], s[4:5]
	s_cbranch_execz .LBB2_83
	s_ashr_i32 s8, s30, 31
	s_mul_i32 s9, s30, s11
	s_mul_hi_u32 s11, s30, s3
	s_add_i32 s9, s11, s9
	s_mul_i32 s8, s8, s3
	s_add_i32 s9, s9, s8
	s_mul_i32 s8, s30, s3
	s_lshl_b64 s[8:9], s[8:9], 7
	s_add_u32 s8, s22, s8
	s_addc_u32 s9, s23, s9
	s_ashr_i32 s3, s2, 31
	s_lshl_b64 s[2:3], s[2:3], 1
	s_add_u32 s2, s8, s2
	s_addc_u32 s3, s9, s3
	v_lshlrev_b32_e32 v0, 1, v26
	v_mov_b32_e32 v1, 0
	s_waitcnt vmcnt(3)
	v_lshl_add_u64 v[8:9], s[2:3], 0, v[0:1]
	ds_read_b128 v[0:3], v34
	v_or_b32_e32 v4, s10, v22
	v_mad_i64_i32 v[4:5], s[2:3], v4, s28, 0
	v_lshl_add_u64 v[10:11], v[4:5], 1, v[8:9]
	ds_read_b128 v[4:7], v33
	s_waitcnt lgkmcnt(1)
	global_store_dwordx4 v[10:11], v[0:3], off sc1
	s_nop 1
	v_or_b32_e32 v0, s10, v30
	v_mad_i64_i32 v[0:1], s[2:3], v0, s28, 0
	v_lshl_add_u64 v[0:1], v[0:1], 1, v[8:9]
	s_waitcnt lgkmcnt(0)
	global_store_dwordx4 v[0:1], v[4:7], off sc1
	ds_read_b128 v[0:3], v32
	s_nop 0
	v_or_b32_e32 v4, s10, v29
	v_mad_i64_i32 v[4:5], s[2:3], v4, s28, 0
	v_lshl_add_u64 v[10:11], v[4:5], 1, v[8:9]
	ds_read_b128 v[4:7], v31
	s_waitcnt lgkmcnt(1)
	global_store_dwordx4 v[10:11], v[0:3], off sc1
	s_nop 1
	v_or_b32_e32 v0, s10, v28
	v_mad_i64_i32 v[0:1], s[2:3], v0, s28, 0
	v_lshl_add_u64 v[0:1], v[0:1], 1, v[8:9]
	s_waitcnt lgkmcnt(0)
	global_store_dwordx4 v[0:1], v[4:7], off sc1

.LBB2_86:
	s_cmp_lt_i32 s40, s34
	s_cselect_b64 s[2:3], -1, 0
	s_and_b64 s[0:1], s[0:1], s[2:3]
	s_andn2_b64 vcc, exec, s[0:1]
	s_cbranch_vccnz .LBB2_34
	s_abs_i32 s0, s27
	v_cvt_f32_u32_e32 v0, s0
	s_sub_i32 s6, 0, s0
	s_add_i32 s1, s40, s35
	s_abs_i32 s3, s1
	v_rcp_iflag_f32_e32 v0, v0
	s_xor_b32 s2, s1, s27
	s_ashr_i32 s2, s2, 31
	v_mul_f32_e32 v0, 0x4f7ffffe, v0
	v_cvt_u32_f32_e32 v0, v0
	s_nop 0
	v_readfirstlane_b32 s7, v0
	s_mul_i32 s6, s6, s7
	s_mul_hi_u32 s6, s7, s6
	s_add_i32 s7, s7, s6
	s_mul_hi_u32 s6, s3, s7
	s_mul_i32 s7, s6, s0
	s_sub_i32 s3, s3, s7
	s_add_i32 s8, s6, 1
	s_sub_i32 s7, s3, s0
	s_cmp_ge_u32 s3, s0
	s_cselect_b32 s6, s8, s6
	s_cselect_b32 s3, s7, s3
	s_add_i32 s7, s6, 1
	s_cmp_ge_u32 s3, s0
	s_cselect_b32 s0, s7, s6
	s_abs_i32 s3, s26
	v_cvt_f32_u32_e32 v0, s3
	s_xor_b32 s0, s0, s2
	s_sub_i32 s6, 0, s3
	s_sub_i32 s0, s0, s2
	v_rcp_iflag_f32_e32 v0, v0
	s_mul_i32 s2, s0, s27
	s_sub_i32 s1, s1, s2
	s_abs_i32 s7, s1
	v_mul_f32_e32 v0, 0x4f7ffffe, v0
	v_cvt_u32_f32_e32 v0, v0
	s_xor_b32 s2, s1, s26
	s_ashr_i32 s2, s2, 31
	v_readfirstlane_b32 s8, v0
	s_mul_i32 s6, s6, s8
	s_mul_hi_u32 s6, s8, s6
	s_add_i32 s8, s8, s6
	s_mul_hi_u32 s6, s7, s8
	s_mul_i32 s8, s6, s3
	s_sub_i32 s7, s7, s8
	s_add_i32 s9, s6, 1
	s_sub_i32 s8, s7, s3
	s_cmp_ge_u32 s7, s3
	s_cselect_b32 s6, s9, s6
	s_cselect_b32 s7, s8, s7
	s_add_i32 s8, s6, 1
	s_cmp_ge_u32 s7, s3
	s_cselect_b32 s3, s8, s6
	s_xor_b32 s3, s3, s2
	s_sub_i32 s2, s3, s2
	s_mul_i32 s3, s2, s26
	s_sub_i32 s3, s1, s3
	s_mul_hi_i32 s9, s0, s24
	s_mul_i32 s1, s0, s24
	s_lshl_b32 s8, s3, 6
	s_lshl_b32 s0, s2, 7
	s_and_saveexec_b64 s[2:3], s[4:5]
	s_cbranch_execz .LBB2_91
	v_or_b32_e32 v0, s8, v37
	v_cmp_gt_i32_e32 vcc, s25, v0
	v_mov_b32_e32 v1, 0
	s_waitcnt vmcnt(5) lgkmcnt(0)
	v_mov_b32_e32 v2, 0
	v_mov_b32_e32 v3, 0
	v_mov_b32_e32 v4, 0
	v_mov_b32_e32 v5, 0
	s_waitcnt vmcnt(4)
	v_mov_b32_e32 v6, 0
	v_mov_b32_e32 v7, 0
	s_waitcnt vmcnt(3)
	v_mov_b32_e32 v8, 0
	v_mov_b32_e32 v9, 0
	v_mov_b32_e32 v10, 0
	v_mov_b32_e32 v11, 0
	s_waitcnt vmcnt(2)
	v_mov_b32_e32 v12, 0
	v_mov_b32_e32 v13, 0
	v_mov_b32_e32 v14, 0
	v_mov_b32_e32 v15, 0
	v_mov_b32_e32 v16, 0
	v_mov_b32_e32 v17, 0
	v_mov_b32_e32 v18, 0
	v_mov_b32_e32 v19, 0
	v_mov_b32_e32 v20, 0
	v_mov_b32_e32 v21, 0
	v_mov_b32_e32 v23, 0
	v_mov_b32_e32 v24, 0
	v_mov_b32_e32 v25, 0
	v_mov_b32_e32 v27, 0
	v_mov_b32_e32 v37, 0
	v_mov_b32_e32 v38, 0
	v_mov_b32_e32 v39, 0
	v_mov_b32_e32 v40, 0
	v_mov_b32_e32 v41, 0
	v_mov_b32_e32 v42, 0
	v_mov_b32_e32 v43, 0
	s_and_saveexec_b64 s[6:7], vcc
	s_cbranch_execz .LBB2_90
	s_ashr_i32 s10, s25, 31
	s_mul_hi_u32 s11, s1, s25
	s_mul_i32 s10, s1, s10
	s_add_i32 s10, s11, s10
	s_mul_i32 s11, s9, s25
	s_add_i32 s11, s10, s11
	s_mul_i32 s10, s1, s25
	s_lshl_b64 s[10:11], s[10:11], 2
	s_add_u32 s10, s16, s10
	s_addc_u32 s11, s17, s11
	v_or_b32_e32 v27, s0, v36
	v_ashrrev_i32_e32 v1, 31, v0
	v_lshl_add_u64 v[36:37], v[0:1], 2, s[10:11]
	v_mad_i64_i32 v[0:1], s[10:11], v27, s25, 0
	v_lshl_add_u64 v[10:11], v[0:1], 2, v[36:37]
	v_or_b32_e32 v0, 1, v27
	v_mad_i64_i32 v[0:1], s[10:11], v0, s25, 0
	v_lshl_add_u64 v[12:13], v[0:1], 2, v[36:37]
	v_or_b32_e32 v0, 2, v27
	v_mad_i64_i32 v[0:1], s[10:11], v0, s25, 0
	v_lshl_add_u64 v[14:15], v[0:1], 2, v[36:37]
	v_or_b32_e32 v0, 3, v27
	v_mad_i64_i32 v[0:1], s[10:11], v0, s25, 0
	v_lshl_add_u64 v[16:17], v[0:1], 2, v[36:37]
	v_or_b32_e32 v0, 4, v27
	v_mad_i64_i32 v[0:1], s[10:11], v0, s25, 0
	v_lshl_add_u64 v[18:19], v[0:1], 2, v[36:37]
	v_or_b32_e32 v0, 5, v27
	v_mad_i64_i32 v[0:1], s[10:11], v0, s25, 0
	v_lshl_add_u64 v[20:21], v[0:1], 2, v[36:37]
	v_or_b32_e32 v0, 6, v27
	v_mad_i64_i32 v[0:1], s[10:11], v0, s25, 0
	v_lshl_add_u64 v[24:25], v[0:1], 2, v[36:37]
	v_or_b32_e32 v0, 7, v27
	v_mad_i64_i32 v[0:1], s[10:11], v0, s25, 0
	v_lshl_add_u64 v[38:39], v[0:1], 2, v[36:37]
	v_or_b32_e32 v0, 8, v27
	global_load_dword v1, v[10:11], off nt
	global_load_dword v2, v[12:13], off nt
	global_load_dword v3, v[14:15], off nt
	global_load_dword v4, v[16:17], off nt
	global_load_dword v5, v[18:19], off nt
	global_load_dword v6, v[20:21], off nt
	global_load_dword v7, v[24:25], off nt
	global_load_dword v8, v[38:39], off nt
	v_mad_i64_i32 v[10:11], s[10:11], v0, s25, 0
	v_or_b32_e32 v0, 9, v27
	v_lshl_add_u64 v[18:19], v[10:11], 2, v[36:37]
	v_mad_i64_i32 v[10:11], s[10:11], v0, s25, 0
	v_or_b32_e32 v0, 10, v27
	v_lshl_add_u64 v[20:21], v[10:11], 2, v[36:37]
	v_mad_i64_i32 v[10:11], s[10:11], v0, s25, 0
	v_or_b32_e32 v0, 11, v27
	v_lshl_add_u64 v[24:25], v[10:11], 2, v[36:37]
	v_mad_i64_i32 v[10:11], s[10:11], v0, s25, 0
	v_or_b32_e32 v0, 12, v27
	v_lshl_add_u64 v[38:39], v[10:11], 2, v[36:37]
	v_mad_i64_i32 v[10:11], s[10:11], v0, s25, 0
	v_or_b32_e32 v0, 13, v27
	v_lshl_add_u64 v[40:41], v[10:11], 2, v[36:37]
	v_mad_i64_i32 v[10:11], s[10:11], v0, s25, 0
	v_or_b32_e32 v0, 14, v27
	v_lshl_add_u64 v[42:43], v[10:11], 2, v[36:37]
	v_mad_i64_i32 v[10:11], s[10:11], v0, s25, 0
	v_or_b32_e32 v0, 15, v27
	v_lshl_add_u64 v[44:45], v[10:11], 2, v[36:37]
	v_mad_i64_i32 v[10:11], s[10:11], v0, s25, 0
	v_or_b32_e32 v0, 16, v27
	v_lshl_add_u64 v[46:47], v[10:11], 2, v[36:37]
	global_load_dword v9, v[18:19], off nt
	global_load_dword v10, v[20:21], off nt
	global_load_dword v11, v[24:25], off nt
	global_load_dword v12, v[38:39], off nt
	global_load_dword v13, v[40:41], off nt
	global_load_dword v14, v[42:43], off nt
	global_load_dword v15, v[44:45], off nt
	global_load_dword v16, v[46:47], off nt
	v_mad_i64_i32 v[18:19], s[10:11], v0, s25, 0
	v_or_b32_e32 v0, 17, v27
	v_lshl_add_u64 v[38:39], v[18:19], 2, v[36:37]
	v_mad_i64_i32 v[18:19], s[10:11], v0, s25, 0
	v_or_b32_e32 v0, 18, v27
	v_lshl_add_u64 v[40:41], v[18:19], 2, v[36:37]
	v_mad_i64_i32 v[18:19], s[10:11], v0, s25, 0
	v_or_b32_e32 v0, 19, v27
	v_lshl_add_u64 v[42:43], v[18:19], 2, v[36:37]
	v_mad_i64_i32 v[18:19], s[10:11], v0, s25, 0
	v_or_b32_e32 v0, 20, v27
	v_lshl_add_u64 v[44:45], v[18:19], 2, v[36:37]
	v_mad_i64_i32 v[18:19], s[10:11], v0, s25, 0
	v_or_b32_e32 v0, 21, v27
	v_lshl_add_u64 v[46:47], v[18:19], 2, v[36:37]
	v_mad_i64_i32 v[18:19], s[10:11], v0, s25, 0
	v_or_b32_e32 v0, 22, v27
	v_lshl_add_u64 v[48:49], v[18:19], 2, v[36:37]
	v_mad_i64_i32 v[18:19], s[10:11], v0, s25, 0
	v_or_b32_e32 v0, 23, v27
	v_lshl_add_u64 v[50:51], v[18:19], 2, v[36:37]
	v_mad_i64_i32 v[18:19], s[10:11], v0, s25, 0
	v_or_b32_e32 v0, 24, v27
	v_lshl_add_u64 v[52:53], v[18:19], 2, v[36:37]
	global_load_dword v17, v[38:39], off nt
	global_load_dword v18, v[40:41], off nt
	global_load_dword v19, v[42:43], off nt
	global_load_dword v20, v[44:45], off nt
	global_load_dword v21, v[46:47], off nt
	global_load_dword v23, v[48:49], off nt
	global_load_dword v24, v[50:51], off nt
	global_load_dword v25, v[52:53], off nt
	v_mad_i64_i32 v[38:39], s[10:11], v0, s25, 0
	v_or_b32_e32 v0, 25, v27
	v_lshl_add_u64 v[44:45], v[38:39], 2, v[36:37]
	v_mad_i64_i32 v[38:39], s[10:11], v0, s25, 0
	v_or_b32_e32 v0, 26, v27
	v_lshl_add_u64 v[46:47], v[38:39], 2, v[36:37]
	v_mad_i64_i32 v[38:39], s[10:11], v0, s25, 0
	v_or_b32_e32 v0, 27, v27
	v_lshl_add_u64 v[48:49], v[38:39], 2, v[36:37]
	v_mad_i64_i32 v[38:39], s[10:11], v0, s25, 0
	v_or_b32_e32 v0, 28, v27
	v_lshl_add_u64 v[50:51], v[38:39], 2, v[36:37]
	v_mad_i64_i32 v[38:39], s[10:11], v0, s25, 0
	v_or_b32_e32 v0, 29, v27
	v_lshl_add_u64 v[52:53], v[38:39], 2, v[36:37]
	v_mad_i64_i32 v[38:39], s[10:11], v0, s25, 0
	v_or_b32_e32 v0, 30, v27
	v_lshl_add_u64 v[54:55], v[38:39], 2, v[36:37]
	v_mad_i64_i32 v[38:39], s[10:11], v0, s25, 0
	v_or_b32_e32 v0, 31, v27
	v_lshl_add_u64 v[56:57], v[38:39], 2, v[36:37]
	v_mad_i64_i32 v[38:39], s[10:11], v0, s25, 0
	v_lshl_add_u64 v[58:59], v[38:39], 2, v[36:37]
	global_load_dword v27, v[44:45], off nt
	global_load_dword v37, v[46:47], off nt
	global_load_dword v38, v[48:49], off nt
	global_load_dword v39, v[50:51], off nt
	global_load_dword v40, v[52:53], off nt
	global_load_dword v41, v[54:55], off nt
	global_load_dword v42, v[56:57], off nt
	global_load_dword v43, v[58:59], off nt

.LBB2_91:
	s_or_b64 exec, exec, s[2:3]
	s_waitcnt lgkmcnt(0)
	s_barrier
	s_and_saveexec_b64 s[2:3], s[4:5]
	s_cbranch_execz .LBB2_34
	s_ashr_i32 s2, s26, 31
	s_mul_i32 s3, s26, s9
	s_mul_hi_u32 s4, s26, s1
	s_add_i32 s3, s4, s3
	s_mul_i32 s2, s2, s1
	s_add_i32 s3, s3, s2
	s_mul_i32 s2, s26, s1
	s_lshl_b64 s[2:3], s[2:3], 7
	s_add_u32 s2, s18, s2
	s_addc_u32 s3, s19, s3
	s_ashr_i32 s1, s0, 31
	s_lshl_b64 s[0:1], s[0:1], 1
	s_add_u32 s0, s2, s0
	s_addc_u32 s1, s3, s1
	v_lshlrev_b32_e32 v0, 1, v26
	v_mov_b32_e32 v1, 0
	s_waitcnt vmcnt(3)
	v_lshl_add_u64 v[8:9], s[0:1], 0, v[0:1]
	ds_read_b128 v[0:3], v34
	v_or_b32_e32 v4, s8, v22
	v_mad_i64_i32 v[4:5], s[0:1], v4, s24, 0
	v_lshl_add_u64 v[10:11], v[4:5], 1, v[8:9]
	ds_read_b128 v[4:7], v33
	s_waitcnt lgkmcnt(1)
	global_store_dwordx4 v[10:11], v[0:3], off sc1
	s_nop 1
	v_or_b32_e32 v0, s8, v30
	v_mad_i64_i32 v[0:1], s[0:1], v0, s24, 0
	v_lshl_add_u64 v[0:1], v[0:1], 1, v[8:9]
	s_waitcnt lgkmcnt(0)
	global_store_dwordx4 v[0:1], v[4:7], off sc1
	ds_read_b128 v[0:3], v32
	s_nop 0
	v_or_b32_e32 v4, s8, v29
	v_mad_i64_i32 v[4:5], s[0:1], v4, s24, 0
	v_lshl_add_u64 v[10:11], v[4:5], 1, v[8:9]
	ds_read_b128 v[4:7], v31
	s_waitcnt lgkmcnt(1)
	global_store_dwordx4 v[10:11], v[0:3], off sc1
	s_nop 1
	v_or_b32_e32 v0, s8, v28
	v_mad_i64_i32 v[0:1], s[0:1], v0, s24, 0
	v_lshl_add_u64 v[0:1], v[0:1], 1, v[8:9]
	s_waitcnt lgkmcnt(0)
	global_store_dwordx4 v[0:1], v[4:7], off sc1
	s_endpgm

_Z9ln_kernelPKfS0_S0_PDF16_7ConvJob:
	s_cmpk_lt_u32 s2, 0x200
	s_mov_b64 s[4:5], -1
	s_cbranch_scc0 .LBB3_2
	s_load_dwordx8 s[4:11], s[0:1], 0x0
	v_lshrrev_b32_e32 v1, 6, v0
	v_lshl_or_b32 v1, s2, 2, v1
	s_movk_i32 s3, 0xc00
	v_lshlrev_b32_e32 v4, 2, v0
	v_mul_lo_u32 v38, v1, s3
	v_mov_b32_e32 v39, 0
	v_and_b32_e32 v52, 0xfc, v4
	s_waitcnt lgkmcnt(0)
	v_lshl_add_u64 v[2:3], s[4:5], 0, v[38:39]
	v_lshlrev_b32_e32 v38, 2, v52
	v_lshl_add_u64 v[14:15], v[2:3], 0, v[38:39]
	global_load_dwordx4 v[2:5], v[14:15], off offset:1024
	global_load_dwordx4 v[6:9], v[14:15], off offset:2048
	global_load_dwordx4 v[10:13], v[14:15], off
	v_mbcnt_lo_u32_b32 v14, -1, 0
	v_mbcnt_hi_u32_b32 v22, -1, v14
	v_and_b32_e32 v14, 64, v22
	v_xor_b32_e32 v15, 32, v22
	v_add_u32_e32 v24, 64, v14
	v_cmp_lt_i32_e32 vcc, v15, v24
	v_xor_b32_e32 v23, 16, v22
	s_movk_i32 s3, 0x600
	v_cndmask_b32_e32 v14, v22, v15, vcc
	v_lshlrev_b32_e32 v53, 2, v14
	v_cmp_lt_i32_e32 vcc, v23, v24
	s_mov_b32 s4, 0x800000
	s_waitcnt vmcnt(2)
	v_mov_b32_e32 v14, v2
	s_waitcnt vmcnt(1)
	v_mov_b32_e32 v15, v6
	v_mov_b32_e32 v16, v3
	v_mov_b32_e32 v17, v7
	s_waitcnt vmcnt(0)
	v_add_f32_e32 v25, v10, v11
	v_mov_b32_e32 v18, v4
	v_mov_b32_e32 v19, v8
	v_pk_add_f32 v[14:15], v[14:15], v[16:17]
	v_add_f32_e32 v16, v25, v12
	v_mov_b32_e32 v20, v5
	v_mov_b32_e32 v21, v9
	v_pk_add_f32 v[14:15], v[14:15], v[18:19]
	v_add_f32_e32 v16, v16, v13
	v_pk_add_f32 v[14:15], v[14:15], v[20:21]
	v_add_f32_e32 v16, 0, v16
	v_add_f32_e32 v14, v16, v14
	v_add_f32_e32 v14, v14, v15
	ds_bpermute_b32 v15, v53, v14
	v_cndmask_b32_e32 v17, v22, v23, vcc
	v_lshlrev_b32_e32 v54, 2, v17
	v_xor_b32_e32 v16, 8, v22
	v_cmp_lt_i32_e32 vcc, v16, v24
	s_waitcnt lgkmcnt(0)
	v_add_f32_e32 v14, v14, v15
	ds_bpermute_b32 v15, v54, v14
	v_cndmask_b32_e32 v16, v22, v16, vcc
	v_lshlrev_b32_e32 v55, 2, v16
	v_xor_b32_e32 v17, 4, v22
	v_cmp_lt_i32_e32 vcc, v17, v24
	s_waitcnt lgkmcnt(0)
	v_add_f32_e32 v14, v14, v15
	ds_bpermute_b32 v15, v55, v14
	v_cndmask_b32_e32 v17, v22, v17, vcc
	v_lshlrev_b32_e32 v56, 2, v17
	v_xor_b32_e32 v16, 2, v22
	v_cmp_lt_i32_e32 vcc, v16, v24
	s_waitcnt lgkmcnt(0)
	v_add_f32_e32 v14, v14, v15
	ds_bpermute_b32 v15, v56, v14
	v_cndmask_b32_e32 v16, v22, v16, vcc
	v_lshlrev_b32_e32 v57, 2, v16
	v_xor_b32_e32 v17, 1, v22
	v_cmp_lt_i32_e32 vcc, v17, v24
	s_waitcnt lgkmcnt(0)
	v_add_f32_e32 v23, v14, v15
	ds_bpermute_b32 v25, v57, v23
	v_cndmask_b32_e32 v14, v22, v17, vcc
	v_lshlrev_b32_e32 v58, 2, v14
	global_load_dwordx4 v[14:17], v38, s[6:7]
	global_load_dwordx4 v[18:21], v38, s[8:9]
	s_waitcnt lgkmcnt(0)
	v_add_f32_e32 v40, v23, v25
	global_load_dwordx4 v[22:25], v38, s[6:7] offset:1024
	global_load_dwordx4 v[26:29], v38, s[8:9] offset:1024
	global_load_dwordx4 v[30:33], v38, s[6:7] offset:2048
	global_load_dwordx4 v[34:37], v38, s[8:9] offset:2048
	ds_bpermute_b32 v41, v58, v40
	s_waitcnt lgkmcnt(0)
	v_add_f32_e32 v38, v40, v41
	v_mul_f32_e32 v38, 0x3aaaaaab, v38
	v_pk_add_f32 v[10:11], v[10:11], v[38:39] op_sel_hi:[1,0] neg_lo:[0,1] neg_hi:[0,1]
	v_pk_add_f32 v[6:7], v[6:7], v[38:39] op_sel_hi:[1,0] neg_lo:[0,1] neg_hi:[0,1]
	v_pk_add_f32 v[2:3], v[2:3], v[38:39] op_sel_hi:[1,0] neg_lo:[0,1] neg_hi:[0,1]
	v_mov_b32_e32 v46, v7
	v_mov_b32_e32 v47, v11
	v_pk_add_f32 v[12:13], v[12:13], v[38:39] op_sel_hi:[1,0] neg_lo:[0,1] neg_hi:[0,1]
	v_pk_add_f32 v[4:5], v[4:5], v[38:39] op_sel_hi:[1,0] neg_lo:[0,1] neg_hi:[0,1]
	v_pk_add_f32 v[8:9], v[8:9], v[38:39] op_sel_hi:[1,0] neg_lo:[0,1] neg_hi:[0,1]
	v_pk_mul_f32 v[40:41], v[2:3], v[2:3]
	v_mov_b32_e32 v44, v6
	v_mov_b32_e32 v45, v10
	v_pk_mul_f32 v[46:47], v[46:47], v[46:47]
	v_pk_mul_f32 v[42:43], v[4:5], v[4:5]
	v_mov_b32_e32 v48, v8
	v_mov_b32_e32 v49, v12
	v_add_f32_e32 v38, v40, v41
	v_pk_fma_f32 v[40:41], v[44:45], v[44:45], v[46:47]
	v_mov_b32_e32 v50, v9
	v_mov_b32_e32 v51, v13
	v_add_f32_e32 v38, v42, v38
	v_pk_fma_f32 v[40:41], v[48:49], v[48:49], v[40:41]
	v_add_f32_e32 v38, v43, v38
	v_pk_fma_f32 v[40:41], v[50:51], v[50:51], v[40:41]
	v_mov_b32_e32 v42, 0x3727c5ac
	v_add_f32_e32 v38, v41, v38
	v_add_f32_e32 v38, v40, v38
	ds_bpermute_b32 v40, v53, v38
	v_mov_b32_e32 v41, v39
	s_waitcnt lgkmcnt(0)
	v_add_f32_e32 v38, v38, v40
	ds_bpermute_b32 v40, v54, v38
	s_waitcnt lgkmcnt(0)
	v_add_f32_e32 v38, v38, v40
	ds_bpermute_b32 v40, v55, v38
	s_waitcnt lgkmcnt(0)
	v_add_f32_e32 v38, v38, v40
	ds_bpermute_b32 v40, v56, v38
	s_waitcnt lgkmcnt(0)
	v_add_f32_e32 v38, v38, v40
	ds_bpermute_b32 v40, v57, v38
	s_waitcnt lgkmcnt(0)
	v_add_f32_e32 v38, v38, v40
	ds_bpermute_b32 v43, v58, v38
	v_mul_lo_u32 v40, v1, s3
	v_lshl_add_u64 v[40:41], s[10:11], 0, v[40:41]
	s_waitcnt lgkmcnt(0)
	v_add_f32_e32 v1, v38, v43
	v_fmac_f32_e32 v42, 0x3aaaaaab, v1
	v_mul_f32_e32 v1, 0x4b800000, v42
	v_cmp_gt_f32_e32 vcc, s4, v42
	v_lshlrev_b32_e32 v38, 1, v52
	v_lshl_add_u64 v[38:39], v[40:41], 0, v[38:39]
	v_cndmask_b32_e32 v1, v42, v1, vcc
	v_rsq_f32_e32 v1, v1
	s_mov_b64 s[4:5], 0
	v_mul_f32_e32 v40, 0x45800000, v1
	v_cndmask_b32_e32 v40, v1, v40, vcc
	v_pk_mul_f32 v[10:11], v[10:11], v[40:41] op_sel_hi:[1,0]
	v_pk_mul_f32 v[12:13], v[12:13], v[40:41] op_sel_hi:[1,0]
	v_pk_mul_f32 v[2:3], v[2:3], v[40:41] op_sel_hi:[1,0]
	v_pk_mul_f32 v[4:5], v[4:5], v[40:41] op_sel_hi:[1,0]
	v_pk_mul_f32 v[6:7], v[6:7], v[40:41] op_sel_hi:[1,0]
	v_pk_mul_f32 v[8:9], v[8:9], v[40:41] op_sel_hi:[1,0]
	s_waitcnt vmcnt(4)
	v_pk_fma_f32 v[10:11], v[14:15], v[10:11], v[18:19]
	v_pk_fma_f32 v[12:13], v[16:17], v[12:13], v[20:21]
	s_waitcnt vmcnt(2)
	v_pk_fma_f32 v[2:3], v[22:23], v[2:3], v[26:27]
	v_pk_fma_f32 v[4:5], v[24:25], v[4:5], v[28:29]
	s_waitcnt vmcnt(0)
	v_pk_fma_f32 v[6:7], v[6:7], v[30:31], v[34:35]
	v_pk_fma_f32 v[8:9], v[8:9], v[32:33], v[36:37]
	v_cvt_pk_f16_f32 v10, v10, v11
	v_cvt_pk_f16_f32 v11, v12, v13
	v_cvt_pk_f16_f32 v2, v2, v3
	v_cvt_pk_f16_f32 v3, v4, v5
	v_cvt_pk_f16_f32 v4, v6, v7
	v_cvt_pk_f16_f32 v5, v8, v9
	global_store_dwordx2 v[38:39], v[10:11], off sc1
	global_store_dwordx2 v[38:39], v[2:3], off offset:512 sc1
	global_store_dwordx2 v[38:39], v[4:5], off offset:1024 sc1

.LBB4_12:
	s_load_dwordx16 s[8:23], s[0:1], 0xd8
	v_mad_u32_u24 v35, v37, s46, v3
	v_lshl_add_u32 v34, v4, 1, v2
	v_lshl_add_u32 v33, v5, 1, v2
	v_lshl_add_u32 v32, v6, 1, v2
	s_andn2_b64 vcc, exec, s[44:45]
	v_lshl_add_u32 v31, v1, 1, v2
	s_cbranch_vccnz .LBB4_36
	s_load_dwordx4 s[44:47], s[0:1], 0x20
	s_load_dwordx4 s[48:51], s[60:61], 0x0
	s_add_i32 s60, s7, s33
	s_abs_i32 s7, s60
	s_waitcnt lgkmcnt(0)
	s_abs_i32 s6, s47
	v_cvt_f32_u32_e32 v1, s6
	s_sub_i32 s62, 0, s6
	s_xor_b32 s61, s60, s47
	s_ashr_i32 s61, s61, 31
	v_rcp_iflag_f32_e32 v1, v1
	s_nop 0
	v_mul_f32_e32 v1, 0x4f7ffffe, v1
	v_cvt_u32_f32_e32 v1, v1
	s_nop 0
	v_readfirstlane_b32 s63, v1
	s_mul_i32 s62, s62, s63
	s_mul_hi_u32 s62, s63, s62
	s_add_i32 s63, s63, s62
	s_mul_hi_u32 s62, s7, s63
	s_mul_i32 s63, s62, s6
	s_sub_i32 s7, s7, s63
	s_add_i32 s64, s62, 1
	s_sub_i32 s63, s7, s6
	s_cmp_ge_u32 s7, s6
	s_cselect_b32 s62, s64, s62
	s_cselect_b32 s7, s63, s7
	s_add_i32 s63, s62, 1
	s_cmp_ge_u32 s7, s6
	s_cselect_b32 s6, s63, s62
	s_abs_i32 s62, s46
	v_cvt_f32_u32_e32 v1, s62
	s_xor_b32 s6, s6, s61
	s_sub_i32 s63, 0, s62
	s_sub_i32 s7, s6, s61
	v_rcp_iflag_f32_e32 v1, v1
	s_mul_i32 s6, s7, s47
	s_sub_i32 s6, s60, s6
	s_abs_i32 s61, s6
	v_mul_f32_e32 v1, 0x4f7ffffe, v1
	v_cvt_u32_f32_e32 v1, v1
	s_xor_b32 s60, s6, s46
	s_ashr_i32 s60, s60, 31
	s_mul_hi_i32 s47, s7, s44
	v_readfirstlane_b32 s64, v1
	s_mul_i32 s63, s63, s64
	s_mul_hi_u32 s63, s64, s63
	s_add_i32 s64, s64, s63
	s_mul_hi_u32 s63, s61, s64
	s_mul_i32 s64, s63, s62
	s_sub_i32 s61, s61, s64
	s_add_i32 s65, s63, 1
	s_sub_i32 s64, s61, s62
	s_cmp_ge_u32 s61, s62
	s_cselect_b32 s63, s65, s63
	s_cselect_b32 s61, s64, s61
	s_add_i32 s64, s63, 1
	s_cmp_ge_u32 s61, s62
	s_cselect_b32 s61, s64, s63
	s_xor_b32 s61, s61, s60
	s_sub_i32 s61, s61, s60
	s_mul_i32 s60, s61, s46
	s_sub_i32 s6, s6, s60
	s_mul_i32 s7, s7, s44
	s_ashr_i32 s66, s45, 31
	s_lshl_b32 s60, s6, 6
	s_lshl_b32 s6, s61, 7
	s_and_saveexec_b64 s[62:63], s[2:3]
	s_cbranch_execz .LBB4_17
	v_or_b32_e32 v2, s60, v37
	v_cmp_gt_i32_e32 vcc, s45, v2
	v_mov_b32_e32 v1, 0
	v_mov_b32_e32 v3, 0
	v_mov_b32_e32 v4, 0
	v_mov_b32_e32 v5, 0
	v_mov_b32_e32 v6, 0
	v_mov_b32_e32 v7, 0
	v_mov_b32_e32 v8, 0
	v_mov_b32_e32 v9, 0
	v_mov_b32_e32 v10, 0
	v_mov_b32_e32 v11, 0
	v_mov_b32_e32 v12, 0
	v_mov_b32_e32 v13, 0
	s_waitcnt vmcnt(3)
	v_mov_b32_e32 v14, 0
	v_mov_b32_e32 v15, 0
	v_mov_b32_e32 v16, 0
	v_mov_b32_e32 v17, 0
	s_waitcnt vmcnt(2)
	v_mov_b32_e32 v18, 0
	v_mov_b32_e32 v19, 0
	v_mov_b32_e32 v20, 0
	v_mov_b32_e32 v21, 0
	s_waitcnt vmcnt(1)
	v_mov_b32_e32 v22, 0
	v_mov_b32_e32 v23, 0
	v_mov_b32_e32 v24, 0
	v_mov_b32_e32 v25, 0
	v_mov_b32_e32 v27, 0
	v_mov_b32_e32 v39, 0
	v_mov_b32_e32 v40, 0
	v_mov_b32_e32 v41, 0
	v_mov_b32_e32 v42, 0
	v_mov_b32_e32 v43, 0
	v_mov_b32_e32 v44, 0
	v_mov_b32_e32 v45, 0
	s_and_saveexec_b64 s[64:65], vcc
	s_cbranch_execz .LBB4_16
	s_mul_i32 s66, s7, s66
	s_mul_hi_u32 s67, s7, s45
	s_add_i32 s66, s67, s66
	s_mul_i32 s67, s47, s45
	s_add_i32 s67, s66, s67
	s_mul_i32 s66, s7, s45
	s_lshl_b64 s[66:67], s[66:67], 2
	s_add_u32 s48, s48, s66
	v_or_b32_e32 v27, s6, v36
	s_addc_u32 s49, s49, s67
	v_ashrrev_i32_e32 v3, 31, v2
	v_or_b32_e32 v1, 1, v27
	v_lshl_add_u64 v[40:41], v[2:3], 2, s[48:49]
	v_mad_i64_i32 v[4:5], s[48:49], v1, s45, 0
	v_or_b32_e32 v1, 2, v27
	v_mad_i64_i32 v[6:7], s[48:49], v1, s45, 0
	v_or_b32_e32 v1, 3, v27
	v_mad_i64_i32 v[8:9], s[48:49], v1, s45, 0
	v_or_b32_e32 v1, 4, v27
	v_mad_i64_i32 v[10:11], s[48:49], v1, s45, 0
	v_or_b32_e32 v1, 5, v27
	v_mad_i64_i32 v[12:13], s[48:49], v1, s45, 0
	v_or_b32_e32 v1, 6, v27
	v_mad_i64_i32 v[2:3], s[48:49], v27, s45, 0
	v_mad_i64_i32 v[14:15], s[48:49], v1, s45, 0
	v_or_b32_e32 v1, 7, v27
	v_lshl_add_u64 v[2:3], v[2:3], 2, v[40:41]
	v_lshl_add_u64 v[4:5], v[4:5], 2, v[40:41]
	v_lshl_add_u64 v[6:7], v[6:7], 2, v[40:41]
	v_lshl_add_u64 v[8:9], v[8:9], 2, v[40:41]
	v_mad_i64_i32 v[16:17], s[48:49], v1, s45, 0
	v_lshl_add_u64 v[10:11], v[10:11], 2, v[40:41]
	v_lshl_add_u64 v[12:13], v[12:13], 2, v[40:41]
	v_lshl_add_u64 v[14:15], v[14:15], 2, v[40:41]
	v_lshl_add_u64 v[16:17], v[16:17], 2, v[40:41]
	global_load_dword v1, v[2:3], off nt
	s_nop 0
	global_load_dword v3, v[4:5], off nt
	s_nop 0
	global_load_dword v4, v[6:7], off nt
	global_load_dword v5, v[8:9], off nt
	s_nop 0
	global_load_dword v6, v[10:11], off nt
	global_load_dword v7, v[12:13], off nt
	global_load_dword v8, v[14:15], off nt
	global_load_dword v9, v[16:17], off nt
	v_or_b32_e32 v2, 8, v27
	v_mad_i64_i32 v[10:11], s[48:49], v2, s45, 0
	v_or_b32_e32 v2, 9, v27
	v_mad_i64_i32 v[12:13], s[48:49], v2, s45, 0
	v_or_b32_e32 v2, 10, v27
	v_mad_i64_i32 v[14:15], s[48:49], v2, s45, 0
	v_or_b32_e32 v2, 11, v27
	v_mad_i64_i32 v[16:17], s[48:49], v2, s45, 0
	v_or_b32_e32 v2, 12, v27
	v_mad_i64_i32 v[18:19], s[48:49], v2, s45, 0
	v_or_b32_e32 v2, 13, v27
	v_mad_i64_i32 v[20:21], s[48:49], v2, s45, 0
	v_or_b32_e32 v2, 14, v27
	v_mad_i64_i32 v[22:23], s[48:49], v2, s45, 0
	v_or_b32_e32 v2, 15, v27
	v_lshl_add_u64 v[10:11], v[10:11], 2, v[40:41]
	v_lshl_add_u64 v[12:13], v[12:13], 2, v[40:41]
	v_lshl_add_u64 v[14:15], v[14:15], 2, v[40:41]
	v_lshl_add_u64 v[16:17], v[16:17], 2, v[40:41]
	v_lshl_add_u64 v[18:19], v[18:19], 2, v[40:41]
	v_mad_i64_i32 v[24:25], s[48:49], v2, s45, 0
	v_or_b32_e32 v2, 16, v27
	v_lshl_add_u64 v[20:21], v[20:21], 2, v[40:41]
	v_lshl_add_u64 v[22:23], v[22:23], 2, v[40:41]
	v_lshl_add_u64 v[24:25], v[24:25], 2, v[40:41]
	global_load_dword v10, v[10:11], off nt
	s_nop 0
	global_load_dword v11, v[12:13], off nt
	s_nop 0
	global_load_dword v12, v[14:15], off nt
	global_load_dword v13, v[16:17], off nt
	s_nop 0
	global_load_dword v14, v[18:19], off nt
	global_load_dword v15, v[20:21], off nt
	global_load_dword v16, v[22:23], off nt
	global_load_dword v17, v[24:25], off nt
	v_mad_i64_i32 v[18:19], s[48:49], v2, s45, 0
	v_or_b32_e32 v2, 17, v27
	v_mad_i64_i32 v[20:21], s[48:49], v2, s45, 0
	v_or_b32_e32 v2, 18, v27
	v_mad_i64_i32 v[22:23], s[48:49], v2, s45, 0
	v_or_b32_e32 v2, 19, v27
	v_mad_i64_i32 v[24:25], s[48:49], v2, s45, 0
	v_or_b32_e32 v2, 20, v27
	v_mad_i64_i32 v[42:43], s[48:49], v2, s45, 0
	v_or_b32_e32 v2, 21, v27
	v_mad_i64_i32 v[44:45], s[48:49], v2, s45, 0
	v_or_b32_e32 v2, 22, v27
	v_mad_i64_i32 v[46:47], s[48:49], v2, s45, 0
	v_or_b32_e32 v2, 23, v27
	v_lshl_add_u64 v[18:19], v[18:19], 2, v[40:41]
	v_lshl_add_u64 v[20:21], v[20:21], 2, v[40:41]
	v_lshl_add_u64 v[22:23], v[22:23], 2, v[40:41]
	v_lshl_add_u64 v[24:25], v[24:25], 2, v[40:41]
	v_lshl_add_u64 v[42:43], v[42:43], 2, v[40:41]
	v_mad_i64_i32 v[48:49], s[48:49], v2, s45, 0
	v_or_b32_e32 v2, 24, v27
	v_lshl_add_u64 v[44:45], v[44:45], 2, v[40:41]
	v_lshl_add_u64 v[46:47], v[46:47], 2, v[40:41]
	v_lshl_add_u64 v[48:49], v[48:49], 2, v[40:41]
	global_load_dword v18, v[18:19], off nt
	s_nop 0
	global_load_dword v19, v[20:21], off nt
	s_nop 0
	global_load_dword v20, v[22:23], off nt
	global_load_dword v21, v[24:25], off nt
	s_nop 0
	global_load_dword v22, v[42:43], off nt
	global_load_dword v23, v[44:45], off nt
	global_load_dword v24, v[46:47], off nt
	global_load_dword v25, v[48:49], off nt
	v_mad_i64_i32 v[42:43], s[48:49], v2, s45, 0
	v_or_b32_e32 v2, 25, v27
	v_mad_i64_i32 v[44:45], s[48:49], v2, s45, 0
	v_or_b32_e32 v2, 26, v27
	v_mad_i64_i32 v[46:47], s[48:49], v2, s45, 0
	v_or_b32_e32 v2, 27, v27
	v_mad_i64_i32 v[48:49], s[48:49], v2, s45, 0
	v_or_b32_e32 v2, 28, v27
	v_mad_i64_i32 v[50:51], s[48:49], v2, s45, 0
	v_or_b32_e32 v2, 29, v27
	v_mad_i64_i32 v[52:53], s[48:49], v2, s45, 0
	v_or_b32_e32 v2, 30, v27
	v_mad_i64_i32 v[54:55], s[48:49], v2, s45, 0
	v_or_b32_e32 v2, 31, v27
	v_lshl_add_u64 v[42:43], v[42:43], 2, v[40:41]
	v_lshl_add_u64 v[44:45], v[44:45], 2, v[40:41]
	v_mad_i64_i32 v[56:57], s[48:49], v2, s45, 0
	v_lshl_add_u64 v[46:47], v[46:47], 2, v[40:41]
	v_lshl_add_u64 v[48:49], v[48:49], 2, v[40:41]
	v_lshl_add_u64 v[50:51], v[50:51], 2, v[40:41]
	v_lshl_add_u64 v[52:53], v[52:53], 2, v[40:41]
	v_lshl_add_u64 v[54:55], v[54:55], 2, v[40:41]
	v_lshl_add_u64 v[56:57], v[56:57], 2, v[40:41]
	global_load_dword v27, v[42:43], off nt
	global_load_dword v39, v[44:45], off nt
	global_load_dword v40, v[46:47], off nt
	global_load_dword v41, v[48:49], off nt
	s_nop 0
	global_load_dword v42, v[50:51], off nt
	global_load_dword v43, v[52:53], off nt
	global_load_dword v44, v[54:55], off nt
	global_load_dword v45, v[56:57], off nt

.LBB4_41:
.LBB4_42:
	s_abs_i32 s6, s43
	v_cvt_f32_u32_e32 v0, s6
	s_add_i32 s7, s62, s57
	s_sub_i32 s57, 0, s6
	s_abs_i32 s56, s7
	v_rcp_iflag_f32_e32 v0, v0
	s_xor_b32 s33, s7, s43
	s_ashr_i32 s33, s33, 31
	v_mul_f32_e32 v0, 0x4f7ffffe, v0
	v_cvt_u32_f32_e32 v0, v0
	s_nop 0
	v_readfirstlane_b32 s58, v0
	s_mul_i32 s57, s57, s58
	s_mul_hi_u32 s57, s58, s57
	s_add_i32 s58, s58, s57
	s_mul_hi_u32 s57, s56, s58
	s_mul_i32 s58, s57, s6
	s_sub_i32 s56, s56, s58
	s_add_i32 s59, s57, 1
	s_sub_i32 s58, s56, s6
	s_cmp_ge_u32 s56, s6
	s_cselect_b32 s57, s59, s57
	s_cselect_b32 s56, s58, s56
	s_add_i32 s58, s57, 1
	s_cmp_ge_u32 s56, s6
	s_cselect_b32 s6, s58, s57
	s_abs_i32 s56, s42
	v_cvt_f32_u32_e32 v0, s56
	s_xor_b32 s6, s6, s33
	s_sub_i32 s57, 0, s56
	s_sub_i32 s6, s6, s33
	v_rcp_iflag_f32_e32 v0, v0
	s_mul_i32 s33, s6, s43
	s_sub_i32 s7, s7, s33
	s_abs_i32 s43, s7
	v_mul_f32_e32 v0, 0x4f7ffffe, v0
	v_cvt_u32_f32_e32 v0, v0
	s_xor_b32 s33, s7, s42
	s_ashr_i32 s33, s33, 31
	v_readfirstlane_b32 s58, v0
	s_mul_i32 s57, s57, s58
	s_mul_hi_u32 s57, s58, s57
	s_add_i32 s58, s58, s57
	s_mul_hi_u32 s57, s43, s58
	s_mul_i32 s58, s57, s56
	s_sub_i32 s43, s43, s58
	s_add_i32 s59, s57, 1
	s_sub_i32 s58, s43, s56
	s_cmp_ge_u32 s43, s56
	s_cselect_b32 s57, s59, s57
	s_cselect_b32 s43, s58, s43
	s_add_i32 s58, s57, 1
	s_cmp_ge_u32 s43, s56
	s_cselect_b32 s43, s58, s57
	s_xor_b32 s43, s43, s33
	s_sub_i32 s56, s43, s33
	s_mul_i32 s33, s56, s42
	s_sub_i32 s33, s7, s33
	s_mul_hi_i32 s43, s6, s40
	s_mul_i32 s7, s6, s40
	s_lshl_b32 s33, s33, 6
	s_lshl_b32 s6, s56, 7
	s_and_saveexec_b64 s[56:57], s[2:3]
	s_cbranch_execz .LBB4_46
	v_or_b32_e32 v0, s33, v37
	v_cmp_gt_i32_e32 vcc, s41, v0
	v_mov_b32_e32 v1, 0
	v_mov_b32_e32 v2, 0
	v_mov_b32_e32 v3, 0
	v_mov_b32_e32 v4, 0
	v_mov_b32_e32 v5, 0
	v_mov_b32_e32 v6, 0
	v_mov_b32_e32 v7, 0
	v_mov_b32_e32 v8, 0
	v_mov_b32_e32 v9, 0
	v_mov_b32_e32 v10, 0
	v_mov_b32_e32 v11, 0
	v_mov_b32_e32 v12, 0
	v_mov_b32_e32 v13, 0
	v_mov_b32_e32 v14, 0
	v_mov_b32_e32 v15, 0
	v_mov_b32_e32 v16, 0
	v_mov_b32_e32 v17, 0
	v_mov_b32_e32 v18, 0
	v_mov_b32_e32 v19, 0
	v_mov_b32_e32 v20, 0
	v_mov_b32_e32 v21, 0
	v_mov_b32_e32 v22, 0
	v_mov_b32_e32 v23, 0
	v_mov_b32_e32 v25, 0
	v_mov_b32_e32 v27, 0
	v_mov_b32_e32 v39, 0
	v_mov_b32_e32 v40, 0
	v_mov_b32_e32 v41, 0
	v_mov_b32_e32 v42, 0
	v_mov_b32_e32 v43, 0
	v_mov_b32_e32 v44, 0
	v_mov_b32_e32 v45, 0
	s_and_saveexec_b64 s[58:59], vcc
	s_cbranch_execz .LBB4_45
	s_ashr_i32 s60, s41, 31
	s_mul_hi_u32 s61, s7, s41
	s_mul_i32 s60, s7, s60
	s_add_i32 s60, s61, s60
	s_mul_i32 s61, s43, s41
	s_add_i32 s61, s60, s61
	s_mul_i32 s60, s7, s41
	s_lshl_b64 s[60:61], s[60:61], 2
	s_add_u32 s48, s48, s60
	v_or_b32_e32 v27, s6, v36
	s_addc_u32 s49, s49, s61
	v_ashrrev_i32_e32 v1, 31, v0
	v_or_b32_e32 v2, 1, v27
	v_or_b32_e32 v4, 2, v27
	v_or_b32_e32 v6, 3, v27
	v_or_b32_e32 v8, 4, v27
	v_lshl_add_u64 v[40:41], v[0:1], 2, s[48:49]
	v_mad_i64_i32 v[0:1], s[48:49], v27, s41, 0
	v_mad_i64_i32 v[2:3], s[48:49], v2, s41, 0
	v_mad_i64_i32 v[4:5], s[48:49], v4, s41, 0
	v_mad_i64_i32 v[6:7], s[48:49], v6, s41, 0
	v_mad_i64_i32 v[8:9], s[48:49], v8, s41, 0
	v_or_b32_e32 v10, 5, v27
	v_or_b32_e32 v12, 6, v27
	v_or_b32_e32 v14, 7, v27
	v_lshl_add_u64 v[0:1], v[0:1], 2, v[40:41]
	v_lshl_add_u64 v[2:3], v[2:3], 2, v[40:41]
	v_lshl_add_u64 v[4:5], v[4:5], 2, v[40:41]
	v_lshl_add_u64 v[6:7], v[6:7], 2, v[40:41]
	v_lshl_add_u64 v[8:9], v[8:9], 2, v[40:41]
	v_mad_i64_i32 v[10:11], s[48:49], v10, s41, 0
	v_mad_i64_i32 v[12:13], s[48:49], v12, s41, 0
	v_mad_i64_i32 v[14:15], s[48:49], v14, s41, 0
	v_lshl_add_u64 v[10:11], v[10:11], 2, v[40:41]
	v_lshl_add_u64 v[12:13], v[12:13], 2, v[40:41]
	v_lshl_add_u64 v[14:15], v[14:15], 2, v[40:41]
	global_load_dword v1, v[0:1], off nt
	s_nop 0
	global_load_dword v2, v[2:3], off nt
	s_nop 0
	global_load_dword v3, v[4:5], off nt
	s_nop 0
	global_load_dword v4, v[6:7], off nt
	global_load_dword v5, v[8:9], off nt
	s_nop 0
	global_load_dword v6, v[10:11], off nt
	global_load_dword v7, v[12:13], off nt
	global_load_dword v8, v[14:15], off nt
	v_or_b32_e32 v0, 8, v27
	v_mad_i64_i32 v[10:11], s[48:49], v0, s41, 0
	v_or_b32_e32 v0, 9, v27
	v_mad_i64_i32 v[12:13], s[48:49], v0, s41, 0
	v_or_b32_e32 v0, 10, v27
	v_mad_i64_i32 v[14:15], s[48:49], v0, s41, 0
	v_or_b32_e32 v0, 11, v27
	v_mad_i64_i32 v[16:17], s[48:49], v0, s41, 0
	v_or_b32_e32 v0, 12, v27
	v_mad_i64_i32 v[18:19], s[48:49], v0, s41, 0
	v_or_b32_e32 v0, 13, v27
	v_mad_i64_i32 v[20:21], s[48:49], v0, s41, 0
	v_or_b32_e32 v0, 14, v27
	v_mad_i64_i32 v[22:23], s[48:49], v0, s41, 0
	v_or_b32_e32 v0, 15, v27
	v_lshl_add_u64 v[10:11], v[10:11], 2, v[40:41]
	v_lshl_add_u64 v[12:13], v[12:13], 2, v[40:41]
	v_lshl_add_u64 v[14:15], v[14:15], 2, v[40:41]
	v_lshl_add_u64 v[16:17], v[16:17], 2, v[40:41]
	v_lshl_add_u64 v[18:19], v[18:19], 2, v[40:41]
	v_mad_i64_i32 v[42:43], s[48:49], v0, s41, 0
	v_or_b32_e32 v0, 16, v27
	v_lshl_add_u64 v[20:21], v[20:21], 2, v[40:41]
	v_lshl_add_u64 v[22:23], v[22:23], 2, v[40:41]
	v_lshl_add_u64 v[42:43], v[42:43], 2, v[40:41]
	global_load_dword v9, v[10:11], off nt
	s_nop 0
	global_load_dword v10, v[12:13], off nt
	global_load_dword v11, v[14:15], off nt
	s_nop 0
	global_load_dword v12, v[16:17], off nt
	global_load_dword v13, v[18:19], off nt
	global_load_dword v14, v[20:21], off nt
	global_load_dword v15, v[22:23], off nt
	s_nop 0
	global_load_dword v16, v[42:43], off nt
	v_mad_i64_i32 v[18:19], s[48:49], v0, s41, 0
	v_or_b32_e32 v0, 17, v27
	v_mad_i64_i32 v[20:21], s[48:49], v0, s41, 0
	v_or_b32_e32 v0, 18, v27
	v_mad_i64_i32 v[22:23], s[48:49], v0, s41, 0
	v_or_b32_e32 v0, 19, v27
	v_mad_i64_i32 v[42:43], s[48:49], v0, s41, 0
	v_or_b32_e32 v0, 20, v27
	v_mad_i64_i32 v[44:45], s[48:49], v0, s41, 0
	v_or_b32_e32 v0, 21, v27
	v_mad_i64_i32 v[46:47], s[48:49], v0, s41, 0
	v_or_b32_e32 v0, 22, v27
	v_mad_i64_i32 v[48:49], s[48:49], v0, s41, 0
	v_or_b32_e32 v0, 23, v27
	v_lshl_add_u64 v[18:19], v[18:19], 2, v[40:41]
	v_lshl_add_u64 v[20:21], v[20:21], 2, v[40:41]
	v_lshl_add_u64 v[22:23], v[22:23], 2, v[40:41]
	v_lshl_add_u64 v[42:43], v[42:43], 2, v[40:41]
	v_mad_i64_i32 v[50:51], s[48:49], v0, s41, 0
	v_or_b32_e32 v0, 24, v27
	v_lshl_add_u64 v[44:45], v[44:45], 2, v[40:41]
	v_lshl_add_u64 v[46:47], v[46:47], 2, v[40:41]
	v_lshl_add_u64 v[48:49], v[48:49], 2, v[40:41]
	v_lshl_add_u64 v[50:51], v[50:51], 2, v[40:41]
	global_load_dword v17, v[18:19], off nt
	s_nop 0
	global_load_dword v18, v[20:21], off nt
	global_load_dword v19, v[22:23], off nt
	s_nop 0
	global_load_dword v20, v[42:43], off nt
	global_load_dword v21, v[44:45], off nt
	global_load_dword v22, v[46:47], off nt
	global_load_dword v23, v[48:49], off nt
	global_load_dword v25, v[50:51], off nt
	v_mad_i64_i32 v[42:43], s[48:49], v0, s41, 0
	v_or_b32_e32 v0, 25, v27
	v_mad_i64_i32 v[44:45], s[48:49], v0, s41, 0
	v_or_b32_e32 v0, 26, v27
	v_mad_i64_i32 v[46:47], s[48:49], v0, s41, 0
	v_or_b32_e32 v0, 27, v27
	v_mad_i64_i32 v[48:49], s[48:49], v0, s41, 0
	v_or_b32_e32 v0, 28, v27
	v_mad_i64_i32 v[50:51], s[48:49], v0, s41, 0
	v_or_b32_e32 v0, 29, v27
	v_mad_i64_i32 v[52:53], s[48:49], v0, s41, 0
	v_or_b32_e32 v0, 30, v27
	v_mad_i64_i32 v[54:55], s[48:49], v0, s41, 0
	v_or_b32_e32 v0, 31, v27
	v_lshl_add_u64 v[42:43], v[42:43], 2, v[40:41]
	v_lshl_add_u64 v[44:45], v[44:45], 2, v[40:41]
	v_mad_i64_i32 v[56:57], s[48:49], v0, s41, 0
	v_lshl_add_u64 v[46:47], v[46:47], 2, v[40:41]
	v_lshl_add_u64 v[48:49], v[48:49], 2, v[40:41]
	v_lshl_add_u64 v[50:51], v[50:51], 2, v[40:41]
	v_lshl_add_u64 v[52:53], v[52:53], 2, v[40:41]
	v_lshl_add_u64 v[54:55], v[54:55], 2, v[40:41]
	v_lshl_add_u64 v[56:57], v[56:57], 2, v[40:41]
	global_load_dword v27, v[42:43], off nt
	global_load_dword v39, v[44:45], off nt
	global_load_dword v40, v[46:47], off nt
	global_load_dword v41, v[48:49], off nt
	s_nop 0
	global_load_dword v42, v[50:51], off nt
	global_load_dword v43, v[52:53], off nt
	global_load_dword v44, v[54:55], off nt
	global_load_dword v45, v[56:57], off nt

.LBB4_52:
.LBB4_53:
	s_abs_i32 s0, s39
	v_cvt_f32_u32_e32 v0, s0
	s_sub_i32 s42, 0, s0
	s_add_i32 s1, s33, s55
	s_abs_i32 s41, s1
	v_rcp_iflag_f32_e32 v0, v0
	s_xor_b32 s40, s1, s39
	s_ashr_i32 s40, s40, 31
	v_mul_f32_e32 v0, 0x4f7ffffe, v0
	v_cvt_u32_f32_e32 v0, v0
	s_nop 0
	v_readfirstlane_b32 s43, v0
	s_mul_i32 s42, s42, s43
	s_mul_hi_u32 s42, s43, s42
	s_add_i32 s43, s43, s42
	s_mul_hi_u32 s42, s41, s43
	s_mul_i32 s43, s42, s0
	s_sub_i32 s41, s41, s43
	s_add_i32 s48, s42, 1
	s_sub_i32 s43, s41, s0
	s_cmp_ge_u32 s41, s0
	s_cselect_b32 s42, s48, s42
	s_cselect_b32 s41, s43, s41
	s_add_i32 s43, s42, 1
	s_cmp_ge_u32 s41, s0
	s_cselect_b32 s0, s43, s42
	s_abs_i32 s41, s38
	v_cvt_f32_u32_e32 v0, s41
	s_xor_b32 s0, s0, s40
	s_sub_i32 s42, 0, s41
	s_sub_i32 s0, s0, s40
	v_rcp_iflag_f32_e32 v0, v0
	s_mul_i32 s39, s0, s39
	s_sub_i32 s39, s1, s39
	s_abs_i32 s40, s39
	v_mul_f32_e32 v0, 0x4f7ffffe, v0
	v_cvt_u32_f32_e32 v0, v0
	s_xor_b32 s1, s39, s38
	s_ashr_i32 s1, s1, 31
	v_readfirstlane_b32 s43, v0
	s_mul_i32 s42, s42, s43
	s_mul_hi_u32 s42, s43, s42
	s_add_i32 s43, s43, s42
	s_mul_hi_u32 s42, s40, s43
	s_mul_i32 s43, s42, s41
	s_sub_i32 s40, s40, s43
	s_add_i32 s48, s42, 1
	s_sub_i32 s43, s40, s41
	s_cmp_ge_u32 s40, s41
	s_cselect_b32 s42, s48, s42
	s_cselect_b32 s40, s43, s40
	s_add_i32 s43, s42, 1
	s_cmp_ge_u32 s40, s41
	s_cselect_b32 s40, s43, s42
	s_xor_b32 s40, s40, s1
	s_sub_i32 s1, s40, s1
	s_mul_i32 s40, s1, s38
	s_sub_i32 s40, s39, s40
	s_mul_hi_i32 s41, s0, s36
	s_mul_i32 s39, s0, s36
	s_ashr_i32 s50, s37, 31
	s_lshl_b32 s40, s40, 6
	s_lshl_b32 s0, s1, 7
	s_and_saveexec_b64 s[42:43], s[2:3]
	s_cbranch_execz .LBB4_57
	v_or_b32_e32 v0, s40, v37
	v_cmp_gt_i32_e32 vcc, s37, v0
	v_mov_b32_e32 v1, 0
	v_mov_b32_e32 v2, 0
	v_mov_b32_e32 v3, 0
	v_mov_b32_e32 v4, 0
	v_mov_b32_e32 v5, 0
	v_mov_b32_e32 v6, 0
	v_mov_b32_e32 v7, 0
	v_mov_b32_e32 v8, 0
	v_mov_b32_e32 v9, 0
	v_mov_b32_e32 v10, 0
	v_mov_b32_e32 v11, 0
	v_mov_b32_e32 v12, 0
	v_mov_b32_e32 v13, 0
	v_mov_b32_e32 v14, 0
	v_mov_b32_e32 v15, 0
	v_mov_b32_e32 v16, 0
	v_mov_b32_e32 v17, 0
	v_mov_b32_e32 v18, 0
	v_mov_b32_e32 v19, 0
	v_mov_b32_e32 v20, 0
	v_mov_b32_e32 v21, 0
	v_mov_b32_e32 v22, 0
	v_mov_b32_e32 v23, 0
	v_mov_b32_e32 v25, 0
	v_mov_b32_e32 v27, 0
	v_mov_b32_e32 v39, 0
	v_mov_b32_e32 v40, 0
	v_mov_b32_e32 v41, 0
	v_mov_b32_e32 v42, 0
	v_mov_b32_e32 v43, 0
	v_mov_b32_e32 v44, 0
	v_mov_b32_e32 v45, 0
	s_and_saveexec_b64 s[48:49], vcc
	s_cbranch_execz .LBB4_56
	s_mul_i32 s50, s39, s50
	s_mul_hi_u32 s51, s39, s37
	s_add_i32 s50, s51, s50
	s_mul_i32 s51, s41, s37
	s_add_i32 s51, s50, s51
	s_mul_i32 s50, s39, s37
	s_lshl_b64 s[50:51], s[50:51], 2
	s_add_u32 s44, s44, s50
	s_addc_u32 s45, s45, s51
	v_or_b32_e32 v27, s0, v36
	v_ashrrev_i32_e32 v1, 31, v0
	v_lshl_add_u64 v[40:41], v[0:1], 2, s[44:45]
	v_mad_i64_i32 v[0:1], s[44:45], v27, s37, 0
	v_lshl_add_u64 v[10:11], v[0:1], 2, v[40:41]
	v_or_b32_e32 v0, 1, v27
	v_mad_i64_i32 v[0:1], s[44:45], v0, s37, 0
	v_lshl_add_u64 v[12:13], v[0:1], 2, v[40:41]
	v_or_b32_e32 v0, 2, v27
	v_mad_i64_i32 v[0:1], s[44:45], v0, s37, 0
	v_lshl_add_u64 v[14:15], v[0:1], 2, v[40:41]
	v_or_b32_e32 v0, 3, v27
	v_mad_i64_i32 v[0:1], s[44:45], v0, s37, 0
	v_lshl_add_u64 v[16:17], v[0:1], 2, v[40:41]
	v_or_b32_e32 v0, 4, v27
	v_mad_i64_i32 v[0:1], s[44:45], v0, s37, 0
	v_lshl_add_u64 v[18:19], v[0:1], 2, v[40:41]
	v_or_b32_e32 v0, 5, v27
	v_mad_i64_i32 v[0:1], s[44:45], v0, s37, 0
	v_lshl_add_u64 v[20:21], v[0:1], 2, v[40:41]
	v_or_b32_e32 v0, 6, v27
	v_mad_i64_i32 v[0:1], s[44:45], v0, s37, 0
	v_lshl_add_u64 v[22:23], v[0:1], 2, v[40:41]
	v_or_b32_e32 v0, 7, v27
	v_mad_i64_i32 v[0:1], s[44:45], v0, s37, 0
	v_lshl_add_u64 v[42:43], v[0:1], 2, v[40:41]
	v_or_b32_e32 v0, 8, v27
	global_load_dword v1, v[10:11], off nt
	global_load_dword v2, v[12:13], off nt
	global_load_dword v3, v[14:15], off nt
	global_load_dword v4, v[16:17], off nt
	global_load_dword v5, v[18:19], off nt
	global_load_dword v6, v[20:21], off nt
	global_load_dword v7, v[22:23], off nt
	global_load_dword v8, v[42:43], off nt
	v_mad_i64_i32 v[10:11], s[44:45], v0, s37, 0
	v_or_b32_e32 v0, 9, v27
	v_mad_i64_i32 v[12:13], s[44:45], v0, s37, 0
	v_or_b32_e32 v0, 10, v27
	v_lshl_add_u64 v[18:19], v[12:13], 2, v[40:41]
	v_mad_i64_i32 v[12:13], s[44:45], v0, s37, 0
	v_or_b32_e32 v0, 11, v27
	v_lshl_add_u64 v[20:21], v[12:13], 2, v[40:41]
	v_mad_i64_i32 v[12:13], s[44:45], v0, s37, 0
	v_or_b32_e32 v0, 12, v27
	v_lshl_add_u64 v[22:23], v[12:13], 2, v[40:41]
	v_mad_i64_i32 v[12:13], s[44:45], v0, s37, 0
	v_or_b32_e32 v0, 13, v27
	v_lshl_add_u64 v[42:43], v[12:13], 2, v[40:41]
	v_mad_i64_i32 v[12:13], s[44:45], v0, s37, 0
	v_or_b32_e32 v0, 14, v27
	v_lshl_add_u64 v[44:45], v[12:13], 2, v[40:41]
	v_mad_i64_i32 v[12:13], s[44:45], v0, s37, 0
	v_or_b32_e32 v0, 15, v27
	v_lshl_add_u64 v[10:11], v[10:11], 2, v[40:41]
	v_lshl_add_u64 v[46:47], v[12:13], 2, v[40:41]
	v_mad_i64_i32 v[12:13], s[44:45], v0, s37, 0
	v_or_b32_e32 v0, 16, v27
	v_lshl_add_u64 v[48:49], v[12:13], 2, v[40:41]
	global_load_dword v9, v[10:11], off nt
	s_nop 0
	global_load_dword v10, v[18:19], off nt
	global_load_dword v11, v[20:21], off nt
	global_load_dword v12, v[22:23], off nt
	global_load_dword v13, v[42:43], off nt
	global_load_dword v14, v[44:45], off nt
	global_load_dword v15, v[46:47], off nt
	global_load_dword v16, v[48:49], off nt
	v_mad_i64_i32 v[18:19], s[44:45], v0, s37, 0
	v_or_b32_e32 v0, 17, v27
	v_mad_i64_i32 v[20:21], s[44:45], v0, s37, 0
	v_or_b32_e32 v0, 18, v27
	v_lshl_add_u64 v[42:43], v[20:21], 2, v[40:41]
	v_mad_i64_i32 v[20:21], s[44:45], v0, s37, 0
	v_or_b32_e32 v0, 19, v27
	v_lshl_add_u64 v[44:45], v[20:21], 2, v[40:41]
	v_mad_i64_i32 v[20:21], s[44:45], v0, s37, 0
	v_or_b32_e32 v0, 20, v27
	v_lshl_add_u64 v[46:47], v[20:21], 2, v[40:41]
	v_mad_i64_i32 v[20:21], s[44:45], v0, s37, 0
	v_or_b32_e32 v0, 21, v27
	v_lshl_add_u64 v[48:49], v[20:21], 2, v[40:41]
	v_mad_i64_i32 v[20:21], s[44:45], v0, s37, 0
	v_or_b32_e32 v0, 22, v27
	v_lshl_add_u64 v[50:51], v[20:21], 2, v[40:41]
	v_mad_i64_i32 v[20:21], s[44:45], v0, s37, 0
	v_or_b32_e32 v0, 23, v27
	v_lshl_add_u64 v[18:19], v[18:19], 2, v[40:41]
	v_lshl_add_u64 v[52:53], v[20:21], 2, v[40:41]
	v_mad_i64_i32 v[20:21], s[44:45], v0, s37, 0
	v_or_b32_e32 v0, 24, v27
	v_lshl_add_u64 v[54:55], v[20:21], 2, v[40:41]
	global_load_dword v17, v[18:19], off nt
	s_nop 0
	global_load_dword v18, v[42:43], off nt
	global_load_dword v19, v[44:45], off nt
	global_load_dword v20, v[46:47], off nt
	global_load_dword v21, v[48:49], off nt
	global_load_dword v22, v[50:51], off nt
	global_load_dword v23, v[52:53], off nt
	global_load_dword v25, v[54:55], off nt
	v_mad_i64_i32 v[42:43], s[44:45], v0, s37, 0
	v_or_b32_e32 v0, 25, v27
	v_mad_i64_i32 v[44:45], s[44:45], v0, s37, 0
	v_or_b32_e32 v0, 26, v27
	v_lshl_add_u64 v[46:47], v[44:45], 2, v[40:41]
	v_mad_i64_i32 v[44:45], s[44:45], v0, s37, 0
	v_or_b32_e32 v0, 27, v27
	v_lshl_add_u64 v[48:49], v[44:45], 2, v[40:41]
	v_mad_i64_i32 v[44:45], s[44:45], v0, s37, 0
	v_or_b32_e32 v0, 28, v27
	v_lshl_add_u64 v[50:51], v[44:45], 2, v[40:41]
	v_mad_i64_i32 v[44:45], s[44:45], v0, s37, 0
	v_or_b32_e32 v0, 29, v27
	v_lshl_add_u64 v[52:53], v[44:45], 2, v[40:41]
	v_mad_i64_i32 v[44:45], s[44:45], v0, s37, 0
	v_or_b32_e32 v0, 30, v27
	v_lshl_add_u64 v[54:55], v[44:45], 2, v[40:41]
	v_mad_i64_i32 v[44:45], s[44:45], v0, s37, 0
	v_or_b32_e32 v0, 31, v27
	v_lshl_add_u64 v[42:43], v[42:43], 2, v[40:41]
	v_lshl_add_u64 v[56:57], v[44:45], 2, v[40:41]
	v_mad_i64_i32 v[44:45], s[44:45], v0, s37, 0
	v_lshl_add_u64 v[58:59], v[44:45], 2, v[40:41]
	global_load_dword v27, v[42:43], off nt
	global_load_dword v39, v[46:47], off nt
	global_load_dword v40, v[48:49], off nt
	global_load_dword v41, v[50:51], off nt
	s_nop 0
	global_load_dword v42, v[52:53], off nt
	global_load_dword v43, v[54:55], off nt
	global_load_dword v44, v[56:57], off nt
	global_load_dword v45, v[58:59], off nt

.LBB4_82:
	s_cmp_ge_i32 s40, s52
	s_cselect_b64 s[0:1], -1, 0
	s_cmp_lt_i32 s40, s52
	s_mov_b64 s[4:5], -1
	s_cbranch_scc0 .LBB4_90
	s_abs_i32 s4, s31
	s_waitcnt vmcnt(5)
	v_cvt_f32_u32_e32 v0, s4
	s_sub_i32 s8, 0, s4
	s_add_i32 s5, s40, s53
	s_abs_i32 s7, s5
	v_rcp_iflag_f32_e32 v0, v0
	s_xor_b32 s6, s5, s31
	s_ashr_i32 s6, s6, 31
	v_mul_f32_e32 v0, 0x4f7ffffe, v0
	v_cvt_u32_f32_e32 v0, v0
	s_nop 0
	v_readfirstlane_b32 s9, v0
	s_mul_i32 s8, s8, s9
	s_mul_hi_u32 s8, s9, s8
	s_add_i32 s9, s9, s8
	s_mul_hi_u32 s8, s7, s9
	s_mul_i32 s9, s8, s4
	s_sub_i32 s7, s7, s9
	s_add_i32 s10, s8, 1
	s_sub_i32 s9, s7, s4
	s_cmp_ge_u32 s7, s4
	s_cselect_b32 s8, s10, s8
	s_cselect_b32 s7, s9, s7
	s_add_i32 s9, s8, 1
	s_cmp_ge_u32 s7, s4
	s_cselect_b32 s4, s9, s8
	s_abs_i32 s7, s30
	v_cvt_f32_u32_e32 v0, s7
	s_xor_b32 s4, s4, s6
	s_sub_i32 s8, 0, s7
	s_sub_i32 s4, s4, s6
	v_rcp_iflag_f32_e32 v0, v0
	s_mul_i32 s6, s4, s31
	s_sub_i32 s5, s5, s6
	s_abs_i32 s9, s5
	v_mul_f32_e32 v0, 0x4f7ffffe, v0
	v_cvt_u32_f32_e32 v0, v0
	s_xor_b32 s6, s5, s30
	s_ashr_i32 s6, s6, 31
	v_readfirstlane_b32 s10, v0
	s_mul_i32 s8, s8, s10
	s_mul_hi_u32 s8, s10, s8
	s_add_i32 s10, s10, s8
	s_mul_hi_u32 s8, s9, s10
	s_mul_i32 s10, s8, s7
	s_sub_i32 s9, s9, s10
	s_add_i32 s11, s8, 1
	s_sub_i32 s10, s9, s7
	s_cmp_ge_u32 s9, s7
	s_cselect_b32 s8, s11, s8
	s_cselect_b32 s9, s10, s9
	s_add_i32 s10, s8, 1
	s_cmp_ge_u32 s9, s7
	s_cselect_b32 s7, s10, s8
	s_xor_b32 s7, s7, s6
	s_sub_i32 s6, s7, s6
	s_mul_i32 s7, s6, s30
	s_sub_i32 s7, s5, s7
	s_mul_hi_i32 s11, s4, s28
	s_mul_i32 s5, s4, s28
	s_lshl_b32 s10, s7, 6
	s_lshl_b32 s4, s6, 7
	s_and_saveexec_b64 s[6:7], s[2:3]
	s_cbranch_execz .LBB4_87
	v_or_b32_e32 v0, s10, v37
	v_cmp_gt_i32_e32 vcc, s29, v0
	v_mov_b32_e32 v1, 0
	s_waitcnt lgkmcnt(0)
	v_mov_b32_e32 v2, 0
	v_mov_b32_e32 v3, 0
	s_waitcnt vmcnt(4)
	v_mov_b32_e32 v4, 0
	v_mov_b32_e32 v5, 0
	v_mov_b32_e32 v6, 0
	v_mov_b32_e32 v7, 0
	s_waitcnt vmcnt(3)
	v_mov_b32_e32 v8, 0
	v_mov_b32_e32 v9, 0
	v_mov_b32_e32 v10, 0
	v_mov_b32_e32 v11, 0
	s_waitcnt vmcnt(2)
	v_mov_b32_e32 v12, 0
	v_mov_b32_e32 v13, 0
	v_mov_b32_e32 v14, 0
	v_mov_b32_e32 v15, 0
	v_mov_b32_e32 v16, 0
	v_mov_b32_e32 v17, 0
	v_mov_b32_e32 v18, 0
	v_mov_b32_e32 v19, 0
	v_mov_b32_e32 v20, 0
	v_mov_b32_e32 v21, 0
	v_mov_b32_e32 v22, 0
	v_mov_b32_e32 v23, 0
	v_mov_b32_e32 v25, 0
	v_mov_b32_e32 v27, 0
	v_mov_b32_e32 v38, 0
	v_mov_b32_e32 v39, 0
	v_mov_b32_e32 v40, 0
	v_mov_b32_e32 v41, 0
	v_mov_b32_e32 v42, 0
	v_mov_b32_e32 v43, 0
	v_mov_b32_e32 v44, 0
	s_and_saveexec_b64 s[8:9], vcc
	s_cbranch_execz .LBB4_86
	s_ashr_i32 s12, s29, 31
	s_mul_hi_u32 s13, s5, s29
	s_mul_i32 s12, s5, s12
	s_add_i32 s12, s13, s12
	s_mul_i32 s13, s11, s29
	s_add_i32 s13, s12, s13
	s_mul_i32 s12, s5, s29
	s_lshl_b64 s[12:13], s[12:13], 2
	s_add_u32 s12, s20, s12
	s_addc_u32 s13, s21, s13
	v_or_b32_e32 v27, s4, v36
	v_ashrrev_i32_e32 v1, 31, v0
	v_lshl_add_u64 v[38:39], v[0:1], 2, s[12:13]
	v_mad_i64_i32 v[0:1], s[12:13], v27, s29, 0
	v_lshl_add_u64 v[10:11], v[0:1], 2, v[38:39]
	v_or_b32_e32 v0, 1, v27
	v_mad_i64_i32 v[0:1], s[12:13], v0, s29, 0
	v_lshl_add_u64 v[12:13], v[0:1], 2, v[38:39]
	v_or_b32_e32 v0, 2, v27
	v_mad_i64_i32 v[0:1], s[12:13], v0, s29, 0
	v_lshl_add_u64 v[14:15], v[0:1], 2, v[38:39]
	v_or_b32_e32 v0, 3, v27
	v_mad_i64_i32 v[0:1], s[12:13], v0, s29, 0
	v_lshl_add_u64 v[16:17], v[0:1], 2, v[38:39]
	v_or_b32_e32 v0, 4, v27
	v_mad_i64_i32 v[0:1], s[12:13], v0, s29, 0
	v_lshl_add_u64 v[18:19], v[0:1], 2, v[38:39]
	v_or_b32_e32 v0, 5, v27
	v_mad_i64_i32 v[0:1], s[12:13], v0, s29, 0
	v_lshl_add_u64 v[20:21], v[0:1], 2, v[38:39]
	v_or_b32_e32 v0, 6, v27
	v_mad_i64_i32 v[0:1], s[12:13], v0, s29, 0
	v_lshl_add_u64 v[22:23], v[0:1], 2, v[38:39]
	v_or_b32_e32 v0, 7, v27
	v_mad_i64_i32 v[0:1], s[12:13], v0, s29, 0
	v_lshl_add_u64 v[40:41], v[0:1], 2, v[38:39]
	v_or_b32_e32 v0, 8, v27
	global_load_dword v1, v[10:11], off nt
	global_load_dword v2, v[12:13], off nt
	global_load_dword v3, v[14:15], off nt
	global_load_dword v4, v[16:17], off nt
	global_load_dword v5, v[18:19], off nt
	global_load_dword v6, v[20:21], off nt
	global_load_dword v7, v[22:23], off nt
	global_load_dword v8, v[40:41], off nt
	v_mad_i64_i32 v[10:11], s[12:13], v0, s29, 0
	v_or_b32_e32 v0, 9, v27
	v_lshl_add_u64 v[18:19], v[10:11], 2, v[38:39]
	v_mad_i64_i32 v[10:11], s[12:13], v0, s29, 0
	v_or_b32_e32 v0, 10, v27
	v_lshl_add_u64 v[20:21], v[10:11], 2, v[38:39]
	v_mad_i64_i32 v[10:11], s[12:13], v0, s29, 0
	v_or_b32_e32 v0, 11, v27
	v_lshl_add_u64 v[22:23], v[10:11], 2, v[38:39]
	v_mad_i64_i32 v[10:11], s[12:13], v0, s29, 0
	v_or_b32_e32 v0, 12, v27
	v_lshl_add_u64 v[40:41], v[10:11], 2, v[38:39]
	v_mad_i64_i32 v[10:11], s[12:13], v0, s29, 0
	v_or_b32_e32 v0, 13, v27
	v_lshl_add_u64 v[42:43], v[10:11], 2, v[38:39]
	v_mad_i64_i32 v[10:11], s[12:13], v0, s29, 0
	v_or_b32_e32 v0, 14, v27
	v_lshl_add_u64 v[44:45], v[10:11], 2, v[38:39]
	v_mad_i64_i32 v[10:11], s[12:13], v0, s29, 0
	v_or_b32_e32 v0, 15, v27
	v_lshl_add_u64 v[46:47], v[10:11], 2, v[38:39]
	v_mad_i64_i32 v[10:11], s[12:13], v0, s29, 0
	v_or_b32_e32 v0, 16, v27
	v_lshl_add_u64 v[48:49], v[10:11], 2, v[38:39]
	global_load_dword v9, v[18:19], off nt
	global_load_dword v10, v[20:21], off nt
	global_load_dword v11, v[22:23], off nt
	global_load_dword v12, v[40:41], off nt
	global_load_dword v13, v[42:43], off nt
	global_load_dword v14, v[44:45], off nt
	global_load_dword v15, v[46:47], off nt
	global_load_dword v16, v[48:49], off nt
	v_mad_i64_i32 v[18:19], s[12:13], v0, s29, 0
	v_or_b32_e32 v0, 17, v27
	v_lshl_add_u64 v[40:41], v[18:19], 2, v[38:39]
	v_mad_i64_i32 v[18:19], s[12:13], v0, s29, 0
	v_or_b32_e32 v0, 18, v27
	v_lshl_add_u64 v[42:43], v[18:19], 2, v[38:39]
	v_mad_i64_i32 v[18:19], s[12:13], v0, s29, 0
	v_or_b32_e32 v0, 19, v27
	v_lshl_add_u64 v[44:45], v[18:19], 2, v[38:39]
	v_mad_i64_i32 v[18:19], s[12:13], v0, s29, 0
	v_or_b32_e32 v0, 20, v27
	v_lshl_add_u64 v[46:47], v[18:19], 2, v[38:39]
	v_mad_i64_i32 v[18:19], s[12:13], v0, s29, 0
	v_or_b32_e32 v0, 21, v27
	v_lshl_add_u64 v[48:49], v[18:19], 2, v[38:39]
	v_mad_i64_i32 v[18:19], s[12:13], v0, s29, 0
	v_or_b32_e32 v0, 22, v27
	v_lshl_add_u64 v[50:51], v[18:19], 2, v[38:39]
	v_mad_i64_i32 v[18:19], s[12:13], v0, s29, 0
	v_or_b32_e32 v0, 23, v27
	v_lshl_add_u64 v[52:53], v[18:19], 2, v[38:39]
	v_mad_i64_i32 v[18:19], s[12:13], v0, s29, 0
	v_or_b32_e32 v0, 24, v27
	v_lshl_add_u64 v[54:55], v[18:19], 2, v[38:39]
	global_load_dword v17, v[40:41], off nt
	global_load_dword v18, v[42:43], off nt
	global_load_dword v19, v[44:45], off nt
	global_load_dword v20, v[46:47], off nt
	global_load_dword v21, v[48:49], off nt
	global_load_dword v22, v[50:51], off nt
	global_load_dword v23, v[52:53], off nt
	global_load_dword v25, v[54:55], off nt
	v_mad_i64_i32 v[40:41], s[12:13], v0, s29, 0
	v_or_b32_e32 v0, 25, v27
	v_lshl_add_u64 v[46:47], v[40:41], 2, v[38:39]
	v_mad_i64_i32 v[40:41], s[12:13], v0, s29, 0
	v_or_b32_e32 v0, 26, v27
	v_lshl_add_u64 v[48:49], v[40:41], 2, v[38:39]
	v_mad_i64_i32 v[40:41], s[12:13], v0, s29, 0
	v_or_b32_e32 v0, 27, v27
	v_lshl_add_u64 v[50:51], v[40:41], 2, v[38:39]
	v_mad_i64_i32 v[40:41], s[12:13], v0, s29, 0
	v_or_b32_e32 v0, 28, v27
	v_lshl_add_u64 v[52:53], v[40:41], 2, v[38:39]
	v_mad_i64_i32 v[40:41], s[12:13], v0, s29, 0
	v_or_b32_e32 v0, 29, v27
	v_lshl_add_u64 v[54:55], v[40:41], 2, v[38:39]
	v_mad_i64_i32 v[40:41], s[12:13], v0, s29, 0
	v_or_b32_e32 v0, 30, v27
	v_lshl_add_u64 v[56:57], v[40:41], 2, v[38:39]
	v_mad_i64_i32 v[40:41], s[12:13], v0, s29, 0
	v_or_b32_e32 v0, 31, v27
	v_lshl_add_u64 v[58:59], v[40:41], 2, v[38:39]
	v_mad_i64_i32 v[40:41], s[12:13], v0, s29, 0
	v_lshl_add_u64 v[60:61], v[40:41], 2, v[38:39]
	global_load_dword v27, v[46:47], off nt
	global_load_dword v38, v[48:49], off nt
	global_load_dword v39, v[50:51], off nt
	global_load_dword v40, v[52:53], off nt
	global_load_dword v41, v[54:55], off nt
	global_load_dword v42, v[56:57], off nt
	global_load_dword v43, v[58:59], off nt
	global_load_dword v44, v[60:61], off nt

.LBB4_92:
	s_cmp_lt_i32 s40, s34
	s_cselect_b64 s[4:5], -1, 0
	s_and_b64 s[0:1], s[0:1], s[4:5]
	s_andn2_b64 vcc, exec, s[0:1]
	s_cbranch_vccnz .LBB4_40
	s_abs_i32 s0, s27
	s_waitcnt vmcnt(5)
	v_cvt_f32_u32_e32 v0, s0
	s_sub_i32 s6, 0, s0
	s_add_i32 s1, s40, s35
	s_abs_i32 s5, s1
	v_rcp_iflag_f32_e32 v0, v0
	s_xor_b32 s4, s1, s27
	s_ashr_i32 s4, s4, 31
	v_mul_f32_e32 v0, 0x4f7ffffe, v0
	v_cvt_u32_f32_e32 v0, v0
	s_nop 0
	v_readfirstlane_b32 s7, v0
	s_mul_i32 s6, s6, s7
	s_mul_hi_u32 s6, s7, s6
	s_add_i32 s7, s7, s6
	s_mul_hi_u32 s6, s5, s7
	s_mul_i32 s7, s6, s0
	s_sub_i32 s5, s5, s7
	s_add_i32 s8, s6, 1
	s_sub_i32 s7, s5, s0
	s_cmp_ge_u32 s5, s0
	s_cselect_b32 s6, s8, s6
	s_cselect_b32 s5, s7, s5
	s_add_i32 s7, s6, 1
	s_cmp_ge_u32 s5, s0
	s_cselect_b32 s0, s7, s6
	s_abs_i32 s5, s26
	v_cvt_f32_u32_e32 v0, s5
	s_xor_b32 s0, s0, s4
	s_sub_i32 s6, 0, s5
	s_sub_i32 s0, s0, s4
	v_rcp_iflag_f32_e32 v0, v0
	s_mul_i32 s4, s0, s27
	s_sub_i32 s1, s1, s4
	s_abs_i32 s7, s1
	v_mul_f32_e32 v0, 0x4f7ffffe, v0
	v_cvt_u32_f32_e32 v0, v0
	s_xor_b32 s4, s1, s26
	s_ashr_i32 s4, s4, 31
	v_readfirstlane_b32 s8, v0
	s_mul_i32 s6, s6, s8
	s_mul_hi_u32 s6, s8, s6
	s_add_i32 s8, s8, s6
	s_mul_hi_u32 s6, s7, s8
	s_mul_i32 s8, s6, s5
	s_sub_i32 s7, s7, s8
	s_add_i32 s9, s6, 1
	s_sub_i32 s8, s7, s5
	s_cmp_ge_u32 s7, s5
	s_cselect_b32 s6, s9, s6
	s_cselect_b32 s7, s8, s7
	s_add_i32 s8, s6, 1
	s_cmp_ge_u32 s7, s5
	s_cselect_b32 s5, s8, s6
	s_xor_b32 s5, s5, s4
	s_sub_i32 s4, s5, s4
	s_mul_i32 s5, s4, s26
	s_sub_i32 s5, s1, s5
	s_mul_hi_i32 s9, s0, s24
	s_mul_i32 s1, s0, s24
	s_lshl_b32 s8, s5, 6
	s_lshl_b32 s0, s4, 7
	s_and_saveexec_b64 s[4:5], s[2:3]
	s_cbranch_execz .LBB4_97
	v_or_b32_e32 v0, s8, v37
	v_cmp_gt_i32_e32 vcc, s25, v0
	v_mov_b32_e32 v1, 0
	s_waitcnt lgkmcnt(0)
	v_mov_b32_e32 v2, 0
	v_mov_b32_e32 v3, 0
	s_waitcnt vmcnt(4)
	v_mov_b32_e32 v4, 0
	v_mov_b32_e32 v5, 0
	v_mov_b32_e32 v6, 0
	v_mov_b32_e32 v7, 0
	s_waitcnt vmcnt(3)
	v_mov_b32_e32 v8, 0
	v_mov_b32_e32 v9, 0
	v_mov_b32_e32 v10, 0
	v_mov_b32_e32 v11, 0
	s_waitcnt vmcnt(2)
	v_mov_b32_e32 v12, 0
	v_mov_b32_e32 v13, 0
	v_mov_b32_e32 v14, 0
	v_mov_b32_e32 v15, 0
	v_mov_b32_e32 v16, 0
	v_mov_b32_e32 v17, 0
	v_mov_b32_e32 v18, 0
	v_mov_b32_e32 v19, 0
	v_mov_b32_e32 v20, 0
	v_mov_b32_e32 v21, 0
	v_mov_b32_e32 v22, 0
	v_mov_b32_e32 v23, 0
	v_mov_b32_e32 v25, 0
	v_mov_b32_e32 v27, 0
	v_mov_b32_e32 v37, 0
	v_mov_b32_e32 v38, 0
	v_mov_b32_e32 v39, 0
	v_mov_b32_e32 v40, 0
	v_mov_b32_e32 v41, 0
	v_mov_b32_e32 v42, 0
	v_mov_b32_e32 v43, 0
	s_and_saveexec_b64 s[6:7], vcc
	s_cbranch_execz .LBB4_96
	s_ashr_i32 s10, s25, 31
	s_mul_hi_u32 s11, s1, s25
	s_mul_i32 s10, s1, s10
	s_add_i32 s10, s11, s10
	s_mul_i32 s11, s9, s25
	s_add_i32 s11, s10, s11
	s_mul_i32 s10, s1, s25
	s_lshl_b64 s[10:11], s[10:11], 2
	s_add_u32 s10, s16, s10
	s_addc_u32 s11, s17, s11
	v_or_b32_e32 v27, s0, v36
	v_ashrrev_i32_e32 v1, 31, v0
	v_lshl_add_u64 v[36:37], v[0:1], 2, s[10:11]
	v_mad_i64_i32 v[0:1], s[10:11], v27, s25, 0
	v_lshl_add_u64 v[10:11], v[0:1], 2, v[36:37]
	v_or_b32_e32 v0, 1, v27
	v_mad_i64_i32 v[0:1], s[10:11], v0, s25, 0
	v_lshl_add_u64 v[12:13], v[0:1], 2, v[36:37]
	v_or_b32_e32 v0, 2, v27
	v_mad_i64_i32 v[0:1], s[10:11], v0, s25, 0
	v_lshl_add_u64 v[14:15], v[0:1], 2, v[36:37]
	v_or_b32_e32 v0, 3, v27
	v_mad_i64_i32 v[0:1], s[10:11], v0, s25, 0
	v_lshl_add_u64 v[16:17], v[0:1], 2, v[36:37]
	v_or_b32_e32 v0, 4, v27
	v_mad_i64_i32 v[0:1], s[10:11], v0, s25, 0
	v_lshl_add_u64 v[18:19], v[0:1], 2, v[36:37]
	v_or_b32_e32 v0, 5, v27
	v_mad_i64_i32 v[0:1], s[10:11], v0, s25, 0
	v_lshl_add_u64 v[20:21], v[0:1], 2, v[36:37]
	v_or_b32_e32 v0, 6, v27
	v_mad_i64_i32 v[0:1], s[10:11], v0, s25, 0
	v_lshl_add_u64 v[22:23], v[0:1], 2, v[36:37]
	v_or_b32_e32 v0, 7, v27
	v_mad_i64_i32 v[0:1], s[10:11], v0, s25, 0
	v_lshl_add_u64 v[38:39], v[0:1], 2, v[36:37]
	v_or_b32_e32 v0, 8, v27
	global_load_dword v1, v[10:11], off nt
	global_load_dword v2, v[12:13], off nt
	global_load_dword v3, v[14:15], off nt
	global_load_dword v4, v[16:17], off nt
	global_load_dword v5, v[18:19], off nt
	global_load_dword v6, v[20:21], off nt
	global_load_dword v7, v[22:23], off nt
	global_load_dword v8, v[38:39], off nt
	v_mad_i64_i32 v[10:11], s[10:11], v0, s25, 0
	v_or_b32_e32 v0, 9, v27
	v_lshl_add_u64 v[18:19], v[10:11], 2, v[36:37]
	v_mad_i64_i32 v[10:11], s[10:11], v0, s25, 0
	v_or_b32_e32 v0, 10, v27
	v_lshl_add_u64 v[20:21], v[10:11], 2, v[36:37]
	v_mad_i64_i32 v[10:11], s[10:11], v0, s25, 0
	v_or_b32_e32 v0, 11, v27
	v_lshl_add_u64 v[22:23], v[10:11], 2, v[36:37]
	v_mad_i64_i32 v[10:11], s[10:11], v0, s25, 0
	v_or_b32_e32 v0, 12, v27
	v_lshl_add_u64 v[38:39], v[10:11], 2, v[36:37]
	v_mad_i64_i32 v[10:11], s[10:11], v0, s25, 0
	v_or_b32_e32 v0, 13, v27
	v_lshl_add_u64 v[40:41], v[10:11], 2, v[36:37]
	v_mad_i64_i32 v[10:11], s[10:11], v0, s25, 0
	v_or_b32_e32 v0, 14, v27
	v_lshl_add_u64 v[42:43], v[10:11], 2, v[36:37]
	v_mad_i64_i32 v[10:11], s[10:11], v0, s25, 0
	v_or_b32_e32 v0, 15, v27
	v_lshl_add_u64 v[44:45], v[10:11], 2, v[36:37]
	v_mad_i64_i32 v[10:11], s[10:11], v0, s25, 0
	v_or_b32_e32 v0, 16, v27
	v_lshl_add_u64 v[46:47], v[10:11], 2, v[36:37]
	global_load_dword v9, v[18:19], off nt
	global_load_dword v10, v[20:21], off nt
	global_load_dword v11, v[22:23], off nt
	global_load_dword v12, v[38:39], off nt
	global_load_dword v13, v[40:41], off nt
	global_load_dword v14, v[42:43], off nt
	global_load_dword v15, v[44:45], off nt
	global_load_dword v16, v[46:47], off nt
	v_mad_i64_i32 v[18:19], s[10:11], v0, s25, 0
	v_or_b32_e32 v0, 17, v27
	v_lshl_add_u64 v[38:39], v[18:19], 2, v[36:37]
	v_mad_i64_i32 v[18:19], s[10:11], v0, s25, 0
	v_or_b32_e32 v0, 18, v27
	v_lshl_add_u64 v[40:41], v[18:19], 2, v[36:37]
	v_mad_i64_i32 v[18:19], s[10:11], v0, s25, 0
	v_or_b32_e32 v0, 19, v27
	v_lshl_add_u64 v[42:43], v[18:19], 2, v[36:37]
	v_mad_i64_i32 v[18:19], s[10:11], v0, s25, 0
	v_or_b32_e32 v0, 20, v27
	v_lshl_add_u64 v[44:45], v[18:19], 2, v[36:37]
	v_mad_i64_i32 v[18:19], s[10:11], v0, s25, 0
	v_or_b32_e32 v0, 21, v27
	v_lshl_add_u64 v[46:47], v[18:19], 2, v[36:37]
	v_mad_i64_i32 v[18:19], s[10:11], v0, s25, 0
	v_or_b32_e32 v0, 22, v27
	v_lshl_add_u64 v[48:49], v[18:19], 2, v[36:37]
	v_mad_i64_i32 v[18:19], s[10:11], v0, s25, 0
	v_or_b32_e32 v0, 23, v27
	v_lshl_add_u64 v[50:51], v[18:19], 2, v[36:37]
	v_mad_i64_i32 v[18:19], s[10:11], v0, s25, 0
	v_or_b32_e32 v0, 24, v27
	v_lshl_add_u64 v[52:53], v[18:19], 2, v[36:37]
	global_load_dword v17, v[38:39], off nt
	global_load_dword v18, v[40:41], off nt
	global_load_dword v19, v[42:43], off nt
	global_load_dword v20, v[44:45], off nt
	global_load_dword v21, v[46:47], off nt
	global_load_dword v22, v[48:49], off nt
	global_load_dword v23, v[50:51], off nt
	global_load_dword v25, v[52:53], off nt
	v_mad_i64_i32 v[38:39], s[10:11], v0, s25, 0
	v_or_b32_e32 v0, 25, v27
	v_lshl_add_u64 v[44:45], v[38:39], 2, v[36:37]
	v_mad_i64_i32 v[38:39], s[10:11], v0, s25, 0
	v_or_b32_e32 v0, 26, v27
	v_lshl_add_u64 v[46:47], v[38:39], 2, v[36:37]
	v_mad_i64_i32 v[38:39], s[10:11], v0, s25, 0
	v_or_b32_e32 v0, 27, v27
	v_lshl_add_u64 v[48:49], v[38:39], 2, v[36:37]
	v_mad_i64_i32 v[38:39], s[10:11], v0, s25, 0
	v_or_b32_e32 v0, 28, v27
	v_lshl_add_u64 v[50:51], v[38:39], 2, v[36:37]
	v_mad_i64_i32 v[38:39], s[10:11], v0, s25, 0
	v_or_b32_e32 v0, 29, v27
	v_lshl_add_u64 v[52:53], v[38:39], 2, v[36:37]
	v_mad_i64_i32 v[38:39], s[10:11], v0, s25, 0
	v_or_b32_e32 v0, 30, v27
	v_lshl_add_u64 v[54:55], v[38:39], 2, v[36:37]
	v_mad_i64_i32 v[38:39], s[10:11], v0, s25, 0
	v_or_b32_e32 v0, 31, v27
	v_lshl_add_u64 v[56:57], v[38:39], 2, v[36:37]
	v_mad_i64_i32 v[38:39], s[10:11], v0, s25, 0
	v_lshl_add_u64 v[58:59], v[38:39], 2, v[36:37]
	global_load_dword v27, v[44:45], off nt
	global_load_dword v37, v[46:47], off nt
	global_load_dword v38, v[48:49], off nt
	global_load_dword v39, v[50:51], off nt
	global_load_dword v40, v[52:53], off nt
	global_load_dword v41, v[54:55], off nt
	global_load_dword v42, v[56:57], off nt
	global_load_dword v43, v[58:59], off nt

.LBB11_27:
	s_andn2_saveexec_b64 s[0:1], s[0:1]
	s_cbranch_execz .LBB11_29
	v_add_f32_e32 v21, 0, v21
	global_store_dwordx4 v[22:23], v[18:21], off nt

.LBB11_37:
	s_andn2_saveexec_b64 s[0:1], s[0:1]
	s_cbranch_execz .LBB11_39
	v_add_f32_e32 v17, 0, v17
	global_store_dwordx4 v[22:23], v[14:17], off offset:64 nt

.LBB11_47:
	s_andn2_saveexec_b64 s[0:1], s[0:1]
	s_cbranch_execz .LBB11_49
	v_add_f32_e32 v13, 0, v13
	global_store_dwordx4 v[22:23], v[10:13], off offset:128 nt

.LBB11_57:
	s_andn2_saveexec_b64 s[0:1], s[0:1]
	s_cbranch_execz .LBB11_59
	v_add_f32_e32 v9, 0, v9
	global_store_dwordx4 v[22:23], v[6:9], off offset:192 nt

.LBB11_67:
	s_andn2_saveexec_b64 s[0:1], s[0:1]
	s_cbranch_execz .LBB11_69
	v_add_f32_e32 v5, 0, v5
	global_store_dwordx4 v[22:23], v[2:5], off offset:256 nt

.LBB11_93:
	s_andn2_saveexec_b64 s[0:1], s[2:3]
	s_cbranch_execz .LBB11_95
	s_waitcnt lgkmcnt(0)
	global_store_dwordx4 v[0:1], v[66:69], off nt

.LBB11_103:
	s_or_saveexec_b64 s[0:1], s[2:3]
	v_mul_u32_u24_e32 v70, 0x410, v71
	s_xor_b64 exec, exec, s[0:1]
	s_cbranch_execz .LBB11_105
	s_waitcnt lgkmcnt(0)
	global_store_dwordx4 v[0:1], v[66:69], off nt

.LBB11_243:
	s_or_saveexec_b64 s[0:1], s[2:3]
	v_mul_i32_i24_e32 v87, 0x410, v137
	v_mul_u32_u24_e32 v86, 0x4100, v149
	s_xor_b64 exec, exec, s[0:1]
	s_cbranch_execz .LBB11_245
	s_waitcnt lgkmcnt(0)
	global_store_dwordx4 v[0:1], v[66:69], off nt

.LBB11_253:
	s_andn2_saveexec_b64 s[0:1], s[2:3]
	s_cbranch_execz .LBB11_255
	s_waitcnt lgkmcnt(0)
	global_store_dwordx4 v[4:5], v[0:3], off nt

.LBB11_403:
	s_andn2_saveexec_b64 s[0:1], s[0:1]
	s_cbranch_execz .LBB11_405
	s_waitcnt lgkmcnt(0)
	global_store_dwordx4 v[4:5], v[0:3], off nt
